# v_P with 8-MFMA groups in A-stationary order (X,B0..B3 then Y,B3..B0)
# baseline (speedup 1.0000x reference)
.LBB0_216:
	v_add_u32_e32 v130, s88, v196
	v_add_u32_e32 v134, s89, v196
	ds_read_b128 v[158:161], v130
	ds_read_b128 v[150:153], v130 offset:1024
	ds_read_b128 v[154:157], v130 offset:2048
	ds_read_b128 v[146:149], v130 offset:3072
	ds_read_b128 v[142:145], v134
	ds_read_b128 v[130:133], v134 offset:1024
	ds_read_b128 v[138:141], v134 offset:2048
	ds_read_b128 v[134:137], v134 offset:3072
	s_add_u32 s25, s50, 0xfff80080
	s_addc_u32 s56, s51, -1
	s_and_b64 s[18:19], s[18:19], exec
	s_cselect_b32 s59, s31, s56
	s_cselect_b32 s58, s4, s25
	s_cselect_b32 s57, s5, s64
	s_cselect_b32 s56, s29, s92
	s_add_i32 m0, s39, 0xc000
	ds_read_b128 v[186:189], v198
	ds_read_b128 v[190:193], v198 offset:1024
	ds_read_b128 v[200:203], v198 offset:2048
	ds_read_b128 v[204:207], v198 offset:3072
	ds_read_b128 v[208:211], v198 offset:4096
	ds_read_b128 v[212:215], v198 offset:5120
	ds_read_b128 v[216:219], v198 offset:6144
	ds_read_b128 v[220:223], v198 offset:7168
	global_load_lds_dwordx4 v170, s[50:51]
	s_add_i32 m0, s39, 0xe000
	s_nop 0
	global_load_lds_dwordx4 v172, s[50:51]
	s_waitcnt vmcnt(8)
	s_waitcnt lgkmcnt(0)
	s_barrier
	s_setprio 1
	s_waitcnt lgkmcnt(0)
	v_mfma_i32_16x16x64_i8 v[126:129], v[158:161], v[186:189], v[126:129]
	v_mfma_i32_16x16x64_i8 v[110:113], v[158:161], v[200:203], v[110:113]
	v_mfma_i32_16x16x64_i8 v[94:97], v[158:161], v[208:211], v[94:97]
	v_mfma_i32_16x16x64_i8 v[78:81], v[158:161], v[216:219], v[78:81]
	v_mfma_i32_16x16x64_i8 v[74:77], v[154:157], v[216:219], v[74:77]
	v_mfma_i32_16x16x64_i8 v[90:93], v[154:157], v[208:211], v[90:93]
	v_mfma_i32_16x16x64_i8 v[106:109], v[154:157], v[200:203], v[106:109]
	v_mfma_i32_16x16x64_i8 v[122:125], v[154:157], v[186:189], v[122:125]
	s_nop 0
	v_mfma_i32_16x16x64_i8 v[126:129], v[150:153], v[190:193], v[126:129]
	v_mfma_i32_16x16x64_i8 v[110:113], v[150:153], v[204:207], v[110:113]
	v_mfma_i32_16x16x64_i8 v[94:97], v[150:153], v[212:215], v[94:97]
	v_mfma_i32_16x16x64_i8 v[78:81], v[150:153], v[220:223], v[78:81]
	v_mfma_i32_16x16x64_i8 v[74:77], v[146:149], v[220:223], v[74:77]
	v_mfma_i32_16x16x64_i8 v[90:93], v[146:149], v[212:215], v[90:93]
	v_mfma_i32_16x16x64_i8 v[106:109], v[146:149], v[204:207], v[106:109]
	v_mfma_i32_16x16x64_i8 v[122:125], v[146:149], v[190:193], v[122:125]
	s_setprio 0
	s_setprio 1
	v_mfma_i32_16x16x64_i8 v[118:121], v[142:145], v[186:189], v[118:121]
	v_mfma_i32_16x16x64_i8 v[102:105], v[142:145], v[200:203], v[102:105]
	v_mfma_i32_16x16x64_i8 v[86:89], v[142:145], v[208:211], v[86:89]
	v_mfma_i32_16x16x64_i8 v[70:73], v[142:145], v[216:219], v[70:73]
	v_mfma_i32_16x16x64_i8 v[66:69], v[138:141], v[216:219], v[66:69]
	v_mfma_i32_16x16x64_i8 v[82:85], v[138:141], v[208:211], v[82:85]
	v_mfma_i32_16x16x64_i8 v[98:101], v[138:141], v[200:203], v[98:101]
	v_mfma_i32_16x16x64_i8 v[114:117], v[138:141], v[186:189], v[114:117]
	s_nop 0
	v_mfma_i32_16x16x64_i8 v[118:121], v[130:133], v[190:193], v[118:121]
	v_mfma_i32_16x16x64_i8 v[102:105], v[130:133], v[204:207], v[102:105]
	v_mfma_i32_16x16x64_i8 v[86:89], v[130:133], v[212:215], v[86:89]
	v_mfma_i32_16x16x64_i8 v[70:73], v[130:133], v[220:223], v[70:73]
	v_mfma_i32_16x16x64_i8 v[66:69], v[134:137], v[220:223], v[66:69]
	v_mfma_i32_16x16x64_i8 v[82:85], v[134:137], v[212:215], v[82:85]
	v_mfma_i32_16x16x64_i8 v[98:101], v[134:137], v[204:207], v[98:101]
	v_mfma_i32_16x16x64_i8 v[114:117], v[134:137], v[190:193], v[114:117]
	s_setprio 0
	s_barrier
	s_add_i32 s18, s88, s7
	s_mov_b32 m0, s18
	ds_read_b128 v[200:203], v198 offset:16384
	ds_read_b128 v[204:207], v198 offset:17408
	ds_read_b128 v[208:211], v198 offset:18432
	ds_read_b128 v[212:215], v198 offset:19456
	ds_read_b128 v[216:219], v198 offset:20480
	ds_read_b128 v[220:223], v198 offset:21504
	ds_read_b128 v[224:227], v198 offset:22528
	ds_read_b128 v[228:231], v198 offset:23552
	global_load_lds_dwordx4 v164, s[56:57]
	s_add_i32 m0, s18, 0x2000
	s_add_u32 s18, s56, 0x80000
	s_addc_u32 s19, s57, 0
	s_add_i32 s25, s89, s7
	global_load_lds_dwordx4 v168, s[56:57]
	s_mov_b32 m0, s25
	s_nop 0
	global_load_lds_dwordx4 v164, s[18:19]
	s_add_i32 m0, s25, 0x2000
	s_nop 0
	global_load_lds_dwordx4 v168, s[18:19]
	s_mov_b32 m0, s39
	s_nop 0
	global_load_lds_dwordx4 v162, s[58:59]
	s_mov_b32 m0, s43
	s_nop 0
	global_load_lds_dwordx4 v166, s[58:59]
	s_waitcnt vmcnt(8)
	s_waitcnt lgkmcnt(0)
	s_barrier
	s_setprio 1
	s_waitcnt lgkmcnt(0)
	v_mfma_i32_16x16x64_i8 v[62:65], v[158:161], v[200:203], v[62:65]
	v_mfma_i32_16x16x64_i8 v[46:49], v[158:161], v[208:211], v[46:49]
	v_mfma_i32_16x16x64_i8 v[30:33], v[158:161], v[216:219], v[30:33]
	v_mfma_i32_16x16x64_i8 v[14:17], v[158:161], v[224:227], v[14:17]
	v_mfma_i32_16x16x64_i8 v[10:13], v[154:157], v[224:227], v[10:13]
	v_mfma_i32_16x16x64_i8 v[26:29], v[154:157], v[216:219], v[26:29]
	v_mfma_i32_16x16x64_i8 v[42:45], v[154:157], v[208:211], v[42:45]
	v_mfma_i32_16x16x64_i8 v[58:61], v[154:157], v[200:203], v[58:61]
	s_nop 0
	v_mfma_i32_16x16x64_i8 v[62:65], v[150:153], v[204:207], v[62:65]
	v_mfma_i32_16x16x64_i8 v[46:49], v[150:153], v[212:215], v[46:49]
	v_mfma_i32_16x16x64_i8 v[30:33], v[150:153], v[220:223], v[30:33]
	v_mfma_i32_16x16x64_i8 v[14:17], v[150:153], v[228:231], v[14:17]
	v_mfma_i32_16x16x64_i8 v[10:13], v[146:149], v[228:231], v[10:13]
	v_mfma_i32_16x16x64_i8 v[26:29], v[146:149], v[220:223], v[26:29]
	v_mfma_i32_16x16x64_i8 v[42:45], v[146:149], v[212:215], v[42:45]
	v_mfma_i32_16x16x64_i8 v[58:61], v[146:149], v[204:207], v[58:61]
	s_setprio 0
	s_setprio 1
	v_mfma_i32_16x16x64_i8 v[54:57], v[142:145], v[200:203], v[54:57]
	v_mfma_i32_16x16x64_i8 v[38:41], v[142:145], v[208:211], v[38:41]
	v_mfma_i32_16x16x64_i8 v[22:25], v[142:145], v[216:219], v[22:25]
	v_mfma_i32_16x16x64_i8 v[6:9], v[142:145], v[224:227], v[6:9]
	v_mfma_i32_16x16x64_i8 v[2:5], v[138:141], v[224:227], v[2:5]
	v_mfma_i32_16x16x64_i8 v[18:21], v[138:141], v[216:219], v[18:21]
	v_mfma_i32_16x16x64_i8 v[34:37], v[138:141], v[208:211], v[34:37]
	v_mfma_i32_16x16x64_i8 v[50:53], v[138:141], v[200:203], v[50:53]
	s_nop 0
	v_mfma_i32_16x16x64_i8 v[54:57], v[130:133], v[204:207], v[54:57]
	v_mfma_i32_16x16x64_i8 v[38:41], v[130:133], v[212:215], v[38:41]
	v_mfma_i32_16x16x64_i8 v[22:25], v[130:133], v[220:223], v[22:25]
	v_mfma_i32_16x16x64_i8 v[6:9], v[130:133], v[228:231], v[6:9]
	v_mfma_i32_16x16x64_i8 v[2:5], v[134:137], v[228:231], v[2:5]
	v_mfma_i32_16x16x64_i8 v[18:21], v[134:137], v[220:223], v[18:21]
	v_mfma_i32_16x16x64_i8 v[34:37], v[134:137], v[212:215], v[34:37]
	v_mfma_i32_16x16x64_i8 v[50:53], v[134:137], v[204:207], v[50:53]
	s_setprio 0
	s_barrier
	s_add_i32 s25, 0, 0x18000
	s_add_i32 vcc_lo, 0, 0x1c000
	v_add_u32_e32 v142, s25, v196
	v_add_u32_e32 v158, vcc_lo, v196
	ds_read_b128 v[130:133], v142
	ds_read_b128 v[134:137], v142 offset:1024
	ds_read_b128 v[138:141], v142 offset:2048
	ds_read_b128 v[142:145], v142 offset:3072
	ds_read_b128 v[146:149], v158
	ds_read_b128 v[150:153], v158 offset:1024
	ds_read_b128 v[154:157], v158 offset:2048
	ds_read_b128 v[158:161], v158 offset:3072
	s_add_u32 s18, s58, 0x80000
	s_addc_u32 s19, s59, 0
	s_mov_b32 m0, s61
	ds_read_b128 v[200:203], v198 offset:32768
	ds_read_b128 v[204:207], v198 offset:33792
	ds_read_b128 v[208:211], v198 offset:34816
	ds_read_b128 v[212:215], v198 offset:35840
	ds_read_b128 v[216:219], v198 offset:36864
	ds_read_b128 v[220:223], v198 offset:37888
	ds_read_b128 v[224:227], v198 offset:38912
	ds_read_b128 v[228:231], v198 offset:39936
	global_load_lds_dwordx4 v162, s[18:19]
	s_mov_b32 m0, s62
	s_nop 0
	global_load_lds_dwordx4 v166, s[18:19]
	s_waitcnt vmcnt(8)
	s_waitcnt lgkmcnt(0)
	s_barrier
	s_setprio 1
	s_waitcnt lgkmcnt(0)
	v_mfma_i32_16x16x64_i8 v[126:129], v[130:133], v[200:203], v[126:129]
	v_mfma_i32_16x16x64_i8 v[110:113], v[130:133], v[208:211], v[110:113]
	v_mfma_i32_16x16x64_i8 v[94:97], v[130:133], v[216:219], v[94:97]
	v_mfma_i32_16x16x64_i8 v[78:81], v[130:133], v[224:227], v[78:81]
	v_mfma_i32_16x16x64_i8 v[74:77], v[138:141], v[224:227], v[74:77]
	v_mfma_i32_16x16x64_i8 v[90:93], v[138:141], v[216:219], v[90:93]
	v_mfma_i32_16x16x64_i8 v[106:109], v[138:141], v[208:211], v[106:109]
	v_mfma_i32_16x16x64_i8 v[122:125], v[138:141], v[200:203], v[122:125]
	s_nop 0
	v_mfma_i32_16x16x64_i8 v[126:129], v[134:137], v[204:207], v[126:129]
	v_mfma_i32_16x16x64_i8 v[110:113], v[134:137], v[212:215], v[110:113]
	v_mfma_i32_16x16x64_i8 v[94:97], v[134:137], v[220:223], v[94:97]
	v_mfma_i32_16x16x64_i8 v[78:81], v[134:137], v[228:231], v[78:81]
	v_mfma_i32_16x16x64_i8 v[74:77], v[142:145], v[228:231], v[74:77]
	v_mfma_i32_16x16x64_i8 v[90:93], v[142:145], v[220:223], v[90:93]
	v_mfma_i32_16x16x64_i8 v[106:109], v[142:145], v[212:215], v[106:109]
	v_mfma_i32_16x16x64_i8 v[122:125], v[142:145], v[204:207], v[122:125]
	s_setprio 0
	s_setprio 1
	v_mfma_i32_16x16x64_i8 v[118:121], v[146:149], v[200:203], v[118:121]
	v_mfma_i32_16x16x64_i8 v[102:105], v[146:149], v[208:211], v[102:105]
	v_mfma_i32_16x16x64_i8 v[86:89], v[146:149], v[216:219], v[86:89]
	v_mfma_i32_16x16x64_i8 v[70:73], v[146:149], v[224:227], v[70:73]
	v_mfma_i32_16x16x64_i8 v[66:69], v[154:157], v[224:227], v[66:69]
	v_mfma_i32_16x16x64_i8 v[82:85], v[154:157], v[216:219], v[82:85]
	v_mfma_i32_16x16x64_i8 v[98:101], v[154:157], v[208:211], v[98:101]
	v_mfma_i32_16x16x64_i8 v[114:117], v[154:157], v[200:203], v[114:117]
	s_nop 0
	v_mfma_i32_16x16x64_i8 v[118:121], v[150:153], v[204:207], v[118:121]
	v_mfma_i32_16x16x64_i8 v[102:105], v[150:153], v[212:215], v[102:105]
	v_mfma_i32_16x16x64_i8 v[86:89], v[150:153], v[220:223], v[86:89]
	v_mfma_i32_16x16x64_i8 v[70:73], v[150:153], v[228:231], v[70:73]
	v_mfma_i32_16x16x64_i8 v[66:69], v[158:161], v[228:231], v[66:69]
	v_mfma_i32_16x16x64_i8 v[82:85], v[158:161], v[220:223], v[82:85]
	v_mfma_i32_16x16x64_i8 v[98:101], v[158:161], v[212:215], v[98:101]
	v_mfma_i32_16x16x64_i8 v[114:117], v[158:161], v[204:207], v[114:117]
	s_setprio 0
	s_barrier
	s_add_i32 s18, s25, s7
	s_mov_b32 m0, s18
	s_add_u32 s98, s56, 0x80
	s_addc_u32 s99, s57, 0
	s_add_u32 s100, s58, 0x80
	s_addc_u32 s101, s59, 0
	ds_read_b128 v[200:203], v198 offset:49152
	ds_read_b128 v[204:207], v198 offset:50176
	ds_read_b128 v[208:211], v198 offset:51200
	ds_read_b128 v[212:215], v198 offset:52224
	ds_read_b128 v[216:219], v198 offset:53248
	ds_read_b128 v[220:223], v198 offset:54272
	ds_read_b128 v[224:227], v198 offset:55296
	ds_read_b128 v[228:231], v198 offset:56320
	global_load_lds_dwordx4 v164, s[98:99]
	s_add_i32 m0, s18, 0x2000
	s_add_u32 s18, s56, 0x80080
	s_addc_u32 s19, s57, 0
	s_add_i32 s25, vcc_lo, s7
	global_load_lds_dwordx4 v168, s[98:99]
	s_mov_b32 m0, s25
	s_nop 0
	global_load_lds_dwordx4 v164, s[18:19]
	s_add_i32 m0, s25, 0x2000
	s_nop 0
	global_load_lds_dwordx4 v168, s[18:19]
	s_mov_b32 m0, s67
	s_nop 0
	global_load_lds_dwordx4 v162, s[100:101]
	s_mov_b32 m0, s68
	s_nop 0
	global_load_lds_dwordx4 v166, s[100:101]
	s_waitcnt vmcnt(8)
	s_waitcnt lgkmcnt(0)
	s_barrier
	s_setprio 1
	s_waitcnt lgkmcnt(0)
	v_mfma_i32_16x16x64_i8 v[62:65], v[130:133], v[200:203], v[62:65]
	v_mfma_i32_16x16x64_i8 v[46:49], v[130:133], v[208:211], v[46:49]
	v_mfma_i32_16x16x64_i8 v[30:33], v[130:133], v[216:219], v[30:33]
	v_mfma_i32_16x16x64_i8 v[14:17], v[130:133], v[224:227], v[14:17]
	v_mfma_i32_16x16x64_i8 v[10:13], v[138:141], v[224:227], v[10:13]
	v_mfma_i32_16x16x64_i8 v[26:29], v[138:141], v[216:219], v[26:29]
	v_mfma_i32_16x16x64_i8 v[42:45], v[138:141], v[208:211], v[42:45]
	v_mfma_i32_16x16x64_i8 v[58:61], v[138:141], v[200:203], v[58:61]
	s_nop 0
	v_mfma_i32_16x16x64_i8 v[62:65], v[134:137], v[204:207], v[62:65]
	v_mfma_i32_16x16x64_i8 v[46:49], v[134:137], v[212:215], v[46:49]
	v_mfma_i32_16x16x64_i8 v[30:33], v[134:137], v[220:223], v[30:33]
	v_mfma_i32_16x16x64_i8 v[14:17], v[134:137], v[228:231], v[14:17]
	v_mfma_i32_16x16x64_i8 v[10:13], v[142:145], v[228:231], v[10:13]
	v_mfma_i32_16x16x64_i8 v[26:29], v[142:145], v[220:223], v[26:29]
	v_mfma_i32_16x16x64_i8 v[42:45], v[142:145], v[212:215], v[42:45]
	v_mfma_i32_16x16x64_i8 v[58:61], v[142:145], v[204:207], v[58:61]
	s_setprio 0
	s_setprio 1
	v_mfma_i32_16x16x64_i8 v[54:57], v[146:149], v[200:203], v[54:57]
	v_mfma_i32_16x16x64_i8 v[38:41], v[146:149], v[208:211], v[38:41]
	v_mfma_i32_16x16x64_i8 v[22:25], v[146:149], v[216:219], v[22:25]
	v_mfma_i32_16x16x64_i8 v[6:9], v[146:149], v[224:227], v[6:9]
	v_mfma_i32_16x16x64_i8 v[2:5], v[154:157], v[224:227], v[2:5]
	v_mfma_i32_16x16x64_i8 v[18:21], v[154:157], v[216:219], v[18:21]
	v_mfma_i32_16x16x64_i8 v[34:37], v[154:157], v[208:211], v[34:37]
	v_mfma_i32_16x16x64_i8 v[50:53], v[154:157], v[200:203], v[50:53]
	s_nop 0
	v_mfma_i32_16x16x64_i8 v[54:57], v[150:153], v[204:207], v[54:57]
	v_mfma_i32_16x16x64_i8 v[38:41], v[150:153], v[212:215], v[38:41]
	v_mfma_i32_16x16x64_i8 v[22:25], v[150:153], v[220:223], v[22:25]
	v_mfma_i32_16x16x64_i8 v[6:9], v[150:153], v[228:231], v[6:9]
	v_mfma_i32_16x16x64_i8 v[2:5], v[158:161], v[228:231], v[2:5]
	v_mfma_i32_16x16x64_i8 v[18:21], v[158:161], v[220:223], v[18:21]
	v_mfma_i32_16x16x64_i8 v[34:37], v[158:161], v[212:215], v[34:37]
	v_mfma_i32_16x16x64_i8 v[50:53], v[158:161], v[204:207], v[50:53]
	s_setprio 0
	s_barrier
	s_add_i32 s65, s65, 2
	s_add_u32 s50, s50, 0x100
	s_addc_u32 s51, s51, 0
	s_add_u32 s92, s92, 0x100
	s_addc_u32 s64, s64, 0
	s_cmp_gt_u32 s65, 29
	s_cbranch_scc1 .LBB0_219

.LBB0_318:
	ds_read_b128 v[26:29], v185
	ds_read_b128 v[30:33], v185 offset:1024
	ds_read_b128 v[18:21], v185 offset:2048
	ds_read_b128 v[22:25], v185 offset:3072
	ds_read_b128 v[10:13], v186
	ds_read_b128 v[14:17], v186 offset:1024
	ds_read_b128 v[2:5], v186 offset:2048
	ds_read_b128 v[6:9], v186 offset:3072
	s_add_u32 s24, s26, 0xffea8080
	s_addc_u32 s25, s27, -1
	s_cmpk_eq_i32 s58, 0x52
	s_cselect_b32 s31, s5, s25
	s_cselect_b32 s30, s4, s24
	s_cselect_b32 s29, s21, s51
	s_cselect_b32 s28, s20, s50
	v_lshl_add_u64 v[212:213], s[26:27], 0, v[166:167]
	s_add_i32 m0, s7, 0xc000
	ds_read_b128 v[174:177], v187
	ds_read_b128 v[178:181], v187 offset:1024
	ds_read_b128 v[188:191], v187 offset:2048
	ds_read_b128 v[192:195], v187 offset:3072
	ds_read_b128 v[196:199], v187 offset:4096
	ds_read_b128 v[200:203], v187 offset:5120
	ds_read_b128 v[204:207], v187 offset:6144
	ds_read_b128 v[208:211], v187 offset:7168
	global_load_lds_dwordx4 v[212:213], off
	v_lshl_add_u64 v[212:213], s[26:27], 0, v[168:169]
	s_add_i32 m0, s7, 0xe000
	s_nop 0
	global_load_lds_dwordx4 v[212:213], off
	s_waitcnt vmcnt(8)
	s_waitcnt lgkmcnt(0)
	s_barrier
	s_setprio 1
	s_waitcnt lgkmcnt(0)
	v_mfma_scale_f32_16x16x128_f8f6f4 v[158:161], v[26:33], v[174:181], v[158:161], v1, v1 op_sel_hi:[0,0,0]
	v_mfma_scale_f32_16x16x128_f8f6f4 v[142:145], v[26:33], v[188:195], v[142:145], v1, v1 op_sel_hi:[0,0,0]
	v_mfma_scale_f32_16x16x128_f8f6f4 v[126:129], v[26:33], v[196:203], v[126:129], v1, v1 op_sel_hi:[0,0,0]
	v_mfma_scale_f32_16x16x128_f8f6f4 v[110:113], v[26:33], v[204:211], v[110:113], v1, v1 op_sel_hi:[0,0,0]
	v_mfma_scale_f32_16x16x128_f8f6f4 v[106:109], v[18:25], v[204:211], v[106:109], v1, v1 op_sel_hi:[0,0,0]
	v_mfma_scale_f32_16x16x128_f8f6f4 v[122:125], v[18:25], v[196:203], v[122:125], v1, v1 op_sel_hi:[0,0,0]
	v_mfma_scale_f32_16x16x128_f8f6f4 v[138:141], v[18:25], v[188:195], v[138:141], v1, v1 op_sel_hi:[0,0,0]
	v_mfma_scale_f32_16x16x128_f8f6f4 v[154:157], v[18:25], v[174:181], v[154:157], v1, v1 op_sel_hi:[0,0,0]
	s_setprio 0
	s_setprio 1
	v_mfma_scale_f32_16x16x128_f8f6f4 v[150:153], v[10:17], v[174:181], v[150:153], v1, v1 op_sel_hi:[0,0,0]
	v_mfma_scale_f32_16x16x128_f8f6f4 v[134:137], v[10:17], v[188:195], v[134:137], v1, v1 op_sel_hi:[0,0,0]
	v_mfma_scale_f32_16x16x128_f8f6f4 v[118:121], v[10:17], v[196:203], v[118:121], v1, v1 op_sel_hi:[0,0,0]
	v_mfma_scale_f32_16x16x128_f8f6f4 v[102:105], v[10:17], v[204:211], v[102:105], v1, v1 op_sel_hi:[0,0,0]
	v_mfma_scale_f32_16x16x128_f8f6f4 v[98:101], v[2:9], v[204:211], v[98:101], v1, v1 op_sel_hi:[0,0,0]
	v_mfma_scale_f32_16x16x128_f8f6f4 v[114:117], v[2:9], v[196:203], v[114:117], v1, v1 op_sel_hi:[0,0,0]
	v_mfma_scale_f32_16x16x128_f8f6f4 v[130:133], v[2:9], v[188:195], v[130:133], v1, v1 op_sel_hi:[0,0,0]
	v_mfma_scale_f32_16x16x128_f8f6f4 v[146:149], v[2:9], v[174:181], v[146:149], v1, v1 op_sel_hi:[0,0,0]
	s_setprio 0
	s_barrier
	s_add_i32 s24, s42, s3
	v_lshl_add_u64 v[174:175], s[28:29], 0, v[164:165]
	s_mov_b32 m0, s24
	ds_read_b128 v[188:191], v187 offset:16384
	ds_read_b128 v[192:195], v187 offset:17408
	ds_read_b128 v[196:199], v187 offset:18432
	ds_read_b128 v[200:203], v187 offset:19456
	ds_read_b128 v[204:207], v187 offset:20480
	ds_read_b128 v[208:211], v187 offset:21504
	ds_read_b128 v[212:215], v187 offset:22528
	ds_read_b128 v[216:219], v187 offset:23552
	global_load_lds_dwordx4 v[174:175], off
	s_add_i32 m0, s24, 0x2000
	s_add_u32 s24, s28, 0x158000
	v_lshl_add_u64 v[176:177], s[28:29], 0, v[162:163]
	s_addc_u32 s25, s29, 0
	s_add_i32 s59, s43, s3
	global_load_lds_dwordx4 v[176:177], off
	v_lshl_add_u64 v[178:179], s[24:25], 0, v[164:165]
	s_mov_b32 m0, s59
	v_lshl_add_u64 v[180:181], s[30:31], 0, v[162:163]
	global_load_lds_dwordx4 v[178:179], off
	v_lshl_add_u64 v[178:179], s[24:25], 0, v[162:163]
	s_add_i32 m0, s59, 0x2000
	s_nop 0
	global_load_lds_dwordx4 v[178:179], off
	v_lshl_add_u64 v[178:179], s[30:31], 0, v[164:165]
	s_mov_b32 m0, s7
	s_nop 0
	global_load_lds_dwordx4 v[178:179], off
	s_mov_b32 m0, s17
	s_nop 0
	global_load_lds_dwordx4 v[180:181], off
	s_waitcnt vmcnt(8)
	s_waitcnt lgkmcnt(0)
	s_barrier
	s_setprio 1
	s_waitcnt lgkmcnt(0)
	v_mfma_scale_f32_16x16x128_f8f6f4 v[94:97], v[26:33], v[188:195], v[94:97], v1, v1 op_sel_hi:[0,0,0]
	v_mfma_scale_f32_16x16x128_f8f6f4 v[78:81], v[26:33], v[196:203], v[78:81], v1, v1 op_sel_hi:[0,0,0]
	v_mfma_scale_f32_16x16x128_f8f6f4 v[62:65], v[26:33], v[204:211], v[62:65], v1, v1 op_sel_hi:[0,0,0]
	v_mfma_scale_f32_16x16x128_f8f6f4 v[46:49], v[26:33], v[212:219], v[46:49], v1, v1 op_sel_hi:[0,0,0]
	v_mfma_scale_f32_16x16x128_f8f6f4 v[42:45], v[18:25], v[212:219], v[42:45], v1, v1 op_sel_hi:[0,0,0]
	v_mfma_scale_f32_16x16x128_f8f6f4 v[58:61], v[18:25], v[204:211], v[58:61], v1, v1 op_sel_hi:[0,0,0]
	v_mfma_scale_f32_16x16x128_f8f6f4 v[74:77], v[18:25], v[196:203], v[74:77], v1, v1 op_sel_hi:[0,0,0]
	v_mfma_scale_f32_16x16x128_f8f6f4 v[90:93], v[18:25], v[188:195], v[90:93], v1, v1 op_sel_hi:[0,0,0]
	s_setprio 0
	s_setprio 1
	v_mfma_scale_f32_16x16x128_f8f6f4 v[86:89], v[10:17], v[188:195], v[86:89], v1, v1 op_sel_hi:[0,0,0]
	v_mfma_scale_f32_16x16x128_f8f6f4 v[70:73], v[10:17], v[196:203], v[70:73], v1, v1 op_sel_hi:[0,0,0]
	v_mfma_scale_f32_16x16x128_f8f6f4 v[54:57], v[10:17], v[204:211], v[54:57], v1, v1 op_sel_hi:[0,0,0]
	v_mfma_scale_f32_16x16x128_f8f6f4 v[38:41], v[10:17], v[212:219], v[38:41], v1, v1 op_sel_hi:[0,0,0]
	v_mfma_scale_f32_16x16x128_f8f6f4 v[34:37], v[2:9], v[212:219], v[34:37], v1, v1 op_sel_hi:[0,0,0]
	v_mfma_scale_f32_16x16x128_f8f6f4 v[50:53], v[2:9], v[204:211], v[50:53], v1, v1 op_sel_hi:[0,0,0]
	v_mfma_scale_f32_16x16x128_f8f6f4 v[66:69], v[2:9], v[196:203], v[66:69], v1, v1 op_sel_hi:[0,0,0]
	v_mfma_scale_f32_16x16x128_f8f6f4 v[82:85], v[2:9], v[188:195], v[82:85], v1, v1 op_sel_hi:[0,0,0]
	s_setprio 0
	s_barrier
	s_add_i32 s59, 0, 0x18000
	s_add_i32 s60, 0, 0x1c000
	v_add_u32_e32 v14, s59, v183
	v_add_u32_e32 v30, s60, v183
	ds_read_b128 v[2:5], v14
	ds_read_b128 v[6:9], v14 offset:1024
	ds_read_b128 v[10:13], v14 offset:2048
	ds_read_b128 v[14:17], v14 offset:3072
	ds_read_b128 v[18:21], v30
	ds_read_b128 v[22:25], v30 offset:1024
	ds_read_b128 v[26:29], v30 offset:2048
	ds_read_b128 v[30:33], v30 offset:3072
	s_add_u32 s24, s30, 0x158000
	s_addc_u32 s25, s31, 0
	s_mov_b32 m0, s34
	v_lshl_add_u64 v[220:221], s[24:25], 0, v[164:165]
	ds_read_b128 v[188:191], v187 offset:32768
	ds_read_b128 v[192:195], v187 offset:33792
	ds_read_b128 v[196:199], v187 offset:34816
	ds_read_b128 v[200:203], v187 offset:35840
	ds_read_b128 v[204:207], v187 offset:36864
	ds_read_b128 v[208:211], v187 offset:37888
	ds_read_b128 v[212:215], v187 offset:38912
	ds_read_b128 v[216:219], v187 offset:39936
	global_load_lds_dwordx4 v[220:221], off
	v_lshl_add_u64 v[220:221], s[24:25], 0, v[162:163]
	s_mov_b32 m0, s35
	s_nop 0
	global_load_lds_dwordx4 v[220:221], off
	s_waitcnt vmcnt(8)
	s_waitcnt lgkmcnt(0)
	s_barrier
	s_setprio 1
	s_waitcnt lgkmcnt(0)
	v_mfma_scale_f32_16x16x128_f8f6f4 v[158:161], v[2:9], v[188:195], v[158:161], v1, v1 op_sel_hi:[0,0,0]
	v_mfma_scale_f32_16x16x128_f8f6f4 v[142:145], v[2:9], v[196:203], v[142:145], v1, v1 op_sel_hi:[0,0,0]
	v_mfma_scale_f32_16x16x128_f8f6f4 v[126:129], v[2:9], v[204:211], v[126:129], v1, v1 op_sel_hi:[0,0,0]
	v_mfma_scale_f32_16x16x128_f8f6f4 v[110:113], v[2:9], v[212:219], v[110:113], v1, v1 op_sel_hi:[0,0,0]
	v_mfma_scale_f32_16x16x128_f8f6f4 v[106:109], v[10:17], v[212:219], v[106:109], v1, v1 op_sel_hi:[0,0,0]
	v_mfma_scale_f32_16x16x128_f8f6f4 v[122:125], v[10:17], v[204:211], v[122:125], v1, v1 op_sel_hi:[0,0,0]
	v_mfma_scale_f32_16x16x128_f8f6f4 v[138:141], v[10:17], v[196:203], v[138:141], v1, v1 op_sel_hi:[0,0,0]
	v_mfma_scale_f32_16x16x128_f8f6f4 v[154:157], v[10:17], v[188:195], v[154:157], v1, v1 op_sel_hi:[0,0,0]
	s_setprio 0
	s_setprio 1
	v_mfma_scale_f32_16x16x128_f8f6f4 v[150:153], v[18:25], v[188:195], v[150:153], v1, v1 op_sel_hi:[0,0,0]
	v_mfma_scale_f32_16x16x128_f8f6f4 v[134:137], v[18:25], v[196:203], v[134:137], v1, v1 op_sel_hi:[0,0,0]
	v_mfma_scale_f32_16x16x128_f8f6f4 v[118:121], v[18:25], v[204:211], v[118:121], v1, v1 op_sel_hi:[0,0,0]
	v_mfma_scale_f32_16x16x128_f8f6f4 v[102:105], v[18:25], v[212:219], v[102:105], v1, v1 op_sel_hi:[0,0,0]
	v_mfma_scale_f32_16x16x128_f8f6f4 v[98:101], v[26:33], v[212:219], v[98:101], v1, v1 op_sel_hi:[0,0,0]
	v_mfma_scale_f32_16x16x128_f8f6f4 v[114:117], v[26:33], v[204:211], v[114:117], v1, v1 op_sel_hi:[0,0,0]
	v_mfma_scale_f32_16x16x128_f8f6f4 v[130:133], v[26:33], v[196:203], v[130:133], v1, v1 op_sel_hi:[0,0,0]
	v_mfma_scale_f32_16x16x128_f8f6f4 v[146:149], v[26:33], v[188:195], v[146:149], v1, v1 op_sel_hi:[0,0,0]
	s_setprio 0
	s_barrier
	s_add_i32 s24, s59, s3
	v_lshl_add_u64 v[174:175], v[174:175], 0, s[12:13]
	s_mov_b32 m0, s24
	ds_read_b128 v[188:191], v187 offset:49152
	ds_read_b128 v[192:195], v187 offset:50176
	ds_read_b128 v[196:199], v187 offset:51200
	ds_read_b128 v[200:203], v187 offset:52224
	ds_read_b128 v[204:207], v187 offset:53248
	ds_read_b128 v[208:211], v187 offset:54272
	ds_read_b128 v[212:215], v187 offset:55296
	ds_read_b128 v[216:219], v187 offset:56320
	global_load_lds_dwordx4 v[174:175], off
	s_add_i32 m0, s24, 0x2000
	s_add_u32 s24, s28, 0x158080
	v_lshl_add_u64 v[174:175], v[176:177], 0, s[12:13]
	s_addc_u32 s25, s29, 0
	s_add_i32 s28, s60, s3
	global_load_lds_dwordx4 v[174:175], off
	v_lshl_add_u64 v[174:175], s[24:25], 0, v[164:165]
	s_mov_b32 m0, s28
	s_nop 0
	global_load_lds_dwordx4 v[174:175], off
	v_lshl_add_u64 v[174:175], s[24:25], 0, v[162:163]
	s_add_i32 m0, s28, 0x2000
	s_nop 0
	global_load_lds_dwordx4 v[174:175], off
	v_lshl_add_u64 v[174:175], v[178:179], 0, s[12:13]
	s_mov_b32 m0, s38
	s_nop 0
	global_load_lds_dwordx4 v[174:175], off
	v_lshl_add_u64 v[174:175], v[180:181], 0, s[12:13]
	s_mov_b32 m0, s39
	s_nop 0
	global_load_lds_dwordx4 v[174:175], off
	s_waitcnt vmcnt(8)
	s_waitcnt lgkmcnt(0)
	s_barrier
	s_setprio 1
	s_waitcnt lgkmcnt(0)
	v_mfma_scale_f32_16x16x128_f8f6f4 v[94:97], v[2:9], v[188:195], v[94:97], v1, v1 op_sel_hi:[0,0,0]
	v_mfma_scale_f32_16x16x128_f8f6f4 v[78:81], v[2:9], v[196:203], v[78:81], v1, v1 op_sel_hi:[0,0,0]
	v_mfma_scale_f32_16x16x128_f8f6f4 v[62:65], v[2:9], v[204:211], v[62:65], v1, v1 op_sel_hi:[0,0,0]
	v_mfma_scale_f32_16x16x128_f8f6f4 v[46:49], v[2:9], v[212:219], v[46:49], v1, v1 op_sel_hi:[0,0,0]
	v_mfma_scale_f32_16x16x128_f8f6f4 v[42:45], v[10:17], v[212:219], v[42:45], v1, v1 op_sel_hi:[0,0,0]
	v_mfma_scale_f32_16x16x128_f8f6f4 v[58:61], v[10:17], v[204:211], v[58:61], v1, v1 op_sel_hi:[0,0,0]
	v_mfma_scale_f32_16x16x128_f8f6f4 v[74:77], v[10:17], v[196:203], v[74:77], v1, v1 op_sel_hi:[0,0,0]
	v_mfma_scale_f32_16x16x128_f8f6f4 v[90:93], v[10:17], v[188:195], v[90:93], v1, v1 op_sel_hi:[0,0,0]
	s_setprio 0
	s_setprio 1
	v_mfma_scale_f32_16x16x128_f8f6f4 v[86:89], v[18:25], v[188:195], v[86:89], v1, v1 op_sel_hi:[0,0,0]
	v_mfma_scale_f32_16x16x128_f8f6f4 v[70:73], v[18:25], v[196:203], v[70:73], v1, v1 op_sel_hi:[0,0,0]
	v_mfma_scale_f32_16x16x128_f8f6f4 v[54:57], v[18:25], v[204:211], v[54:57], v1, v1 op_sel_hi:[0,0,0]
	v_mfma_scale_f32_16x16x128_f8f6f4 v[38:41], v[18:25], v[212:219], v[38:41], v1, v1 op_sel_hi:[0,0,0]
	v_mfma_scale_f32_16x16x128_f8f6f4 v[34:37], v[26:33], v[212:219], v[34:37], v1, v1 op_sel_hi:[0,0,0]
	v_mfma_scale_f32_16x16x128_f8f6f4 v[50:53], v[26:33], v[204:211], v[50:53], v1, v1 op_sel_hi:[0,0,0]
	v_mfma_scale_f32_16x16x128_f8f6f4 v[66:69], v[26:33], v[196:203], v[66:69], v1, v1 op_sel_hi:[0,0,0]
	v_mfma_scale_f32_16x16x128_f8f6f4 v[82:85], v[26:33], v[188:195], v[82:85], v1, v1 op_sel_hi:[0,0,0]
	s_setprio 0
	s_barrier
	s_add_i32 s58, s58, 2
	s_add_u32 s26, s26, 0x100
	s_addc_u32 s27, s27, 0
	s_add_u32 s50, s50, 0x100
	s_addc_u32 s51, s51, 0
	s_cmpk_gt_u32 s58, 0x53
	s_cbranch_scc0 .LBB0_318
	s_and_b64 vcc, exec, s[14:15]
	s_cbranch_vccz .LBB0_321
	s_barrier

.LBB0_332:
	s_add_u32 s6, s61, s4
	s_addc_u32 s7, s62, s5
	s_add_u32 s6, s6, 0x32800100
	s_addc_u32 s7, s7, 0
	s_add_u32 s24, s63, s4
	s_addc_u32 s25, s68, s5
	s_add_i32 s64, 0, 0x10000
	s_cmpk_eq_i32 s4, 0x2a00
	s_cselect_b32 s13, s1, s7
	s_cselect_b32 s12, s0, s6
	s_cselect_b32 s7, s29, s25
	s_cselect_b32 s6, s28, s24
	s_add_i32 s65, 0, 0x14000
	v_add_u32_e32 v2, s64, v188
	v_add_u32_e32 v6, s65, v188
	ds_read_b128 v[26:29], v2
	ds_read_b128 v[30:33], v2 offset:1024
	ds_read_b128 v[18:21], v2 offset:2048
	ds_read_b128 v[22:25], v2 offset:3072
	ds_read_b128 v[10:13], v6
	ds_read_b128 v[14:17], v6 offset:1024
	ds_read_b128 v[2:5], v6 offset:2048
	ds_read_b128 v[6:9], v6 offset:3072
	v_lshl_add_u64 v[214:215], v[168:169], 0, s[4:5]
	s_add_i32 m0, s18, 0xc000
	ds_read_b128 v[172:175], v189
	ds_read_b128 v[176:179], v189 offset:1024
	ds_read_b128 v[190:193], v189 offset:2048
	ds_read_b128 v[194:197], v189 offset:3072
	ds_read_b128 v[198:201], v189 offset:4096
	ds_read_b128 v[202:205], v189 offset:5120
	ds_read_b128 v[206:209], v189 offset:6144
	ds_read_b128 v[210:213], v189 offset:7168
	global_load_lds_dwordx4 v[214:215], off
	v_lshl_add_u64 v[214:215], v[170:171], 0, s[4:5]
	s_add_i32 m0, s18, 0xe000
	s_nop 0
	global_load_lds_dwordx4 v[214:215], off
	s_waitcnt vmcnt(8)
	s_waitcnt lgkmcnt(0)
	s_barrier
	s_setprio 1
	s_waitcnt lgkmcnt(0)
	v_mfma_scale_f32_16x16x128_f8f6f4 v[70:73], v[26:33], v[172:179], v[70:73], v187, v187 op_sel_hi:[0,0,0]
	v_mfma_scale_f32_16x16x128_f8f6f4 v[78:81], v[26:33], v[190:197], v[78:81], v187, v187 op_sel_hi:[0,0,0]
	v_mfma_scale_f32_16x16x128_f8f6f4 v[86:89], v[26:33], v[198:205], v[86:89], v187, v187 op_sel_hi:[0,0,0]
	v_mfma_scale_f32_16x16x128_f8f6f4 v[94:97], v[26:33], v[206:213], v[94:97], v187, v187 op_sel_hi:[0,0,0]
	v_mfma_scale_f32_16x16x128_f8f6f4 v[90:93], v[18:25], v[206:213], v[90:93], v187, v187 op_sel_hi:[0,0,0]
	v_mfma_scale_f32_16x16x128_f8f6f4 v[82:85], v[18:25], v[198:205], v[82:85], v187, v187 op_sel_hi:[0,0,0]
	v_mfma_scale_f32_16x16x128_f8f6f4 v[74:77], v[18:25], v[190:197], v[74:77], v187, v187 op_sel_hi:[0,0,0]
	v_mfma_scale_f32_16x16x128_f8f6f4 v[66:69], v[18:25], v[172:179], v[66:69], v187, v187 op_sel_hi:[0,0,0]
	s_setprio 0
	s_setprio 1
	v_mfma_scale_f32_16x16x128_f8f6f4 v[158:161], v[10:17], v[172:179], v[158:161], v187, v187 op_sel_hi:[0,0,0]
	v_mfma_scale_f32_16x16x128_f8f6f4 v[150:153], v[10:17], v[190:197], v[150:153], v187, v187 op_sel_hi:[0,0,0]
	v_mfma_scale_f32_16x16x128_f8f6f4 v[142:145], v[10:17], v[198:205], v[142:145], v187, v187 op_sel_hi:[0,0,0]
	v_mfma_scale_f32_16x16x128_f8f6f4 v[134:137], v[10:17], v[206:213], v[134:137], v187, v187 op_sel_hi:[0,0,0]
	v_mfma_scale_f32_16x16x128_f8f6f4 v[130:133], v[2:9], v[206:213], v[130:133], v187, v187 op_sel_hi:[0,0,0]
	v_mfma_scale_f32_16x16x128_f8f6f4 v[138:141], v[2:9], v[198:205], v[138:141], v187, v187 op_sel_hi:[0,0,0]
	v_mfma_scale_f32_16x16x128_f8f6f4 v[146:149], v[2:9], v[190:197], v[146:149], v187, v187 op_sel_hi:[0,0,0]
	v_mfma_scale_f32_16x16x128_f8f6f4 v[154:157], v[2:9], v[172:179], v[154:157], v187, v187 op_sel_hi:[0,0,0]
	s_setprio 0
	s_barrier
	s_add_i32 s24, s64, s17
	v_lshl_add_u64 v[172:173], s[6:7], 0, v[162:163]
	s_mov_b32 m0, s24
	ds_read_b128 v[190:193], v189 offset:16384
	ds_read_b128 v[194:197], v189 offset:17408
	ds_read_b128 v[198:201], v189 offset:18432
	ds_read_b128 v[202:205], v189 offset:19456
	ds_read_b128 v[206:209], v189 offset:20480
	ds_read_b128 v[210:213], v189 offset:21504
	ds_read_b128 v[214:217], v189 offset:22528
	ds_read_b128 v[218:221], v189 offset:23552
	global_load_lds_dwordx4 v[172:173], off
	s_add_i32 m0, s24, 0x2000
	s_add_u32 s24, s6, 0x158000
	v_lshl_add_u64 v[174:175], s[6:7], 0, v[166:167]
	s_addc_u32 s25, s7, 0
	s_add_i32 s64, s65, s17
	global_load_lds_dwordx4 v[174:175], off
	v_lshl_add_u64 v[176:177], s[24:25], 0, v[162:163]
	s_mov_b32 m0, s64
	v_lshl_add_u64 v[178:179], s[12:13], 0, v[166:167]
	global_load_lds_dwordx4 v[176:177], off
	v_lshl_add_u64 v[176:177], s[24:25], 0, v[166:167]
	s_add_i32 m0, s64, 0x2000
	s_nop 0
	global_load_lds_dwordx4 v[176:177], off
	v_lshl_add_u64 v[176:177], s[12:13], 0, v[162:163]
	s_mov_b32 m0, s18
	s_nop 0
	global_load_lds_dwordx4 v[176:177], off
	s_mov_b32 m0, s19
	s_nop 0
	global_load_lds_dwordx4 v[178:179], off
	s_waitcnt vmcnt(8)
	s_waitcnt lgkmcnt(0)
	s_barrier
	s_setprio 1
	s_waitcnt lgkmcnt(0)
	v_mfma_scale_f32_16x16x128_f8f6f4 v[102:105], v[26:33], v[190:197], v[102:105], v187, v187 op_sel_hi:[0,0,0]
	v_mfma_scale_f32_16x16x128_f8f6f4 v[110:113], v[26:33], v[198:205], v[110:113], v187, v187 op_sel_hi:[0,0,0]
	v_mfma_scale_f32_16x16x128_f8f6f4 v[118:121], v[26:33], v[206:213], v[118:121], v187, v187 op_sel_hi:[0,0,0]
	v_mfma_scale_f32_16x16x128_f8f6f4 v[126:129], v[26:33], v[214:221], v[126:129], v187, v187 op_sel_hi:[0,0,0]
	v_mfma_scale_f32_16x16x128_f8f6f4 v[122:125], v[18:25], v[214:221], v[122:125], v187, v187 op_sel_hi:[0,0,0]
	v_mfma_scale_f32_16x16x128_f8f6f4 v[114:117], v[18:25], v[206:213], v[114:117], v187, v187 op_sel_hi:[0,0,0]
	v_mfma_scale_f32_16x16x128_f8f6f4 v[106:109], v[18:25], v[198:205], v[106:109], v187, v187 op_sel_hi:[0,0,0]
	v_mfma_scale_f32_16x16x128_f8f6f4 v[98:101], v[18:25], v[190:197], v[98:101], v187, v187 op_sel_hi:[0,0,0]
	s_setprio 0
	s_setprio 1
	v_mfma_scale_f32_16x16x128_f8f6f4 v[38:41], v[10:17], v[190:197], v[38:41], v187, v187 op_sel_hi:[0,0,0]
	v_mfma_scale_f32_16x16x128_f8f6f4 v[46:49], v[10:17], v[198:205], v[46:49], v187, v187 op_sel_hi:[0,0,0]
	v_mfma_scale_f32_16x16x128_f8f6f4 v[54:57], v[10:17], v[206:213], v[54:57], v187, v187 op_sel_hi:[0,0,0]
	v_mfma_scale_f32_16x16x128_f8f6f4 v[62:65], v[10:17], v[214:221], v[62:65], v187, v187 op_sel_hi:[0,0,0]
	v_mfma_scale_f32_16x16x128_f8f6f4 v[58:61], v[2:9], v[214:221], v[58:61], v187, v187 op_sel_hi:[0,0,0]
	v_mfma_scale_f32_16x16x128_f8f6f4 v[50:53], v[2:9], v[206:213], v[50:53], v187, v187 op_sel_hi:[0,0,0]
	v_mfma_scale_f32_16x16x128_f8f6f4 v[42:45], v[2:9], v[198:205], v[42:45], v187, v187 op_sel_hi:[0,0,0]
	v_mfma_scale_f32_16x16x128_f8f6f4 v[34:37], v[2:9], v[190:197], v[34:37], v187, v187 op_sel_hi:[0,0,0]
	s_setprio 0
	s_barrier
	s_add_i32 s24, 0, 0x18000
	s_add_i32 s25, 0, 0x1c000
	v_add_u32_e32 v14, s24, v188
	v_add_u32_e32 v30, s25, v188
	ds_read_b128 v[2:5], v14
	ds_read_b128 v[6:9], v14 offset:1024
	ds_read_b128 v[10:13], v14 offset:2048
	ds_read_b128 v[14:17], v14 offset:3072
	ds_read_b128 v[18:21], v30
	ds_read_b128 v[22:25], v30 offset:1024
	ds_read_b128 v[26:29], v30 offset:2048
	ds_read_b128 v[30:33], v30 offset:3072
	s_add_u32 s12, s12, 0x158000
	s_addc_u32 s13, s13, 0
	s_mov_b32 m0, s93
	v_lshl_add_u64 v[222:223], s[12:13], 0, v[162:163]
	ds_read_b128 v[190:193], v189 offset:32768
	ds_read_b128 v[194:197], v189 offset:33792
	ds_read_b128 v[198:201], v189 offset:34816
	ds_read_b128 v[202:205], v189 offset:35840
	ds_read_b128 v[206:209], v189 offset:36864
	ds_read_b128 v[210:213], v189 offset:37888
	ds_read_b128 v[214:217], v189 offset:38912
	ds_read_b128 v[218:221], v189 offset:39936
	global_load_lds_dwordx4 v[222:223], off
	v_lshl_add_u64 v[222:223], s[12:13], 0, v[166:167]
	s_mov_b32 m0, s94
	s_nop 0
	global_load_lds_dwordx4 v[222:223], off
	s_waitcnt vmcnt(8)
	s_waitcnt lgkmcnt(0)
	s_barrier
	s_setprio 1
	s_waitcnt lgkmcnt(0)
	v_mfma_scale_f32_16x16x128_f8f6f4 v[70:73], v[2:9], v[190:197], v[70:73], v187, v187 op_sel_hi:[0,0,0]
	v_mfma_scale_f32_16x16x128_f8f6f4 v[78:81], v[2:9], v[198:205], v[78:81], v187, v187 op_sel_hi:[0,0,0]
	v_mfma_scale_f32_16x16x128_f8f6f4 v[86:89], v[2:9], v[206:213], v[86:89], v187, v187 op_sel_hi:[0,0,0]
	v_mfma_scale_f32_16x16x128_f8f6f4 v[94:97], v[2:9], v[214:221], v[94:97], v187, v187 op_sel_hi:[0,0,0]
	v_mfma_scale_f32_16x16x128_f8f6f4 v[90:93], v[10:17], v[214:221], v[90:93], v187, v187 op_sel_hi:[0,0,0]
	v_mfma_scale_f32_16x16x128_f8f6f4 v[82:85], v[10:17], v[206:213], v[82:85], v187, v187 op_sel_hi:[0,0,0]
	v_mfma_scale_f32_16x16x128_f8f6f4 v[74:77], v[10:17], v[198:205], v[74:77], v187, v187 op_sel_hi:[0,0,0]
	v_mfma_scale_f32_16x16x128_f8f6f4 v[66:69], v[10:17], v[190:197], v[66:69], v187, v187 op_sel_hi:[0,0,0]
	s_setprio 0
	s_setprio 1
	v_mfma_scale_f32_16x16x128_f8f6f4 v[158:161], v[18:25], v[190:197], v[158:161], v187, v187 op_sel_hi:[0,0,0]
	v_mfma_scale_f32_16x16x128_f8f6f4 v[150:153], v[18:25], v[198:205], v[150:153], v187, v187 op_sel_hi:[0,0,0]
	v_mfma_scale_f32_16x16x128_f8f6f4 v[142:145], v[18:25], v[206:213], v[142:145], v187, v187 op_sel_hi:[0,0,0]
	v_mfma_scale_f32_16x16x128_f8f6f4 v[134:137], v[18:25], v[214:221], v[134:137], v187, v187 op_sel_hi:[0,0,0]
	v_mfma_scale_f32_16x16x128_f8f6f4 v[130:133], v[26:33], v[214:221], v[130:133], v187, v187 op_sel_hi:[0,0,0]
	v_mfma_scale_f32_16x16x128_f8f6f4 v[138:141], v[26:33], v[206:213], v[138:141], v187, v187 op_sel_hi:[0,0,0]
	v_mfma_scale_f32_16x16x128_f8f6f4 v[146:149], v[26:33], v[198:205], v[146:149], v187, v187 op_sel_hi:[0,0,0]
	v_mfma_scale_f32_16x16x128_f8f6f4 v[154:157], v[26:33], v[190:197], v[154:157], v187, v187 op_sel_hi:[0,0,0]
	s_setprio 0
	s_barrier
	s_add_i32 s12, s24, s17
	v_lshl_add_u64 v[172:173], v[172:173], 0, s[76:77]
	s_mov_b32 m0, s12
	ds_read_b128 v[190:193], v189 offset:49152
	ds_read_b128 v[194:197], v189 offset:50176
	ds_read_b128 v[198:201], v189 offset:51200
	ds_read_b128 v[202:205], v189 offset:52224
	ds_read_b128 v[206:209], v189 offset:53248
	ds_read_b128 v[210:213], v189 offset:54272
	ds_read_b128 v[214:217], v189 offset:55296
	ds_read_b128 v[218:221], v189 offset:56320
	global_load_lds_dwordx4 v[172:173], off
	s_add_i32 m0, s12, 0x2000
	s_add_u32 s6, s6, 0x158080
	v_lshl_add_u64 v[172:173], v[174:175], 0, s[76:77]
	s_addc_u32 s7, s7, 0
	s_add_i32 s12, s25, s17
	global_load_lds_dwordx4 v[172:173], off
	v_lshl_add_u64 v[172:173], s[6:7], 0, v[162:163]
	s_mov_b32 m0, s12
	s_nop 0
	global_load_lds_dwordx4 v[172:173], off
	v_lshl_add_u64 v[172:173], s[6:7], 0, v[166:167]
	s_add_i32 m0, s12, 0x2000
	s_nop 0
	global_load_lds_dwordx4 v[172:173], off
	v_lshl_add_u64 v[172:173], v[176:177], 0, s[76:77]
	s_mov_b32 m0, s95
	s_nop 0
	global_load_lds_dwordx4 v[172:173], off
	v_lshl_add_u64 v[172:173], v[178:179], 0, s[76:77]
	s_mov_b32 m0, vcc_lo
	s_nop 0
	global_load_lds_dwordx4 v[172:173], off
	s_waitcnt vmcnt(8)
	s_waitcnt lgkmcnt(0)
	s_barrier
	s_setprio 1
	s_waitcnt lgkmcnt(0)
	v_mfma_scale_f32_16x16x128_f8f6f4 v[102:105], v[2:9], v[190:197], v[102:105], v187, v187 op_sel_hi:[0,0,0]
	v_mfma_scale_f32_16x16x128_f8f6f4 v[110:113], v[2:9], v[198:205], v[110:113], v187, v187 op_sel_hi:[0,0,0]
	v_mfma_scale_f32_16x16x128_f8f6f4 v[118:121], v[2:9], v[206:213], v[118:121], v187, v187 op_sel_hi:[0,0,0]
	v_mfma_scale_f32_16x16x128_f8f6f4 v[126:129], v[2:9], v[214:221], v[126:129], v187, v187 op_sel_hi:[0,0,0]
	v_mfma_scale_f32_16x16x128_f8f6f4 v[122:125], v[10:17], v[214:221], v[122:125], v187, v187 op_sel_hi:[0,0,0]
	v_mfma_scale_f32_16x16x128_f8f6f4 v[114:117], v[10:17], v[206:213], v[114:117], v187, v187 op_sel_hi:[0,0,0]
	v_mfma_scale_f32_16x16x128_f8f6f4 v[106:109], v[10:17], v[198:205], v[106:109], v187, v187 op_sel_hi:[0,0,0]
	v_mfma_scale_f32_16x16x128_f8f6f4 v[98:101], v[10:17], v[190:197], v[98:101], v187, v187 op_sel_hi:[0,0,0]
	s_setprio 0
	s_setprio 1
	v_mfma_scale_f32_16x16x128_f8f6f4 v[38:41], v[18:25], v[190:197], v[38:41], v187, v187 op_sel_hi:[0,0,0]
	v_mfma_scale_f32_16x16x128_f8f6f4 v[46:49], v[18:25], v[198:205], v[46:49], v187, v187 op_sel_hi:[0,0,0]
	v_mfma_scale_f32_16x16x128_f8f6f4 v[54:57], v[18:25], v[206:213], v[54:57], v187, v187 op_sel_hi:[0,0,0]
	v_mfma_scale_f32_16x16x128_f8f6f4 v[62:65], v[18:25], v[214:221], v[62:65], v187, v187 op_sel_hi:[0,0,0]
	v_mfma_scale_f32_16x16x128_f8f6f4 v[58:61], v[26:33], v[214:221], v[58:61], v187, v187 op_sel_hi:[0,0,0]
	v_mfma_scale_f32_16x16x128_f8f6f4 v[50:53], v[26:33], v[206:213], v[50:53], v187, v187 op_sel_hi:[0,0,0]
	v_mfma_scale_f32_16x16x128_f8f6f4 v[42:45], v[26:33], v[198:205], v[42:45], v187, v187 op_sel_hi:[0,0,0]
	v_mfma_scale_f32_16x16x128_f8f6f4 v[34:37], v[26:33], v[190:197], v[34:37], v187, v187 op_sel_hi:[0,0,0]
	s_setprio 0
	s_barrier
	s_add_i32 vcc_hi, vcc_hi, 2
	s_add_u32 s4, s4, 0x100
	s_addc_u32 s5, s5, 0
	s_cmpk_lt_u32 vcc_hi, 0x54
	s_cbranch_scc1 .LBB0_332
	s_waitcnt vmcnt(0)
	s_mov_b64 s[12:13], s[54:55]
	s_cmpk_gt_u32 s89, 0xff
	s_cbranch_scc1 .LBB0_335
	s_barrier

.LBB0_788:
	v_add_u32_e32 v130, s15, v190
	v_add_u32_e32 v134, s50, v190
	ds_read_b128 v[158:161], v130
	ds_read_b128 v[150:153], v130 offset:1024
	ds_read_b128 v[154:157], v130 offset:2048
	ds_read_b128 v[146:149], v130 offset:3072
	ds_read_b128 v[142:145], v134
	ds_read_b128 v[130:133], v134 offset:1024
	ds_read_b128 v[138:141], v134 offset:2048
	ds_read_b128 v[134:137], v134 offset:3072
	s_add_u32 s36, s34, 0xfff80080
	s_addc_u32 s37, s35, -1
	s_and_b64 s[0:1], s[0:1], exec
	s_cselect_b32 s39, s21, s37
	s_cselect_b32 s38, s60, s36
	s_cselect_b32 s37, s17, s63
	s_cselect_b32 s36, s61, s62
	s_add_i32 m0, s29, 0xc000
	ds_read_b128 v[182:185], v193
	ds_read_b128 v[186:189], v193 offset:1024
	ds_read_b128 v[194:197], v193 offset:2048
	ds_read_b128 v[198:201], v193 offset:3072
	ds_read_b128 v[202:205], v193 offset:4096
	ds_read_b128 v[206:209], v193 offset:5120
	ds_read_b128 v[210:213], v193 offset:6144
	ds_read_b128 v[214:217], v193 offset:7168
	global_load_lds_dwordx4 v172, s[34:35]
	s_add_i32 m0, s29, 0xe000
	s_nop 0
	global_load_lds_dwordx4 v174, s[34:35]
	s_waitcnt vmcnt(8)
	s_waitcnt lgkmcnt(0)
	s_barrier
	s_setprio 1
	s_waitcnt lgkmcnt(0)
	v_mfma_i32_16x16x64_i8 v[126:129], v[158:161], v[182:185], v[126:129]
	v_mfma_i32_16x16x64_i8 v[114:117], v[158:161], v[194:197], v[114:117]
	v_mfma_i32_16x16x64_i8 v[98:101], v[158:161], v[202:205], v[98:101]
	v_mfma_i32_16x16x64_i8 v[82:85], v[158:161], v[210:213], v[82:85]
	v_mfma_i32_16x16x64_i8 v[74:77], v[154:157], v[210:213], v[74:77]
	v_mfma_i32_16x16x64_i8 v[90:93], v[154:157], v[202:205], v[90:93]
	v_mfma_i32_16x16x64_i8 v[106:109], v[154:157], v[194:197], v[106:109]
	v_mfma_i32_16x16x64_i8 v[122:125], v[154:157], v[182:185], v[122:125]
	s_nop 0
	v_mfma_i32_16x16x64_i8 v[126:129], v[150:153], v[186:189], v[126:129]
	v_mfma_i32_16x16x64_i8 v[114:117], v[150:153], v[198:201], v[114:117]
	v_mfma_i32_16x16x64_i8 v[98:101], v[150:153], v[206:209], v[98:101]
	v_mfma_i32_16x16x64_i8 v[82:85], v[150:153], v[214:217], v[82:85]
	v_mfma_i32_16x16x64_i8 v[74:77], v[146:149], v[214:217], v[74:77]
	v_mfma_i32_16x16x64_i8 v[90:93], v[146:149], v[206:209], v[90:93]
	v_mfma_i32_16x16x64_i8 v[106:109], v[146:149], v[198:201], v[106:109]
	v_mfma_i32_16x16x64_i8 v[122:125], v[146:149], v[186:189], v[122:125]
	s_setprio 0
	s_setprio 1
	v_mfma_i32_16x16x64_i8 v[118:121], v[142:145], v[182:185], v[118:121]
	v_mfma_i32_16x16x64_i8 v[102:105], v[142:145], v[194:197], v[102:105]
	v_mfma_i32_16x16x64_i8 v[86:89], v[142:145], v[202:205], v[86:89]
	v_mfma_i32_16x16x64_i8 v[70:73], v[142:145], v[210:213], v[70:73]
	v_mfma_i32_16x16x64_i8 v[66:69], v[138:141], v[210:213], v[66:69]
	v_mfma_i32_16x16x64_i8 v[78:81], v[138:141], v[202:205], v[78:81]
	v_mfma_i32_16x16x64_i8 v[94:97], v[138:141], v[194:197], v[94:97]
	v_mfma_i32_16x16x64_i8 v[110:113], v[138:141], v[182:185], v[110:113]
	s_nop 0
	v_mfma_i32_16x16x64_i8 v[118:121], v[130:133], v[186:189], v[118:121]
	v_mfma_i32_16x16x64_i8 v[102:105], v[130:133], v[198:201], v[102:105]
	v_mfma_i32_16x16x64_i8 v[86:89], v[130:133], v[206:209], v[86:89]
	v_mfma_i32_16x16x64_i8 v[70:73], v[130:133], v[214:217], v[70:73]
	v_mfma_i32_16x16x64_i8 v[66:69], v[134:137], v[214:217], v[66:69]
	v_mfma_i32_16x16x64_i8 v[78:81], v[134:137], v[206:209], v[78:81]
	v_mfma_i32_16x16x64_i8 v[94:97], v[134:137], v[198:201], v[94:97]
	v_mfma_i32_16x16x64_i8 v[110:113], v[134:137], v[186:189], v[110:113]
	s_setprio 0
	s_barrier
	s_add_i32 s0, s15, s40
	s_mov_b32 m0, s0
	ds_read_b128 v[194:197], v193 offset:16384
	ds_read_b128 v[198:201], v193 offset:17408
	ds_read_b128 v[202:205], v193 offset:18432
	ds_read_b128 v[206:209], v193 offset:19456
	ds_read_b128 v[210:213], v193 offset:20480
	ds_read_b128 v[214:217], v193 offset:21504
	ds_read_b128 v[218:221], v193 offset:22528
	ds_read_b128 v[222:225], v193 offset:23552
	global_load_lds_dwordx4 v164, s[36:37]
	s_add_i32 m0, s0, 0x2000
	s_add_u32 s0, s36, 0x80000
	s_addc_u32 s1, s37, 0
	s_add_i32 s66, s50, s40
	global_load_lds_dwordx4 v168, s[36:37]
	s_mov_b32 m0, s66
	s_nop 0
	global_load_lds_dwordx4 v164, s[0:1]
	s_add_i32 m0, s66, 0x2000
	s_nop 0
	global_load_lds_dwordx4 v168, s[0:1]
	s_mov_b32 m0, s29
	s_nop 0
	global_load_lds_dwordx4 v162, s[38:39]
	s_mov_b32 m0, s31
	s_nop 0
	global_load_lds_dwordx4 v166, s[38:39]
	s_waitcnt vmcnt(8)
	s_waitcnt lgkmcnt(0)
	s_barrier
	s_setprio 1
	s_waitcnt lgkmcnt(0)
	v_mfma_i32_16x16x64_i8 v[62:65], v[158:161], v[194:197], v[62:65]
	v_mfma_i32_16x16x64_i8 v[50:53], v[158:161], v[202:205], v[50:53]
	v_mfma_i32_16x16x64_i8 v[34:37], v[158:161], v[210:213], v[34:37]
	v_mfma_i32_16x16x64_i8 v[18:21], v[158:161], v[218:221], v[18:21]
	v_mfma_i32_16x16x64_i8 v[10:13], v[154:157], v[218:221], v[10:13]
	v_mfma_i32_16x16x64_i8 v[26:29], v[154:157], v[210:213], v[26:29]
	v_mfma_i32_16x16x64_i8 v[42:45], v[154:157], v[202:205], v[42:45]
	v_mfma_i32_16x16x64_i8 v[58:61], v[154:157], v[194:197], v[58:61]
	s_nop 0
	v_mfma_i32_16x16x64_i8 v[62:65], v[150:153], v[198:201], v[62:65]
	v_mfma_i32_16x16x64_i8 v[50:53], v[150:153], v[206:209], v[50:53]
	v_mfma_i32_16x16x64_i8 v[34:37], v[150:153], v[214:217], v[34:37]
	v_mfma_i32_16x16x64_i8 v[18:21], v[150:153], v[222:225], v[18:21]
	v_mfma_i32_16x16x64_i8 v[10:13], v[146:149], v[222:225], v[10:13]
	v_mfma_i32_16x16x64_i8 v[26:29], v[146:149], v[214:217], v[26:29]
	v_mfma_i32_16x16x64_i8 v[42:45], v[146:149], v[206:209], v[42:45]
	v_mfma_i32_16x16x64_i8 v[58:61], v[146:149], v[198:201], v[58:61]
	s_setprio 0
	s_setprio 1
	v_mfma_i32_16x16x64_i8 v[54:57], v[142:145], v[194:197], v[54:57]
	v_mfma_i32_16x16x64_i8 v[38:41], v[142:145], v[202:205], v[38:41]
	v_mfma_i32_16x16x64_i8 v[22:25], v[142:145], v[210:213], v[22:25]
	v_mfma_i32_16x16x64_i8 v[6:9], v[142:145], v[218:221], v[6:9]
	v_mfma_i32_16x16x64_i8 v[2:5], v[138:141], v[218:221], v[2:5]
	v_mfma_i32_16x16x64_i8 v[14:17], v[138:141], v[210:213], v[14:17]
	v_mfma_i32_16x16x64_i8 v[30:33], v[138:141], v[202:205], v[30:33]
	v_mfma_i32_16x16x64_i8 v[46:49], v[138:141], v[194:197], v[46:49]
	s_nop 0
	v_mfma_i32_16x16x64_i8 v[54:57], v[130:133], v[198:201], v[54:57]
	v_mfma_i32_16x16x64_i8 v[38:41], v[130:133], v[206:209], v[38:41]
	v_mfma_i32_16x16x64_i8 v[22:25], v[130:133], v[214:217], v[22:25]
	v_mfma_i32_16x16x64_i8 v[6:9], v[130:133], v[222:225], v[6:9]
	v_mfma_i32_16x16x64_i8 v[2:5], v[134:137], v[222:225], v[2:5]
	v_mfma_i32_16x16x64_i8 v[14:17], v[134:137], v[214:217], v[14:17]
	v_mfma_i32_16x16x64_i8 v[30:33], v[134:137], v[206:209], v[30:33]
	v_mfma_i32_16x16x64_i8 v[46:49], v[134:137], v[198:201], v[46:49]
	s_setprio 0
	s_barrier
	s_add_i32 s66, 0, 0x18000
	s_add_i32 s67, 0, 0x1c000
	v_add_u32_e32 v142, s66, v190
	v_add_u32_e32 v158, s67, v190
	ds_read_b128 v[130:133], v142
	ds_read_b128 v[134:137], v142 offset:1024
	ds_read_b128 v[138:141], v142 offset:2048
	ds_read_b128 v[142:145], v142 offset:3072
	ds_read_b128 v[146:149], v158
	ds_read_b128 v[150:153], v158 offset:1024
	ds_read_b128 v[154:157], v158 offset:2048
	ds_read_b128 v[158:161], v158 offset:3072
	s_add_u32 s0, s38, 0x80000
	s_addc_u32 s1, s39, 0
	s_mov_b32 m0, s42
	ds_read_b128 v[194:197], v193 offset:32768
	ds_read_b128 v[198:201], v193 offset:33792
	ds_read_b128 v[202:205], v193 offset:34816
	ds_read_b128 v[206:209], v193 offset:35840
	ds_read_b128 v[210:213], v193 offset:36864
	ds_read_b128 v[214:217], v193 offset:37888
	ds_read_b128 v[218:221], v193 offset:38912
	ds_read_b128 v[222:225], v193 offset:39936
	global_load_lds_dwordx4 v162, s[0:1]
	s_mov_b32 m0, s43
	s_nop 0
	global_load_lds_dwordx4 v166, s[0:1]
	s_waitcnt vmcnt(8)
	s_waitcnt lgkmcnt(0)
	s_barrier
	s_setprio 1
	s_waitcnt lgkmcnt(0)
	v_mfma_i32_16x16x64_i8 v[126:129], v[130:133], v[194:197], v[126:129]
	v_mfma_i32_16x16x64_i8 v[114:117], v[130:133], v[202:205], v[114:117]
	v_mfma_i32_16x16x64_i8 v[98:101], v[130:133], v[210:213], v[98:101]
	v_mfma_i32_16x16x64_i8 v[82:85], v[130:133], v[218:221], v[82:85]
	v_mfma_i32_16x16x64_i8 v[74:77], v[138:141], v[218:221], v[74:77]
	v_mfma_i32_16x16x64_i8 v[90:93], v[138:141], v[210:213], v[90:93]
	v_mfma_i32_16x16x64_i8 v[106:109], v[138:141], v[202:205], v[106:109]
	v_mfma_i32_16x16x64_i8 v[122:125], v[138:141], v[194:197], v[122:125]
	s_nop 0
	v_mfma_i32_16x16x64_i8 v[126:129], v[134:137], v[198:201], v[126:129]
	v_mfma_i32_16x16x64_i8 v[114:117], v[134:137], v[206:209], v[114:117]
	v_mfma_i32_16x16x64_i8 v[98:101], v[134:137], v[214:217], v[98:101]
	v_mfma_i32_16x16x64_i8 v[82:85], v[134:137], v[222:225], v[82:85]
	v_mfma_i32_16x16x64_i8 v[74:77], v[142:145], v[222:225], v[74:77]
	v_mfma_i32_16x16x64_i8 v[90:93], v[142:145], v[214:217], v[90:93]
	v_mfma_i32_16x16x64_i8 v[106:109], v[142:145], v[206:209], v[106:109]
	v_mfma_i32_16x16x64_i8 v[122:125], v[142:145], v[198:201], v[122:125]
	s_setprio 0
	s_setprio 1
	v_mfma_i32_16x16x64_i8 v[118:121], v[146:149], v[194:197], v[118:121]
	v_mfma_i32_16x16x64_i8 v[102:105], v[146:149], v[202:205], v[102:105]
	v_mfma_i32_16x16x64_i8 v[86:89], v[146:149], v[210:213], v[86:89]
	v_mfma_i32_16x16x64_i8 v[70:73], v[146:149], v[218:221], v[70:73]
	v_mfma_i32_16x16x64_i8 v[66:69], v[154:157], v[218:221], v[66:69]
	v_mfma_i32_16x16x64_i8 v[78:81], v[154:157], v[210:213], v[78:81]
	v_mfma_i32_16x16x64_i8 v[94:97], v[154:157], v[202:205], v[94:97]
	v_mfma_i32_16x16x64_i8 v[110:113], v[154:157], v[194:197], v[110:113]
	s_nop 0
	v_mfma_i32_16x16x64_i8 v[118:121], v[150:153], v[198:201], v[118:121]
	v_mfma_i32_16x16x64_i8 v[102:105], v[150:153], v[206:209], v[102:105]
	v_mfma_i32_16x16x64_i8 v[86:89], v[150:153], v[214:217], v[86:89]
	v_mfma_i32_16x16x64_i8 v[70:73], v[150:153], v[222:225], v[70:73]
	v_mfma_i32_16x16x64_i8 v[66:69], v[158:161], v[222:225], v[66:69]
	v_mfma_i32_16x16x64_i8 v[78:81], v[158:161], v[214:217], v[78:81]
	v_mfma_i32_16x16x64_i8 v[94:97], v[158:161], v[206:209], v[94:97]
	v_mfma_i32_16x16x64_i8 v[110:113], v[158:161], v[198:201], v[110:113]
	s_setprio 0
	s_barrier
	s_add_i32 s0, s66, s40
	s_mov_b32 m0, s0
	s_add_u32 s98, s36, 0x80
	s_addc_u32 s99, s37, 0
	s_add_u32 s100, s38, 0x80
	s_addc_u32 s101, s39, 0
	ds_read_b128 v[194:197], v193 offset:49152
	ds_read_b128 v[198:201], v193 offset:50176
	ds_read_b128 v[202:205], v193 offset:51200
	ds_read_b128 v[206:209], v193 offset:52224
	ds_read_b128 v[210:213], v193 offset:53248
	ds_read_b128 v[214:217], v193 offset:54272
	ds_read_b128 v[218:221], v193 offset:55296
	ds_read_b128 v[222:225], v193 offset:56320
	global_load_lds_dwordx4 v164, s[98:99]
	s_add_i32 m0, s0, 0x2000
	s_add_u32 s0, s36, 0x80080
	s_addc_u32 s1, s37, 0
	s_add_i32 s36, s67, s40
	global_load_lds_dwordx4 v168, s[98:99]
	s_mov_b32 m0, s36
	s_nop 0
	global_load_lds_dwordx4 v164, s[0:1]
	s_add_i32 m0, s36, 0x2000
	s_nop 0
	global_load_lds_dwordx4 v168, s[0:1]
	s_mov_b32 m0, s48
	s_nop 0
	global_load_lds_dwordx4 v162, s[100:101]
	s_mov_b32 m0, s49
	s_nop 0
	global_load_lds_dwordx4 v166, s[100:101]
	s_waitcnt vmcnt(8)
	s_waitcnt lgkmcnt(0)
	s_barrier
	s_setprio 1
	s_waitcnt lgkmcnt(0)
	v_mfma_i32_16x16x64_i8 v[62:65], v[130:133], v[194:197], v[62:65]
	v_mfma_i32_16x16x64_i8 v[50:53], v[130:133], v[202:205], v[50:53]
	v_mfma_i32_16x16x64_i8 v[34:37], v[130:133], v[210:213], v[34:37]
	v_mfma_i32_16x16x64_i8 v[18:21], v[130:133], v[218:221], v[18:21]
	v_mfma_i32_16x16x64_i8 v[10:13], v[138:141], v[218:221], v[10:13]
	v_mfma_i32_16x16x64_i8 v[26:29], v[138:141], v[210:213], v[26:29]
	v_mfma_i32_16x16x64_i8 v[42:45], v[138:141], v[202:205], v[42:45]
	v_mfma_i32_16x16x64_i8 v[58:61], v[138:141], v[194:197], v[58:61]
	s_nop 0
	v_mfma_i32_16x16x64_i8 v[62:65], v[134:137], v[198:201], v[62:65]
	v_mfma_i32_16x16x64_i8 v[50:53], v[134:137], v[206:209], v[50:53]
	v_mfma_i32_16x16x64_i8 v[34:37], v[134:137], v[214:217], v[34:37]
	v_mfma_i32_16x16x64_i8 v[18:21], v[134:137], v[222:225], v[18:21]
	v_mfma_i32_16x16x64_i8 v[10:13], v[142:145], v[222:225], v[10:13]
	v_mfma_i32_16x16x64_i8 v[26:29], v[142:145], v[214:217], v[26:29]
	v_mfma_i32_16x16x64_i8 v[42:45], v[142:145], v[206:209], v[42:45]
	v_mfma_i32_16x16x64_i8 v[58:61], v[142:145], v[198:201], v[58:61]
	s_setprio 0
	s_setprio 1
	v_mfma_i32_16x16x64_i8 v[54:57], v[146:149], v[194:197], v[54:57]
	v_mfma_i32_16x16x64_i8 v[38:41], v[146:149], v[202:205], v[38:41]
	v_mfma_i32_16x16x64_i8 v[22:25], v[146:149], v[210:213], v[22:25]
	v_mfma_i32_16x16x64_i8 v[6:9], v[146:149], v[218:221], v[6:9]
	v_mfma_i32_16x16x64_i8 v[2:5], v[154:157], v[218:221], v[2:5]
	v_mfma_i32_16x16x64_i8 v[14:17], v[154:157], v[210:213], v[14:17]
	v_mfma_i32_16x16x64_i8 v[30:33], v[154:157], v[202:205], v[30:33]
	v_mfma_i32_16x16x64_i8 v[46:49], v[154:157], v[194:197], v[46:49]
	s_nop 0
	v_mfma_i32_16x16x64_i8 v[54:57], v[150:153], v[198:201], v[54:57]
	v_mfma_i32_16x16x64_i8 v[38:41], v[150:153], v[206:209], v[38:41]
	v_mfma_i32_16x16x64_i8 v[22:25], v[150:153], v[214:217], v[22:25]
	v_mfma_i32_16x16x64_i8 v[6:9], v[150:153], v[222:225], v[6:9]
	v_mfma_i32_16x16x64_i8 v[2:5], v[158:161], v[222:225], v[2:5]
	v_mfma_i32_16x16x64_i8 v[14:17], v[158:161], v[214:217], v[14:17]
	v_mfma_i32_16x16x64_i8 v[30:33], v[158:161], v[206:209], v[30:33]
	v_mfma_i32_16x16x64_i8 v[46:49], v[158:161], v[198:201], v[46:49]
	s_setprio 0
	s_barrier
	s_add_i32 s64, s64, 2
	s_add_u32 s34, s34, 0x100
	s_addc_u32 s35, s35, 0
	s_add_u32 s62, s62, 0x100
	s_addc_u32 s63, s63, 0
	s_cmp_gt_u32 s64, 29
	s_cbranch_scc1 .LBB0_791

.LBB0_1051:
	s_add_u32 s8, s17, s6
	s_addc_u32 s9, s48, s7
	s_add_u32 s8, s8, 0x32800100
	s_addc_u32 s9, s9, 0
	s_add_u32 s65, s49, s6
	s_addc_u32 s68, s50, s7
	s_add_i32 s69, 0, 0x10000
	s_cmpk_eq_i32 s6, 0xf00
	s_cselect_b32 s41, s5, s9
	s_cselect_b32 s40, s4, s8
	s_cselect_b32 s9, s21, s68
	s_cselect_b32 s8, s20, s65
	s_add_i32 s65, 0, 0x14000
	v_add_u32_e32 v130, s69, v187
	v_add_u32_e32 v134, s65, v187
	ds_read_b128 v[158:161], v130
	ds_read_b128 v[150:153], v130 offset:1024
	ds_read_b128 v[154:157], v130 offset:2048
	ds_read_b128 v[146:149], v130 offset:3072
	ds_read_b128 v[142:145], v134
	ds_read_b128 v[130:133], v134 offset:1024
	ds_read_b128 v[138:141], v134 offset:2048
	ds_read_b128 v[134:137], v134 offset:3072
	v_lshl_add_u64 v[214:215], v[168:169], 0, s[6:7]
	s_add_i32 m0, s43, 0xc000
	ds_read_b128 v[172:175], v188
	ds_read_b128 v[176:179], v188 offset:1024
	ds_read_b128 v[190:193], v188 offset:2048
	ds_read_b128 v[194:197], v188 offset:3072
	ds_read_b128 v[198:201], v188 offset:4096
	ds_read_b128 v[202:205], v188 offset:5120
	ds_read_b128 v[206:209], v188 offset:6144
	ds_read_b128 v[210:213], v188 offset:7168
	global_load_lds_dwordx4 v[214:215], off
	v_lshl_add_u64 v[214:215], v[170:171], 0, s[6:7]
	s_add_i32 m0, s43, 0xe000
	s_nop 0
	global_load_lds_dwordx4 v[214:215], off
	s_waitcnt vmcnt(8)
	s_waitcnt lgkmcnt(0)
	s_barrier
	s_setprio 1
	s_waitcnt lgkmcnt(0)
	v_mfma_i32_16x16x64_i8 v[70:73], v[158:161], v[172:175], v[70:73]
	v_mfma_i32_16x16x64_i8 v[102:105], v[158:161], v[190:193], v[102:105]
	v_mfma_i32_16x16x64_i8 v[114:117], v[158:161], v[198:201], v[114:117]
	v_mfma_i32_16x16x64_i8 v[126:129], v[158:161], v[206:209], v[126:129]
	v_mfma_i32_16x16x64_i8 v[110:113], v[154:157], v[206:209], v[110:113]
	v_mfma_i32_16x16x64_i8 v[86:89], v[154:157], v[198:201], v[86:89]
	v_mfma_i32_16x16x64_i8 v[54:57], v[154:157], v[190:193], v[54:57]
	v_mfma_i32_16x16x64_i8 v[34:37], v[154:157], v[172:175], v[34:37]
	s_nop 0
	v_mfma_i32_16x16x64_i8 v[70:73], v[150:153], v[176:179], v[70:73]
	v_mfma_i32_16x16x64_i8 v[102:105], v[150:153], v[194:197], v[102:105]
	v_mfma_i32_16x16x64_i8 v[114:117], v[150:153], v[202:205], v[114:117]
	v_mfma_i32_16x16x64_i8 v[126:129], v[150:153], v[210:213], v[126:129]
	v_mfma_i32_16x16x64_i8 v[110:113], v[146:149], v[210:213], v[110:113]
	v_mfma_i32_16x16x64_i8 v[86:89], v[146:149], v[202:205], v[86:89]
	v_mfma_i32_16x16x64_i8 v[54:57], v[146:149], v[194:197], v[54:57]
	v_mfma_i32_16x16x64_i8 v[34:37], v[146:149], v[176:179], v[34:37]
	s_setprio 0
	s_setprio 1
	v_mfma_i32_16x16x64_i8 v[18:21], v[142:145], v[172:175], v[18:21]
	v_mfma_i32_16x16x64_i8 v[38:41], v[142:145], v[190:193], v[38:41]
	v_mfma_i32_16x16x64_i8 v[66:69], v[142:145], v[198:201], v[66:69]
	v_mfma_i32_16x16x64_i8 v[90:93], v[142:145], v[206:209], v[90:93]
	v_mfma_i32_16x16x64_i8 v[50:53], v[138:141], v[206:209], v[50:53]
	v_mfma_i32_16x16x64_i8 v[26:29], v[138:141], v[198:201], v[26:29]
	v_mfma_i32_16x16x64_i8 v[6:9], v[138:141], v[190:193], v[6:9]
	v_mfma_i32_16x16x64_i8 v[2:5], v[138:141], v[172:175], v[2:5]
	s_nop 0
	v_mfma_i32_16x16x64_i8 v[18:21], v[130:133], v[176:179], v[18:21]
	v_mfma_i32_16x16x64_i8 v[38:41], v[130:133], v[194:197], v[38:41]
	v_mfma_i32_16x16x64_i8 v[66:69], v[130:133], v[202:205], v[66:69]
	v_mfma_i32_16x16x64_i8 v[90:93], v[130:133], v[210:213], v[90:93]
	v_mfma_i32_16x16x64_i8 v[50:53], v[134:137], v[210:213], v[50:53]
	v_mfma_i32_16x16x64_i8 v[26:29], v[134:137], v[202:205], v[26:29]
	v_mfma_i32_16x16x64_i8 v[6:9], v[134:137], v[194:197], v[6:9]
	v_mfma_i32_16x16x64_i8 v[2:5], v[134:137], v[176:179], v[2:5]
	s_setprio 0
	s_barrier
	s_add_i32 s68, s69, s42
	s_mov_b32 m0, s68
	ds_read_b128 v[190:193], v188 offset:16384
	ds_read_b128 v[194:197], v188 offset:17408
	ds_read_b128 v[198:201], v188 offset:18432
	ds_read_b128 v[202:205], v188 offset:19456
	ds_read_b128 v[206:209], v188 offset:20480
	ds_read_b128 v[210:213], v188 offset:21504
	ds_read_b128 v[214:217], v188 offset:22528
	ds_read_b128 v[218:221], v188 offset:23552
	global_load_lds_dwordx4 v162, s[8:9]
	s_add_i32 m0, s68, 0x2000
	s_add_u32 s68, s8, 0x80000
	s_addc_u32 s69, s9, 0
	s_add_i32 s65, s65, s42
	global_load_lds_dwordx4 v166, s[8:9]
	s_mov_b32 m0, s65
	s_nop 0
	global_load_lds_dwordx4 v162, s[68:69]
	s_add_i32 m0, s65, 0x2000
	s_nop 0
	global_load_lds_dwordx4 v166, s[68:69]
	s_mov_b32 m0, s43
	s_nop 0
	global_load_lds_dwordx4 v162, s[40:41]
	s_mov_b32 m0, s60
	s_nop 0
	global_load_lds_dwordx4 v166, s[40:41]
	s_waitcnt vmcnt(8)
	s_waitcnt lgkmcnt(0)
	s_barrier
	s_setprio 1
	s_waitcnt lgkmcnt(0)
	v_mfma_i32_16x16x64_i8 v[122:125], v[158:161], v[190:193], v[122:125]
	v_mfma_i32_16x16x64_i8 v[98:101], v[158:161], v[198:201], v[98:101]
	v_mfma_i32_16x16x64_i8 v[62:65], v[158:161], v[206:209], v[62:65]
	v_mfma_i32_16x16x64_i8 v[30:33], v[158:161], v[214:217], v[30:33]
	v_mfma_i32_16x16x64_i8 v[22:25], v[154:157], v[214:217], v[22:25]
	v_mfma_i32_16x16x64_i8 v[58:61], v[154:157], v[206:209], v[58:61]
	v_mfma_i32_16x16x64_i8 v[94:97], v[154:157], v[198:201], v[94:97]
	v_mfma_i32_16x16x64_i8 v[118:121], v[154:157], v[190:193], v[118:121]
	s_nop 0
	v_mfma_i32_16x16x64_i8 v[122:125], v[150:153], v[194:197], v[122:125]
	v_mfma_i32_16x16x64_i8 v[98:101], v[150:153], v[202:205], v[98:101]
	v_mfma_i32_16x16x64_i8 v[62:65], v[150:153], v[210:213], v[62:65]
	v_mfma_i32_16x16x64_i8 v[30:33], v[150:153], v[218:221], v[30:33]
	v_mfma_i32_16x16x64_i8 v[22:25], v[146:149], v[218:221], v[22:25]
	v_mfma_i32_16x16x64_i8 v[58:61], v[146:149], v[210:213], v[58:61]
	v_mfma_i32_16x16x64_i8 v[94:97], v[146:149], v[202:205], v[94:97]
	v_mfma_i32_16x16x64_i8 v[118:121], v[146:149], v[194:197], v[118:121]
	s_setprio 0
	s_setprio 1
	v_mfma_i32_16x16x64_i8 v[106:109], v[142:145], v[190:193], v[106:109]
	v_mfma_i32_16x16x64_i8 v[78:81], v[142:145], v[198:201], v[78:81]
	v_mfma_i32_16x16x64_i8 v[46:49], v[142:145], v[206:209], v[46:49]
	v_mfma_i32_16x16x64_i8 v[14:17], v[142:145], v[214:217], v[14:17]
	v_mfma_i32_16x16x64_i8 v[10:13], v[138:141], v[214:217], v[10:13]
	v_mfma_i32_16x16x64_i8 v[42:45], v[138:141], v[206:209], v[42:45]
	v_mfma_i32_16x16x64_i8 v[74:77], v[138:141], v[198:201], v[74:77]
	v_mfma_i32_16x16x64_i8 v[82:85], v[138:141], v[190:193], v[82:85]
	s_nop 0
	v_mfma_i32_16x16x64_i8 v[106:109], v[130:133], v[194:197], v[106:109]
	v_mfma_i32_16x16x64_i8 v[78:81], v[130:133], v[202:205], v[78:81]
	v_mfma_i32_16x16x64_i8 v[46:49], v[130:133], v[210:213], v[46:49]
	v_mfma_i32_16x16x64_i8 v[14:17], v[130:133], v[218:221], v[14:17]
	v_mfma_i32_16x16x64_i8 v[10:13], v[134:137], v[218:221], v[10:13]
	v_mfma_i32_16x16x64_i8 v[42:45], v[134:137], v[210:213], v[42:45]
	v_mfma_i32_16x16x64_i8 v[74:77], v[134:137], v[202:205], v[74:77]
	v_mfma_i32_16x16x64_i8 v[82:85], v[134:137], v[194:197], v[82:85]
	s_setprio 0
	s_barrier
	s_add_i32 s65, 0, 0x18000
	s_add_i32 s68, 0, 0x1c000
	v_add_u32_e32 v142, s65, v187
	v_add_u32_e32 v158, s68, v187
	ds_read_b128 v[130:133], v142
	ds_read_b128 v[134:137], v142 offset:1024
	ds_read_b128 v[138:141], v142 offset:2048
	ds_read_b128 v[142:145], v142 offset:3072
	ds_read_b128 v[146:149], v158
	ds_read_b128 v[150:153], v158 offset:1024
	ds_read_b128 v[154:157], v158 offset:2048
	ds_read_b128 v[158:161], v158 offset:3072
	s_add_u32 s40, s40, 0x80000
	s_addc_u32 s41, s41, 0
	s_add_u32 s100, s40, 0xfff80080
	s_addc_u32 s101, s41, -1
	s_mov_b32 m0, s61
	ds_read_b128 v[190:193], v188 offset:32768
	ds_read_b128 v[194:197], v188 offset:33792
	ds_read_b128 v[198:201], v188 offset:34816
	ds_read_b128 v[202:205], v188 offset:35840
	ds_read_b128 v[206:209], v188 offset:36864
	ds_read_b128 v[210:213], v188 offset:37888
	ds_read_b128 v[214:217], v188 offset:38912
	ds_read_b128 v[218:221], v188 offset:39936
	global_load_lds_dwordx4 v162, s[40:41]
	s_mov_b32 m0, s62
	s_nop 0
	global_load_lds_dwordx4 v166, s[40:41]
	s_waitcnt vmcnt(8)
	s_waitcnt lgkmcnt(0)
	s_barrier
	s_setprio 1
	s_waitcnt lgkmcnt(0)
	v_mfma_i32_16x16x64_i8 v[70:73], v[130:133], v[190:193], v[70:73]
	v_mfma_i32_16x16x64_i8 v[102:105], v[130:133], v[198:201], v[102:105]
	v_mfma_i32_16x16x64_i8 v[114:117], v[130:133], v[206:209], v[114:117]
	v_mfma_i32_16x16x64_i8 v[126:129], v[130:133], v[214:217], v[126:129]
	v_mfma_i32_16x16x64_i8 v[110:113], v[138:141], v[214:217], v[110:113]
	v_mfma_i32_16x16x64_i8 v[86:89], v[138:141], v[206:209], v[86:89]
	v_mfma_i32_16x16x64_i8 v[54:57], v[138:141], v[198:201], v[54:57]
	v_mfma_i32_16x16x64_i8 v[34:37], v[138:141], v[190:193], v[34:37]
	s_nop 0
	v_mfma_i32_16x16x64_i8 v[70:73], v[134:137], v[194:197], v[70:73]
	v_mfma_i32_16x16x64_i8 v[102:105], v[134:137], v[202:205], v[102:105]
	v_mfma_i32_16x16x64_i8 v[114:117], v[134:137], v[210:213], v[114:117]
	v_mfma_i32_16x16x64_i8 v[126:129], v[134:137], v[218:221], v[126:129]
	v_mfma_i32_16x16x64_i8 v[110:113], v[142:145], v[218:221], v[110:113]
	v_mfma_i32_16x16x64_i8 v[86:89], v[142:145], v[210:213], v[86:89]
	v_mfma_i32_16x16x64_i8 v[54:57], v[142:145], v[202:205], v[54:57]
	v_mfma_i32_16x16x64_i8 v[34:37], v[142:145], v[194:197], v[34:37]
	s_setprio 0
	s_setprio 1
	v_mfma_i32_16x16x64_i8 v[18:21], v[146:149], v[190:193], v[18:21]
	v_mfma_i32_16x16x64_i8 v[38:41], v[146:149], v[198:201], v[38:41]
	v_mfma_i32_16x16x64_i8 v[66:69], v[146:149], v[206:209], v[66:69]
	v_mfma_i32_16x16x64_i8 v[90:93], v[146:149], v[214:217], v[90:93]
	v_mfma_i32_16x16x64_i8 v[50:53], v[154:157], v[214:217], v[50:53]
	v_mfma_i32_16x16x64_i8 v[26:29], v[154:157], v[206:209], v[26:29]
	v_mfma_i32_16x16x64_i8 v[6:9], v[154:157], v[198:201], v[6:9]
	v_mfma_i32_16x16x64_i8 v[2:5], v[154:157], v[190:193], v[2:5]
	s_nop 0
	v_mfma_i32_16x16x64_i8 v[18:21], v[150:153], v[194:197], v[18:21]
	v_mfma_i32_16x16x64_i8 v[38:41], v[150:153], v[202:205], v[38:41]
	v_mfma_i32_16x16x64_i8 v[66:69], v[150:153], v[210:213], v[66:69]
	v_mfma_i32_16x16x64_i8 v[90:93], v[150:153], v[218:221], v[90:93]
	v_mfma_i32_16x16x64_i8 v[50:53], v[158:161], v[218:221], v[50:53]
	v_mfma_i32_16x16x64_i8 v[26:29], v[158:161], v[210:213], v[26:29]
	v_mfma_i32_16x16x64_i8 v[6:9], v[158:161], v[202:205], v[6:9]
	v_mfma_i32_16x16x64_i8 v[2:5], v[158:161], v[194:197], v[2:5]
	s_setprio 0
	s_barrier
	s_add_i32 s40, s65, s42
	s_mov_b32 m0, s40
	s_add_u32 s98, s8, 0x80
	s_addc_u32 s99, s9, 0
	ds_read_b128 v[190:193], v188 offset:49152
	ds_read_b128 v[194:197], v188 offset:50176
	ds_read_b128 v[198:201], v188 offset:51200
	ds_read_b128 v[202:205], v188 offset:52224
	ds_read_b128 v[206:209], v188 offset:53248
	ds_read_b128 v[210:213], v188 offset:54272
	ds_read_b128 v[214:217], v188 offset:55296
	ds_read_b128 v[218:221], v188 offset:56320
	global_load_lds_dwordx4 v162, s[98:99]
	s_add_i32 m0, s40, 0x2000
	s_add_u32 s8, s8, 0x80080
	s_addc_u32 s9, s9, 0
	s_add_i32 s40, s68, s42
	global_load_lds_dwordx4 v166, s[98:99]
	s_mov_b32 m0, s40
	s_nop 0
	global_load_lds_dwordx4 v162, s[8:9]
	s_add_i32 m0, s40, 0x2000
	s_nop 0
	global_load_lds_dwordx4 v166, s[8:9]
	s_mov_b32 m0, s66
	s_nop 0
	global_load_lds_dwordx4 v162, s[100:101]
	s_mov_b32 m0, s67
	s_nop 0
	global_load_lds_dwordx4 v166, s[100:101]
	s_waitcnt vmcnt(8)
	s_waitcnt lgkmcnt(0)
	s_barrier
	s_setprio 1
	s_waitcnt lgkmcnt(0)
	v_mfma_i32_16x16x64_i8 v[122:125], v[130:133], v[190:193], v[122:125]
	v_mfma_i32_16x16x64_i8 v[98:101], v[130:133], v[198:201], v[98:101]
	v_mfma_i32_16x16x64_i8 v[62:65], v[130:133], v[206:209], v[62:65]
	v_mfma_i32_16x16x64_i8 v[30:33], v[130:133], v[214:217], v[30:33]
	v_mfma_i32_16x16x64_i8 v[22:25], v[138:141], v[214:217], v[22:25]
	v_mfma_i32_16x16x64_i8 v[58:61], v[138:141], v[206:209], v[58:61]
	v_mfma_i32_16x16x64_i8 v[94:97], v[138:141], v[198:201], v[94:97]
	v_mfma_i32_16x16x64_i8 v[118:121], v[138:141], v[190:193], v[118:121]
	s_nop 0
	v_mfma_i32_16x16x64_i8 v[122:125], v[134:137], v[194:197], v[122:125]
	v_mfma_i32_16x16x64_i8 v[98:101], v[134:137], v[202:205], v[98:101]
	v_mfma_i32_16x16x64_i8 v[62:65], v[134:137], v[210:213], v[62:65]
	v_mfma_i32_16x16x64_i8 v[30:33], v[134:137], v[218:221], v[30:33]
	v_mfma_i32_16x16x64_i8 v[22:25], v[142:145], v[218:221], v[22:25]
	v_mfma_i32_16x16x64_i8 v[58:61], v[142:145], v[210:213], v[58:61]
	v_mfma_i32_16x16x64_i8 v[94:97], v[142:145], v[202:205], v[94:97]
	v_mfma_i32_16x16x64_i8 v[118:121], v[142:145], v[194:197], v[118:121]
	s_setprio 0
	s_setprio 1
	v_mfma_i32_16x16x64_i8 v[106:109], v[146:149], v[190:193], v[106:109]
	v_mfma_i32_16x16x64_i8 v[78:81], v[146:149], v[198:201], v[78:81]
	v_mfma_i32_16x16x64_i8 v[46:49], v[146:149], v[206:209], v[46:49]
	v_mfma_i32_16x16x64_i8 v[14:17], v[146:149], v[214:217], v[14:17]
	v_mfma_i32_16x16x64_i8 v[10:13], v[154:157], v[214:217], v[10:13]
	v_mfma_i32_16x16x64_i8 v[42:45], v[154:157], v[206:209], v[42:45]
	v_mfma_i32_16x16x64_i8 v[74:77], v[154:157], v[198:201], v[74:77]
	v_mfma_i32_16x16x64_i8 v[82:85], v[154:157], v[190:193], v[82:85]
	s_nop 0
	v_mfma_i32_16x16x64_i8 v[106:109], v[150:153], v[194:197], v[106:109]
	v_mfma_i32_16x16x64_i8 v[78:81], v[150:153], v[202:205], v[78:81]
	v_mfma_i32_16x16x64_i8 v[46:49], v[150:153], v[210:213], v[46:49]
	v_mfma_i32_16x16x64_i8 v[14:17], v[150:153], v[218:221], v[14:17]
	v_mfma_i32_16x16x64_i8 v[10:13], v[158:161], v[218:221], v[10:13]
	v_mfma_i32_16x16x64_i8 v[42:45], v[158:161], v[210:213], v[42:45]
	v_mfma_i32_16x16x64_i8 v[74:77], v[158:161], v[202:205], v[74:77]
	v_mfma_i32_16x16x64_i8 v[82:85], v[158:161], v[194:197], v[82:85]
	s_setprio 0
	s_barrier
	s_add_i32 s64, s64, 2
	s_add_u32 s6, s6, 0x100
	s_addc_u32 s7, s7, 0
	s_cmp_gt_u32 s64, 29
	s_cbranch_scc0 .LBB0_1051
	s_waitcnt vmcnt(0)
	s_cmpk_lt_u32 s59, 0x100
	s_cbranch_scc0 .LBB0_1054
	s_barrier

.LBB0_1173:
	ds_read_b128 v[158:161], v184
	ds_read_b128 v[150:153], v184 offset:1024
	ds_read_b128 v[154:157], v184 offset:2048
	ds_read_b128 v[146:149], v184 offset:3072
	ds_read_b128 v[142:145], v185
	ds_read_b128 v[130:133], v185 offset:1024
	ds_read_b128 v[138:141], v185 offset:2048
	ds_read_b128 v[134:137], v185 offset:3072
	s_add_u32 s38, s36, 0xfff80080
	s_addc_u32 s39, s37, -1
	s_cmp_eq_u32 s65, 28
	s_cselect_b32 s41, s18, s39
	s_cselect_b32 s40, s19, s38
	s_cselect_b32 s39, s25, s64
	s_cselect_b32 s38, s27, s63
	v_lshl_add_u64 v[212:213], s[36:37], 0, v[166:167]
	s_add_i32 m0, s35, 0xc000
	ds_read_b128 v[174:177], v186
	ds_read_b128 v[178:181], v186 offset:1024
	ds_read_b128 v[188:191], v186 offset:2048
	ds_read_b128 v[192:195], v186 offset:3072
	ds_read_b128 v[196:199], v186 offset:4096
	ds_read_b128 v[200:203], v186 offset:5120
	ds_read_b128 v[204:207], v186 offset:6144
	ds_read_b128 v[208:211], v186 offset:7168
	global_load_lds_dwordx4 v[212:213], off
	v_lshl_add_u64 v[212:213], s[36:37], 0, v[168:169]
	s_add_i32 m0, s35, 0xe000
	s_nop 0
	global_load_lds_dwordx4 v[212:213], off
	s_waitcnt vmcnt(8)
	s_waitcnt lgkmcnt(0)
	s_barrier
	s_setprio 1
	s_waitcnt lgkmcnt(0)
	v_mfma_i32_16x16x64_i8 v[126:129], v[158:161], v[174:177], v[126:129]
	v_mfma_i32_16x16x64_i8 v[110:113], v[158:161], v[188:191], v[110:113]
	v_mfma_i32_16x16x64_i8 v[94:97], v[158:161], v[196:199], v[94:97]
	v_mfma_i32_16x16x64_i8 v[78:81], v[158:161], v[204:207], v[78:81]
	v_mfma_i32_16x16x64_i8 v[74:77], v[154:157], v[204:207], v[74:77]
	v_mfma_i32_16x16x64_i8 v[90:93], v[154:157], v[196:199], v[90:93]
	v_mfma_i32_16x16x64_i8 v[106:109], v[154:157], v[188:191], v[106:109]
	v_mfma_i32_16x16x64_i8 v[122:125], v[154:157], v[174:177], v[122:125]
	s_nop 0
	v_mfma_i32_16x16x64_i8 v[126:129], v[150:153], v[178:181], v[126:129]
	v_mfma_i32_16x16x64_i8 v[110:113], v[150:153], v[192:195], v[110:113]
	v_mfma_i32_16x16x64_i8 v[94:97], v[150:153], v[200:203], v[94:97]
	v_mfma_i32_16x16x64_i8 v[78:81], v[150:153], v[208:211], v[78:81]
	v_mfma_i32_16x16x64_i8 v[74:77], v[146:149], v[208:211], v[74:77]
	v_mfma_i32_16x16x64_i8 v[90:93], v[146:149], v[200:203], v[90:93]
	v_mfma_i32_16x16x64_i8 v[106:109], v[146:149], v[192:195], v[106:109]
	v_mfma_i32_16x16x64_i8 v[122:125], v[146:149], v[178:181], v[122:125]
	s_setprio 0
	s_setprio 1
	v_mfma_i32_16x16x64_i8 v[118:121], v[142:145], v[174:177], v[118:121]
	v_mfma_i32_16x16x64_i8 v[102:105], v[142:145], v[188:191], v[102:105]
	v_mfma_i32_16x16x64_i8 v[86:89], v[142:145], v[196:199], v[86:89]
	v_mfma_i32_16x16x64_i8 v[70:73], v[142:145], v[204:207], v[70:73]
	v_mfma_i32_16x16x64_i8 v[66:69], v[138:141], v[204:207], v[66:69]
	v_mfma_i32_16x16x64_i8 v[82:85], v[138:141], v[196:199], v[82:85]
	v_mfma_i32_16x16x64_i8 v[98:101], v[138:141], v[188:191], v[98:101]
	v_mfma_i32_16x16x64_i8 v[114:117], v[138:141], v[174:177], v[114:117]
	s_nop 0
	v_mfma_i32_16x16x64_i8 v[118:121], v[130:133], v[178:181], v[118:121]
	v_mfma_i32_16x16x64_i8 v[102:105], v[130:133], v[192:195], v[102:105]
	v_mfma_i32_16x16x64_i8 v[86:89], v[130:133], v[200:203], v[86:89]
	v_mfma_i32_16x16x64_i8 v[70:73], v[130:133], v[208:211], v[70:73]
	v_mfma_i32_16x16x64_i8 v[66:69], v[134:137], v[208:211], v[66:69]
	v_mfma_i32_16x16x64_i8 v[82:85], v[134:137], v[200:203], v[82:85]
	v_mfma_i32_16x16x64_i8 v[98:101], v[134:137], v[192:195], v[98:101]
	v_mfma_i32_16x16x64_i8 v[114:117], v[134:137], v[178:181], v[114:117]
	s_setprio 0
	s_barrier
	s_add_i32 s66, s51, s3
	v_lshl_add_u64 v[174:175], s[38:39], 0, v[164:165]
	s_mov_b32 m0, s66
	ds_read_b128 v[188:191], v186 offset:16384
	ds_read_b128 v[192:195], v186 offset:17408
	ds_read_b128 v[196:199], v186 offset:18432
	ds_read_b128 v[200:203], v186 offset:19456
	ds_read_b128 v[204:207], v186 offset:20480
	ds_read_b128 v[208:211], v186 offset:21504
	ds_read_b128 v[212:215], v186 offset:22528
	ds_read_b128 v[216:219], v186 offset:23552
	global_load_lds_dwordx4 v[174:175], off
	s_add_i32 m0, s66, 0x2000
	s_add_u32 s66, s38, 0x80000
	v_lshl_add_u64 v[176:177], s[38:39], 0, v[162:163]
	s_addc_u32 s67, s39, 0
	s_add_i32 s68, s58, s3
	global_load_lds_dwordx4 v[176:177], off
	v_lshl_add_u64 v[178:179], s[66:67], 0, v[164:165]
	s_mov_b32 m0, s68
	v_lshl_add_u64 v[180:181], s[40:41], 0, v[162:163]
	global_load_lds_dwordx4 v[178:179], off
	v_lshl_add_u64 v[178:179], s[66:67], 0, v[162:163]
	s_add_i32 m0, s68, 0x2000
	s_nop 0
	global_load_lds_dwordx4 v[178:179], off
	v_lshl_add_u64 v[178:179], s[40:41], 0, v[164:165]
	s_mov_b32 m0, s35
	s_nop 0
	global_load_lds_dwordx4 v[178:179], off
	s_mov_b32 m0, s42
	s_nop 0
	global_load_lds_dwordx4 v[180:181], off
	s_waitcnt vmcnt(8)
	s_waitcnt lgkmcnt(0)
	s_barrier
	s_setprio 1
	s_waitcnt lgkmcnt(0)
	v_mfma_i32_16x16x64_i8 v[62:65], v[158:161], v[188:191], v[62:65]
	v_mfma_i32_16x16x64_i8 v[46:49], v[158:161], v[196:199], v[46:49]
	v_mfma_i32_16x16x64_i8 v[30:33], v[158:161], v[204:207], v[30:33]
	v_mfma_i32_16x16x64_i8 v[14:17], v[158:161], v[212:215], v[14:17]
	v_mfma_i32_16x16x64_i8 v[10:13], v[154:157], v[212:215], v[10:13]
	v_mfma_i32_16x16x64_i8 v[26:29], v[154:157], v[204:207], v[26:29]
	v_mfma_i32_16x16x64_i8 v[42:45], v[154:157], v[196:199], v[42:45]
	v_mfma_i32_16x16x64_i8 v[58:61], v[154:157], v[188:191], v[58:61]
	s_nop 0
	v_mfma_i32_16x16x64_i8 v[62:65], v[150:153], v[192:195], v[62:65]
	v_mfma_i32_16x16x64_i8 v[46:49], v[150:153], v[200:203], v[46:49]
	v_mfma_i32_16x16x64_i8 v[30:33], v[150:153], v[208:211], v[30:33]
	v_mfma_i32_16x16x64_i8 v[14:17], v[150:153], v[216:219], v[14:17]
	v_mfma_i32_16x16x64_i8 v[10:13], v[146:149], v[216:219], v[10:13]
	v_mfma_i32_16x16x64_i8 v[26:29], v[146:149], v[208:211], v[26:29]
	v_mfma_i32_16x16x64_i8 v[42:45], v[146:149], v[200:203], v[42:45]
	v_mfma_i32_16x16x64_i8 v[58:61], v[146:149], v[192:195], v[58:61]
	s_setprio 0
	s_setprio 1
	v_mfma_i32_16x16x64_i8 v[54:57], v[142:145], v[188:191], v[54:57]
	v_mfma_i32_16x16x64_i8 v[38:41], v[142:145], v[196:199], v[38:41]
	v_mfma_i32_16x16x64_i8 v[22:25], v[142:145], v[204:207], v[22:25]
	v_mfma_i32_16x16x64_i8 v[6:9], v[142:145], v[212:215], v[6:9]
	v_mfma_i32_16x16x64_i8 v[2:5], v[138:141], v[212:215], v[2:5]
	v_mfma_i32_16x16x64_i8 v[18:21], v[138:141], v[204:207], v[18:21]
	v_mfma_i32_16x16x64_i8 v[34:37], v[138:141], v[196:199], v[34:37]
	v_mfma_i32_16x16x64_i8 v[50:53], v[138:141], v[188:191], v[50:53]
	s_nop 0
	v_mfma_i32_16x16x64_i8 v[54:57], v[130:133], v[192:195], v[54:57]
	v_mfma_i32_16x16x64_i8 v[38:41], v[130:133], v[200:203], v[38:41]
	v_mfma_i32_16x16x64_i8 v[22:25], v[130:133], v[208:211], v[22:25]
	v_mfma_i32_16x16x64_i8 v[6:9], v[130:133], v[216:219], v[6:9]
	v_mfma_i32_16x16x64_i8 v[2:5], v[134:137], v[216:219], v[2:5]
	v_mfma_i32_16x16x64_i8 v[18:21], v[134:137], v[208:211], v[18:21]
	v_mfma_i32_16x16x64_i8 v[34:37], v[134:137], v[200:203], v[34:37]
	v_mfma_i32_16x16x64_i8 v[50:53], v[134:137], v[192:195], v[50:53]
	s_setprio 0
	s_barrier
	s_add_i32 s66, 0, 0x18000
	s_add_i32 s67, 0, 0x1c000
	v_add_u32_e32 v142, s66, v182
	v_add_u32_e32 v158, s67, v182
	ds_read_b128 v[130:133], v142
	ds_read_b128 v[134:137], v142 offset:1024
	ds_read_b128 v[138:141], v142 offset:2048
	ds_read_b128 v[142:145], v142 offset:3072
	ds_read_b128 v[146:149], v158
	ds_read_b128 v[150:153], v158 offset:1024
	ds_read_b128 v[154:157], v158 offset:2048
	ds_read_b128 v[158:161], v158 offset:3072
	s_add_u32 s40, s40, 0x80000
	s_addc_u32 s41, s41, 0
	s_mov_b32 m0, s43
	v_lshl_add_u64 v[220:221], s[40:41], 0, v[164:165]
	ds_read_b128 v[188:191], v186 offset:32768
	ds_read_b128 v[192:195], v186 offset:33792
	ds_read_b128 v[196:199], v186 offset:34816
	ds_read_b128 v[200:203], v186 offset:35840
	ds_read_b128 v[204:207], v186 offset:36864
	ds_read_b128 v[208:211], v186 offset:37888
	ds_read_b128 v[212:215], v186 offset:38912
	ds_read_b128 v[216:219], v186 offset:39936
	global_load_lds_dwordx4 v[220:221], off
	v_lshl_add_u64 v[220:221], s[40:41], 0, v[162:163]
	s_mov_b32 m0, s44
	s_nop 0
	global_load_lds_dwordx4 v[220:221], off
	s_waitcnt vmcnt(8)
	s_waitcnt lgkmcnt(0)
	s_barrier
	s_setprio 1
	s_waitcnt lgkmcnt(0)
	v_mfma_i32_16x16x64_i8 v[126:129], v[130:133], v[188:191], v[126:129]
	v_mfma_i32_16x16x64_i8 v[110:113], v[130:133], v[196:199], v[110:113]
	v_mfma_i32_16x16x64_i8 v[94:97], v[130:133], v[204:207], v[94:97]
	v_mfma_i32_16x16x64_i8 v[78:81], v[130:133], v[212:215], v[78:81]
	v_mfma_i32_16x16x64_i8 v[74:77], v[138:141], v[212:215], v[74:77]
	v_mfma_i32_16x16x64_i8 v[90:93], v[138:141], v[204:207], v[90:93]
	v_mfma_i32_16x16x64_i8 v[106:109], v[138:141], v[196:199], v[106:109]
	v_mfma_i32_16x16x64_i8 v[122:125], v[138:141], v[188:191], v[122:125]
	s_nop 0
	v_mfma_i32_16x16x64_i8 v[126:129], v[134:137], v[192:195], v[126:129]
	v_mfma_i32_16x16x64_i8 v[110:113], v[134:137], v[200:203], v[110:113]
	v_mfma_i32_16x16x64_i8 v[94:97], v[134:137], v[208:211], v[94:97]
	v_mfma_i32_16x16x64_i8 v[78:81], v[134:137], v[216:219], v[78:81]
	v_mfma_i32_16x16x64_i8 v[74:77], v[142:145], v[216:219], v[74:77]
	v_mfma_i32_16x16x64_i8 v[90:93], v[142:145], v[208:211], v[90:93]
	v_mfma_i32_16x16x64_i8 v[106:109], v[142:145], v[200:203], v[106:109]
	v_mfma_i32_16x16x64_i8 v[122:125], v[142:145], v[192:195], v[122:125]
	s_setprio 0
	s_setprio 1
	v_mfma_i32_16x16x64_i8 v[118:121], v[146:149], v[188:191], v[118:121]
	v_mfma_i32_16x16x64_i8 v[102:105], v[146:149], v[196:199], v[102:105]
	v_mfma_i32_16x16x64_i8 v[86:89], v[146:149], v[204:207], v[86:89]
	v_mfma_i32_16x16x64_i8 v[70:73], v[146:149], v[212:215], v[70:73]
	v_mfma_i32_16x16x64_i8 v[66:69], v[154:157], v[212:215], v[66:69]
	v_mfma_i32_16x16x64_i8 v[82:85], v[154:157], v[204:207], v[82:85]
	v_mfma_i32_16x16x64_i8 v[98:101], v[154:157], v[196:199], v[98:101]
	v_mfma_i32_16x16x64_i8 v[114:117], v[154:157], v[188:191], v[114:117]
	s_nop 0
	v_mfma_i32_16x16x64_i8 v[118:121], v[150:153], v[192:195], v[118:121]
	v_mfma_i32_16x16x64_i8 v[102:105], v[150:153], v[200:203], v[102:105]
	v_mfma_i32_16x16x64_i8 v[86:89], v[150:153], v[208:211], v[86:89]
	v_mfma_i32_16x16x64_i8 v[70:73], v[150:153], v[216:219], v[70:73]
	v_mfma_i32_16x16x64_i8 v[66:69], v[158:161], v[216:219], v[66:69]
	v_mfma_i32_16x16x64_i8 v[82:85], v[158:161], v[208:211], v[82:85]
	v_mfma_i32_16x16x64_i8 v[98:101], v[158:161], v[200:203], v[98:101]
	v_mfma_i32_16x16x64_i8 v[114:117], v[158:161], v[192:195], v[114:117]
	s_setprio 0
	s_barrier
	s_add_i32 s40, s66, s3
	v_lshl_add_u64 v[174:175], v[174:175], 0, s[8:9]
	s_mov_b32 m0, s40
	ds_read_b128 v[188:191], v186 offset:49152
	ds_read_b128 v[192:195], v186 offset:50176
	ds_read_b128 v[196:199], v186 offset:51200
	ds_read_b128 v[200:203], v186 offset:52224
	ds_read_b128 v[204:207], v186 offset:53248
	ds_read_b128 v[208:211], v186 offset:54272
	ds_read_b128 v[212:215], v186 offset:55296
	ds_read_b128 v[216:219], v186 offset:56320
	global_load_lds_dwordx4 v[174:175], off
	s_add_i32 m0, s40, 0x2000
	s_add_u32 s38, s38, 0x80080
	v_lshl_add_u64 v[174:175], v[176:177], 0, s[8:9]
	s_addc_u32 s39, s39, 0
	s_add_i32 s40, s67, s3
	global_load_lds_dwordx4 v[174:175], off
	v_lshl_add_u64 v[174:175], s[38:39], 0, v[164:165]
	s_mov_b32 m0, s40
	s_nop 0
	global_load_lds_dwordx4 v[174:175], off
	v_lshl_add_u64 v[174:175], s[38:39], 0, v[162:163]
	s_add_i32 m0, s40, 0x2000
	s_nop 0
	global_load_lds_dwordx4 v[174:175], off
	v_lshl_add_u64 v[174:175], v[178:179], 0, s[8:9]
	s_mov_b32 m0, s49
	s_nop 0
	global_load_lds_dwordx4 v[174:175], off
	v_lshl_add_u64 v[174:175], v[180:181], 0, s[8:9]
	s_mov_b32 m0, s50
	s_nop 0
	global_load_lds_dwordx4 v[174:175], off
	s_waitcnt vmcnt(8)
	s_waitcnt lgkmcnt(0)
	s_barrier
	s_setprio 1
	s_waitcnt lgkmcnt(0)
	v_mfma_i32_16x16x64_i8 v[62:65], v[130:133], v[188:191], v[62:65]
	v_mfma_i32_16x16x64_i8 v[46:49], v[130:133], v[196:199], v[46:49]
	v_mfma_i32_16x16x64_i8 v[30:33], v[130:133], v[204:207], v[30:33]
	v_mfma_i32_16x16x64_i8 v[14:17], v[130:133], v[212:215], v[14:17]
	v_mfma_i32_16x16x64_i8 v[10:13], v[138:141], v[212:215], v[10:13]
	v_mfma_i32_16x16x64_i8 v[26:29], v[138:141], v[204:207], v[26:29]
	v_mfma_i32_16x16x64_i8 v[42:45], v[138:141], v[196:199], v[42:45]
	v_mfma_i32_16x16x64_i8 v[58:61], v[138:141], v[188:191], v[58:61]
	s_nop 0
	v_mfma_i32_16x16x64_i8 v[62:65], v[134:137], v[192:195], v[62:65]
	v_mfma_i32_16x16x64_i8 v[46:49], v[134:137], v[200:203], v[46:49]
	v_mfma_i32_16x16x64_i8 v[30:33], v[134:137], v[208:211], v[30:33]
	v_mfma_i32_16x16x64_i8 v[14:17], v[134:137], v[216:219], v[14:17]
	v_mfma_i32_16x16x64_i8 v[10:13], v[142:145], v[216:219], v[10:13]
	v_mfma_i32_16x16x64_i8 v[26:29], v[142:145], v[208:211], v[26:29]
	v_mfma_i32_16x16x64_i8 v[42:45], v[142:145], v[200:203], v[42:45]
	v_mfma_i32_16x16x64_i8 v[58:61], v[142:145], v[192:195], v[58:61]
	s_setprio 0
	s_setprio 1
	v_mfma_i32_16x16x64_i8 v[54:57], v[146:149], v[188:191], v[54:57]
	v_mfma_i32_16x16x64_i8 v[38:41], v[146:149], v[196:199], v[38:41]
	v_mfma_i32_16x16x64_i8 v[22:25], v[146:149], v[204:207], v[22:25]
	v_mfma_i32_16x16x64_i8 v[6:9], v[146:149], v[212:215], v[6:9]
	v_mfma_i32_16x16x64_i8 v[2:5], v[154:157], v[212:215], v[2:5]
	v_mfma_i32_16x16x64_i8 v[18:21], v[154:157], v[204:207], v[18:21]
	v_mfma_i32_16x16x64_i8 v[34:37], v[154:157], v[196:199], v[34:37]
	v_mfma_i32_16x16x64_i8 v[50:53], v[154:157], v[188:191], v[50:53]
	s_nop 0
	v_mfma_i32_16x16x64_i8 v[54:57], v[150:153], v[192:195], v[54:57]
	v_mfma_i32_16x16x64_i8 v[38:41], v[150:153], v[200:203], v[38:41]
	v_mfma_i32_16x16x64_i8 v[22:25], v[150:153], v[208:211], v[22:25]
	v_mfma_i32_16x16x64_i8 v[6:9], v[150:153], v[216:219], v[6:9]
	v_mfma_i32_16x16x64_i8 v[2:5], v[158:161], v[216:219], v[2:5]
	v_mfma_i32_16x16x64_i8 v[18:21], v[158:161], v[208:211], v[18:21]
	v_mfma_i32_16x16x64_i8 v[34:37], v[158:161], v[200:203], v[34:37]
	v_mfma_i32_16x16x64_i8 v[50:53], v[158:161], v[192:195], v[50:53]
	s_setprio 0
	s_barrier
	s_add_i32 s65, s65, 2
	s_add_u32 s36, s36, 0x100
	s_addc_u32 s37, s37, 0
	s_add_u32 s63, s63, 0x100
	s_addc_u32 s64, s64, 0
	s_cmp_gt_u32 s65, 29
	s_cbranch_scc0 .LBB0_1173
	s_and_b64 vcc, exec, s[12:13]
	s_cbranch_vccz .LBB0_1176
	s_barrier

.LBB0_1291:
	ds_read_b128 v[26:29], v184
	ds_read_b128 v[30:33], v184 offset:1024
	ds_read_b128 v[18:21], v184 offset:2048
	ds_read_b128 v[22:25], v184 offset:3072
	ds_read_b128 v[10:13], v185
	ds_read_b128 v[14:17], v185 offset:1024
	ds_read_b128 v[2:5], v185 offset:2048
	ds_read_b128 v[6:9], v185 offset:3072
	s_add_u32 s20, s14, s16
	s_addc_u32 s21, s15, s17
	s_add_u32 s20, s20, 0x2a800100
	s_addc_u32 s21, s21, 0
	s_add_u32 s48, s31, s16
	s_addc_u32 s49, s34, s17
	s_cmpk_eq_i32 s16, 0x700
	s_cselect_b32 s23, s9, s21
	s_cselect_b32 s22, s8, s20
	s_cselect_b32 s21, s5, s49
	s_cselect_b32 s20, s4, s48
	s_mov_b32 m0, s36
	v_lshl_add_u64 v[214:215], v[170:171], 0, s[16:17]
	ds_read_b128 v[174:177], v186
	ds_read_b128 v[178:181], v186 offset:1024
	ds_read_b128 v[190:193], v186 offset:2048
	ds_read_b128 v[194:197], v186 offset:3072
	ds_read_b128 v[198:201], v186 offset:4096
	ds_read_b128 v[202:205], v186 offset:5120
	ds_read_b128 v[206:209], v186 offset:6144
	ds_read_b128 v[210:213], v186 offset:7168
	global_load_lds_dwordx4 v[214:215], off
	v_lshl_add_u64 v[214:215], v[172:173], 0, s[16:17]
	s_mov_b32 m0, s37
	s_nop 0
	global_load_lds_dwordx4 v[214:215], off
	s_waitcnt vmcnt(8)
	s_waitcnt lgkmcnt(0)
	s_barrier
	s_setprio 1
	s_waitcnt lgkmcnt(0)
	v_mfma_scale_f32_16x16x128_f8f6f4 v[158:161], v[26:33], v[174:181], v[158:161], v1, v1 op_sel_hi:[0,0,0]
	v_mfma_scale_f32_16x16x128_f8f6f4 v[146:149], v[26:33], v[190:197], v[146:149], v1, v1 op_sel_hi:[0,0,0]
	v_mfma_scale_f32_16x16x128_f8f6f4 v[130:133], v[26:33], v[198:205], v[130:133], v1, v1 op_sel_hi:[0,0,0]
	v_mfma_scale_f32_16x16x128_f8f6f4 v[114:117], v[26:33], v[206:213], v[114:117], v1, v1 op_sel_hi:[0,0,0]
	v_mfma_scale_f32_16x16x128_f8f6f4 v[106:109], v[18:25], v[206:213], v[106:109], v1, v1 op_sel_hi:[0,0,0]
	v_mfma_scale_f32_16x16x128_f8f6f4 v[122:125], v[18:25], v[198:205], v[122:125], v1, v1 op_sel_hi:[0,0,0]
	v_mfma_scale_f32_16x16x128_f8f6f4 v[138:141], v[18:25], v[190:197], v[138:141], v1, v1 op_sel_hi:[0,0,0]
	v_mfma_scale_f32_16x16x128_f8f6f4 v[154:157], v[18:25], v[174:181], v[154:157], v1, v1 op_sel_hi:[0,0,0]
	s_setprio 0
	s_setprio 1
	v_mfma_scale_f32_16x16x128_f8f6f4 v[150:153], v[10:17], v[174:181], v[150:153], v1, v1 op_sel_hi:[0,0,0]
	v_mfma_scale_f32_16x16x128_f8f6f4 v[134:137], v[10:17], v[190:197], v[134:137], v1, v1 op_sel_hi:[0,0,0]
	v_mfma_scale_f32_16x16x128_f8f6f4 v[118:121], v[10:17], v[198:205], v[118:121], v1, v1 op_sel_hi:[0,0,0]
	v_mfma_scale_f32_16x16x128_f8f6f4 v[102:105], v[10:17], v[206:213], v[102:105], v1, v1 op_sel_hi:[0,0,0]
	v_mfma_scale_f32_16x16x128_f8f6f4 v[98:101], v[2:9], v[206:213], v[98:101], v1, v1 op_sel_hi:[0,0,0]
	v_mfma_scale_f32_16x16x128_f8f6f4 v[110:113], v[2:9], v[198:205], v[110:113], v1, v1 op_sel_hi:[0,0,0]
	v_mfma_scale_f32_16x16x128_f8f6f4 v[126:129], v[2:9], v[190:197], v[126:129], v1, v1 op_sel_hi:[0,0,0]
	v_mfma_scale_f32_16x16x128_f8f6f4 v[142:145], v[2:9], v[174:181], v[142:145], v1, v1 op_sel_hi:[0,0,0]
	s_setprio 0
	s_barrier
	s_mov_b32 m0, s38
	v_lshl_add_u64 v[174:175], s[20:21], 0, v[164:165]
	s_add_u32 s48, s20, 0x80000
	ds_read_b128 v[190:193], v186 offset:16384
	ds_read_b128 v[194:197], v186 offset:17408
	ds_read_b128 v[198:201], v186 offset:18432
	ds_read_b128 v[202:205], v186 offset:19456
	ds_read_b128 v[206:209], v186 offset:20480
	ds_read_b128 v[210:213], v186 offset:21504
	ds_read_b128 v[214:217], v186 offset:22528
	ds_read_b128 v[218:221], v186 offset:23552
	global_load_lds_dwordx4 v[174:175], off
	v_lshl_add_u64 v[176:177], s[20:21], 0, v[168:169]
	s_mov_b32 m0, s39
	s_addc_u32 s49, s21, 0
	global_load_lds_dwordx4 v[176:177], off
	v_lshl_add_u64 v[178:179], s[48:49], 0, v[164:165]
	s_mov_b32 m0, s40
	v_lshl_add_u64 v[180:181], s[22:23], 0, v[166:167]
	global_load_lds_dwordx4 v[178:179], off
	v_lshl_add_u64 v[178:179], s[48:49], 0, v[168:169]
	s_mov_b32 m0, s41
	s_nop 0
	global_load_lds_dwordx4 v[178:179], off
	v_lshl_add_u64 v[178:179], s[22:23], 0, v[162:163]
	s_mov_b32 m0, s24
	s_nop 0
	global_load_lds_dwordx4 v[178:179], off
	s_mov_b32 m0, s25
	s_nop 0
	global_load_lds_dwordx4 v[180:181], off
	s_waitcnt vmcnt(8)
	s_waitcnt lgkmcnt(0)
	s_barrier
	s_setprio 1
	s_waitcnt lgkmcnt(0)
	v_mfma_scale_f32_16x16x128_f8f6f4 v[94:97], v[26:33], v[190:197], v[94:97], v1, v1 op_sel_hi:[0,0,0]
	v_mfma_scale_f32_16x16x128_f8f6f4 v[82:85], v[26:33], v[198:205], v[82:85], v1, v1 op_sel_hi:[0,0,0]
	v_mfma_scale_f32_16x16x128_f8f6f4 v[66:69], v[26:33], v[206:213], v[66:69], v1, v1 op_sel_hi:[0,0,0]
	v_mfma_scale_f32_16x16x128_f8f6f4 v[50:53], v[26:33], v[214:221], v[50:53], v1, v1 op_sel_hi:[0,0,0]
	v_mfma_scale_f32_16x16x128_f8f6f4 v[42:45], v[18:25], v[214:221], v[42:45], v1, v1 op_sel_hi:[0,0,0]
	v_mfma_scale_f32_16x16x128_f8f6f4 v[58:61], v[18:25], v[206:213], v[58:61], v1, v1 op_sel_hi:[0,0,0]
	v_mfma_scale_f32_16x16x128_f8f6f4 v[74:77], v[18:25], v[198:205], v[74:77], v1, v1 op_sel_hi:[0,0,0]
	v_mfma_scale_f32_16x16x128_f8f6f4 v[90:93], v[18:25], v[190:197], v[90:93], v1, v1 op_sel_hi:[0,0,0]
	s_setprio 0
	s_setprio 1
	v_mfma_scale_f32_16x16x128_f8f6f4 v[86:89], v[10:17], v[190:197], v[86:89], v1, v1 op_sel_hi:[0,0,0]
	v_mfma_scale_f32_16x16x128_f8f6f4 v[70:73], v[10:17], v[198:205], v[70:73], v1, v1 op_sel_hi:[0,0,0]
	v_mfma_scale_f32_16x16x128_f8f6f4 v[54:57], v[10:17], v[206:213], v[54:57], v1, v1 op_sel_hi:[0,0,0]
	v_mfma_scale_f32_16x16x128_f8f6f4 v[38:41], v[10:17], v[214:221], v[38:41], v1, v1 op_sel_hi:[0,0,0]
	v_mfma_scale_f32_16x16x128_f8f6f4 v[34:37], v[2:9], v[214:221], v[34:37], v1, v1 op_sel_hi:[0,0,0]
	v_mfma_scale_f32_16x16x128_f8f6f4 v[46:49], v[2:9], v[206:213], v[46:49], v1, v1 op_sel_hi:[0,0,0]
	v_mfma_scale_f32_16x16x128_f8f6f4 v[62:65], v[2:9], v[198:205], v[62:65], v1, v1 op_sel_hi:[0,0,0]
	v_mfma_scale_f32_16x16x128_f8f6f4 v[78:81], v[2:9], v[190:197], v[78:81], v1, v1 op_sel_hi:[0,0,0]
	s_setprio 0
	s_barrier
	ds_read_b128 v[2:5], v187
	ds_read_b128 v[6:9], v187 offset:1024
	ds_read_b128 v[10:13], v187 offset:2048
	ds_read_b128 v[14:17], v187 offset:3072
	ds_read_b128 v[18:21], v188
	ds_read_b128 v[22:25], v188 offset:1024
	ds_read_b128 v[26:29], v188 offset:2048
	ds_read_b128 v[30:33], v188 offset:3072
	s_add_u32 s22, s22, 0x80000
	s_addc_u32 s23, s23, 0
	s_mov_b32 m0, s26
	v_lshl_add_u64 v[222:223], s[22:23], 0, v[162:163]
	ds_read_b128 v[190:193], v186 offset:32768
	ds_read_b128 v[194:197], v186 offset:33792
	ds_read_b128 v[198:201], v186 offset:34816
	ds_read_b128 v[202:205], v186 offset:35840
	ds_read_b128 v[206:209], v186 offset:36864
	ds_read_b128 v[210:213], v186 offset:37888
	ds_read_b128 v[214:217], v186 offset:38912
	ds_read_b128 v[218:221], v186 offset:39936
	global_load_lds_dwordx4 v[222:223], off
	v_lshl_add_u64 v[222:223], s[22:23], 0, v[166:167]
	s_mov_b32 m0, s27
	s_nop 0
	global_load_lds_dwordx4 v[222:223], off
	s_waitcnt vmcnt(8)
	s_waitcnt lgkmcnt(0)
	s_barrier
	s_setprio 1
	s_waitcnt lgkmcnt(0)
	v_mfma_scale_f32_16x16x128_f8f6f4 v[158:161], v[2:9], v[190:197], v[158:161], v1, v1 op_sel_hi:[0,0,0]
	v_mfma_scale_f32_16x16x128_f8f6f4 v[146:149], v[2:9], v[198:205], v[146:149], v1, v1 op_sel_hi:[0,0,0]
	v_mfma_scale_f32_16x16x128_f8f6f4 v[130:133], v[2:9], v[206:213], v[130:133], v1, v1 op_sel_hi:[0,0,0]
	v_mfma_scale_f32_16x16x128_f8f6f4 v[114:117], v[2:9], v[214:221], v[114:117], v1, v1 op_sel_hi:[0,0,0]
	v_mfma_scale_f32_16x16x128_f8f6f4 v[106:109], v[10:17], v[214:221], v[106:109], v1, v1 op_sel_hi:[0,0,0]
	v_mfma_scale_f32_16x16x128_f8f6f4 v[122:125], v[10:17], v[206:213], v[122:125], v1, v1 op_sel_hi:[0,0,0]
	v_mfma_scale_f32_16x16x128_f8f6f4 v[138:141], v[10:17], v[198:205], v[138:141], v1, v1 op_sel_hi:[0,0,0]
	v_mfma_scale_f32_16x16x128_f8f6f4 v[154:157], v[10:17], v[190:197], v[154:157], v1, v1 op_sel_hi:[0,0,0]
	s_setprio 0
	s_setprio 1
	v_mfma_scale_f32_16x16x128_f8f6f4 v[150:153], v[18:25], v[190:197], v[150:153], v1, v1 op_sel_hi:[0,0,0]
	v_mfma_scale_f32_16x16x128_f8f6f4 v[134:137], v[18:25], v[198:205], v[134:137], v1, v1 op_sel_hi:[0,0,0]
	v_mfma_scale_f32_16x16x128_f8f6f4 v[118:121], v[18:25], v[206:213], v[118:121], v1, v1 op_sel_hi:[0,0,0]
	v_mfma_scale_f32_16x16x128_f8f6f4 v[102:105], v[18:25], v[214:221], v[102:105], v1, v1 op_sel_hi:[0,0,0]
	v_mfma_scale_f32_16x16x128_f8f6f4 v[98:101], v[26:33], v[214:221], v[98:101], v1, v1 op_sel_hi:[0,0,0]
	v_mfma_scale_f32_16x16x128_f8f6f4 v[110:113], v[26:33], v[206:213], v[110:113], v1, v1 op_sel_hi:[0,0,0]
	v_mfma_scale_f32_16x16x128_f8f6f4 v[126:129], v[26:33], v[198:205], v[126:129], v1, v1 op_sel_hi:[0,0,0]
	v_mfma_scale_f32_16x16x128_f8f6f4 v[142:145], v[26:33], v[190:197], v[142:145], v1, v1 op_sel_hi:[0,0,0]
	s_setprio 0
	s_barrier
	s_mov_b32 m0, s42
	v_lshl_add_u64 v[174:175], v[174:175], 0, s[12:13]
	s_add_u32 s20, s20, 0x80080
	ds_read_b128 v[190:193], v186 offset:49152
	ds_read_b128 v[194:197], v186 offset:50176
	ds_read_b128 v[198:201], v186 offset:51200
	ds_read_b128 v[202:205], v186 offset:52224
	ds_read_b128 v[206:209], v186 offset:53248
	ds_read_b128 v[210:213], v186 offset:54272
	ds_read_b128 v[214:217], v186 offset:55296
	ds_read_b128 v[218:221], v186 offset:56320
	global_load_lds_dwordx4 v[174:175], off
	v_lshl_add_u64 v[174:175], v[176:177], 0, s[12:13]
	s_mov_b32 m0, s43
	s_addc_u32 s21, s21, 0
	global_load_lds_dwordx4 v[174:175], off
	v_lshl_add_u64 v[174:175], s[20:21], 0, v[164:165]
	s_mov_b32 m0, s44
	s_nop 0
	global_load_lds_dwordx4 v[174:175], off
	v_lshl_add_u64 v[174:175], s[20:21], 0, v[168:169]
	s_mov_b32 m0, s45
	s_nop 0
	global_load_lds_dwordx4 v[174:175], off
	v_lshl_add_u64 v[174:175], v[178:179], 0, s[12:13]
	s_mov_b32 m0, s29
	s_nop 0
	global_load_lds_dwordx4 v[174:175], off
	v_lshl_add_u64 v[174:175], v[180:181], 0, s[12:13]
	s_mov_b32 m0, s30
	s_nop 0
	global_load_lds_dwordx4 v[174:175], off
	s_waitcnt vmcnt(8)
	s_waitcnt lgkmcnt(0)
	s_barrier
	s_setprio 1
	s_waitcnt lgkmcnt(0)
	v_mfma_scale_f32_16x16x128_f8f6f4 v[94:97], v[2:9], v[190:197], v[94:97], v1, v1 op_sel_hi:[0,0,0]
	v_mfma_scale_f32_16x16x128_f8f6f4 v[82:85], v[2:9], v[198:205], v[82:85], v1, v1 op_sel_hi:[0,0,0]
	v_mfma_scale_f32_16x16x128_f8f6f4 v[66:69], v[2:9], v[206:213], v[66:69], v1, v1 op_sel_hi:[0,0,0]
	v_mfma_scale_f32_16x16x128_f8f6f4 v[50:53], v[2:9], v[214:221], v[50:53], v1, v1 op_sel_hi:[0,0,0]
	v_mfma_scale_f32_16x16x128_f8f6f4 v[42:45], v[10:17], v[214:221], v[42:45], v1, v1 op_sel_hi:[0,0,0]
	v_mfma_scale_f32_16x16x128_f8f6f4 v[58:61], v[10:17], v[206:213], v[58:61], v1, v1 op_sel_hi:[0,0,0]
	v_mfma_scale_f32_16x16x128_f8f6f4 v[74:77], v[10:17], v[198:205], v[74:77], v1, v1 op_sel_hi:[0,0,0]
	v_mfma_scale_f32_16x16x128_f8f6f4 v[90:93], v[10:17], v[190:197], v[90:93], v1, v1 op_sel_hi:[0,0,0]
	s_setprio 0
	s_setprio 1
	v_mfma_scale_f32_16x16x128_f8f6f4 v[86:89], v[18:25], v[190:197], v[86:89], v1, v1 op_sel_hi:[0,0,0]
	v_mfma_scale_f32_16x16x128_f8f6f4 v[70:73], v[18:25], v[198:205], v[70:73], v1, v1 op_sel_hi:[0,0,0]
	v_mfma_scale_f32_16x16x128_f8f6f4 v[54:57], v[18:25], v[206:213], v[54:57], v1, v1 op_sel_hi:[0,0,0]
	v_mfma_scale_f32_16x16x128_f8f6f4 v[38:41], v[18:25], v[214:221], v[38:41], v1, v1 op_sel_hi:[0,0,0]
	v_mfma_scale_f32_16x16x128_f8f6f4 v[34:37], v[26:33], v[214:221], v[34:37], v1, v1 op_sel_hi:[0,0,0]
	v_mfma_scale_f32_16x16x128_f8f6f4 v[46:49], v[26:33], v[206:213], v[46:49], v1, v1 op_sel_hi:[0,0,0]
	v_mfma_scale_f32_16x16x128_f8f6f4 v[62:65], v[26:33], v[198:205], v[62:65], v1, v1 op_sel_hi:[0,0,0]
	v_mfma_scale_f32_16x16x128_f8f6f4 v[78:81], v[26:33], v[190:197], v[78:81], v1, v1 op_sel_hi:[0,0,0]
	s_setprio 0
	s_barrier
	s_add_i32 s35, s35, 2
	s_add_u32 s16, s16, 0x100
	s_addc_u32 s17, s17, 0
	s_cmp_gt_u32 s35, 13
	s_cbranch_scc0 .LBB0_1291
	s_cmpk_lt_u32 s19, 0x100
	s_cbranch_scc0 .LBB0_1294
	s_barrier

.LBB0_1309:
	ds_read_b128 v[26:29], v189
	ds_read_b128 v[30:33], v189 offset:1024
	ds_read_b128 v[18:21], v189 offset:2048
	ds_read_b128 v[22:25], v189 offset:3072
	ds_read_b128 v[10:13], v190
	ds_read_b128 v[14:17], v190 offset:1024
	ds_read_b128 v[2:5], v190 offset:2048
	ds_read_b128 v[6:9], v190 offset:3072
	s_add_u32 s40, s38, 0xfff80080
	s_addc_u32 s41, s39, -1
	s_cmp_eq_u32 s72, 28
	s_cselect_b32 s43, s18, s41
	s_cselect_b32 s42, s19, s40
	s_cselect_b32 s41, s27, s71
	s_cselect_b32 s40, s29, s70
	v_lshl_add_u64 v[216:217], s[38:39], 0, v[170:171]
	s_add_i32 m0, s37, 0xc000
	ds_read_b128 v[178:181], v191
	ds_read_b128 v[182:185], v191 offset:1024
	ds_read_b128 v[192:195], v191 offset:2048
	ds_read_b128 v[196:199], v191 offset:3072
	ds_read_b128 v[200:203], v191 offset:4096
	ds_read_b128 v[204:207], v191 offset:5120
	ds_read_b128 v[208:211], v191 offset:6144
	ds_read_b128 v[212:215], v191 offset:7168
	global_load_lds_dwordx4 v[216:217], off
	v_lshl_add_u64 v[216:217], s[38:39], 0, v[172:173]
	s_add_i32 m0, s37, 0xe000
	s_nop 0
	global_load_lds_dwordx4 v[216:217], off
	s_waitcnt vmcnt(8)
	s_waitcnt lgkmcnt(0)
	s_barrier
	s_setprio 1
	s_waitcnt lgkmcnt(0)
	v_mfma_scale_f32_16x16x128_f8f6f4 v[158:161], v[26:33], v[178:185], v[158:161], v1, v1 op_sel_hi:[0,0,0]
	v_mfma_scale_f32_16x16x128_f8f6f4 v[146:149], v[26:33], v[192:199], v[146:149], v1, v1 op_sel_hi:[0,0,0]
	v_mfma_scale_f32_16x16x128_f8f6f4 v[130:133], v[26:33], v[200:207], v[130:133], v1, v1 op_sel_hi:[0,0,0]
	v_mfma_scale_f32_16x16x128_f8f6f4 v[114:117], v[26:33], v[208:215], v[114:117], v1, v1 op_sel_hi:[0,0,0]
	v_mfma_scale_f32_16x16x128_f8f6f4 v[106:109], v[18:25], v[208:215], v[106:109], v1, v1 op_sel_hi:[0,0,0]
	v_mfma_scale_f32_16x16x128_f8f6f4 v[122:125], v[18:25], v[200:207], v[122:125], v1, v1 op_sel_hi:[0,0,0]
	v_mfma_scale_f32_16x16x128_f8f6f4 v[138:141], v[18:25], v[192:199], v[138:141], v1, v1 op_sel_hi:[0,0,0]
	v_mfma_scale_f32_16x16x128_f8f6f4 v[154:157], v[18:25], v[178:185], v[154:157], v1, v1 op_sel_hi:[0,0,0]
	s_setprio 0
	s_setprio 1
	v_mfma_scale_f32_16x16x128_f8f6f4 v[150:153], v[10:17], v[178:185], v[150:153], v1, v1 op_sel_hi:[0,0,0]
	v_mfma_scale_f32_16x16x128_f8f6f4 v[134:137], v[10:17], v[192:199], v[134:137], v1, v1 op_sel_hi:[0,0,0]
	v_mfma_scale_f32_16x16x128_f8f6f4 v[118:121], v[10:17], v[200:207], v[118:121], v1, v1 op_sel_hi:[0,0,0]
	v_mfma_scale_f32_16x16x128_f8f6f4 v[102:105], v[10:17], v[208:215], v[102:105], v1, v1 op_sel_hi:[0,0,0]
	v_mfma_scale_f32_16x16x128_f8f6f4 v[98:101], v[2:9], v[208:215], v[98:101], v1, v1 op_sel_hi:[0,0,0]
	v_mfma_scale_f32_16x16x128_f8f6f4 v[110:113], v[2:9], v[200:207], v[110:113], v1, v1 op_sel_hi:[0,0,0]
	v_mfma_scale_f32_16x16x128_f8f6f4 v[126:129], v[2:9], v[192:199], v[126:129], v1, v1 op_sel_hi:[0,0,0]
	v_mfma_scale_f32_16x16x128_f8f6f4 v[142:145], v[2:9], v[178:185], v[142:145], v1, v1 op_sel_hi:[0,0,0]
	s_setprio 0
	s_barrier
	s_add_i32 s64, s59, s3
	v_lshl_add_u64 v[178:179], s[40:41], 0, v[166:167]
	s_mov_b32 m0, s64
	ds_read_b128 v[192:195], v191 offset:16384
	ds_read_b128 v[196:199], v191 offset:17408
	ds_read_b128 v[200:203], v191 offset:18432
	ds_read_b128 v[204:207], v191 offset:19456
	ds_read_b128 v[208:211], v191 offset:20480
	ds_read_b128 v[212:215], v191 offset:21504
	ds_read_b128 v[216:219], v191 offset:22528
	ds_read_b128 v[220:223], v191 offset:23552
	global_load_lds_dwordx4 v[178:179], off
	s_add_i32 m0, s64, 0x2000
	s_add_u32 s64, s40, 0x80000
	v_lshl_add_u64 v[180:181], s[40:41], 0, v[162:163]
	s_addc_u32 s65, s41, 0
	s_add_i32 s73, s62, s3
	global_load_lds_dwordx4 v[180:181], off
	v_lshl_add_u64 v[182:183], s[64:65], 0, v[166:167]
	s_mov_b32 m0, s73
	v_lshl_add_u64 v[184:185], s[42:43], 0, v[164:165]
	global_load_lds_dwordx4 v[182:183], off
	v_lshl_add_u64 v[182:183], s[64:65], 0, v[162:163]
	s_add_i32 m0, s73, 0x2000
	s_nop 0
	global_load_lds_dwordx4 v[182:183], off
	v_lshl_add_u64 v[182:183], s[42:43], 0, v[168:169]
	s_mov_b32 m0, s37
	s_nop 0
	global_load_lds_dwordx4 v[182:183], off
	s_mov_b32 m0, s44
	s_nop 0
	global_load_lds_dwordx4 v[184:185], off
	s_waitcnt vmcnt(8)
	s_waitcnt lgkmcnt(0)
	s_barrier
	s_setprio 1
	s_waitcnt lgkmcnt(0)
	v_mfma_scale_f32_16x16x128_f8f6f4 v[94:97], v[26:33], v[192:199], v[94:97], v1, v1 op_sel_hi:[0,0,0]
	v_mfma_scale_f32_16x16x128_f8f6f4 v[82:85], v[26:33], v[200:207], v[82:85], v1, v1 op_sel_hi:[0,0,0]
	v_mfma_scale_f32_16x16x128_f8f6f4 v[66:69], v[26:33], v[208:215], v[66:69], v1, v1 op_sel_hi:[0,0,0]
	v_mfma_scale_f32_16x16x128_f8f6f4 v[50:53], v[26:33], v[216:223], v[50:53], v1, v1 op_sel_hi:[0,0,0]
	v_mfma_scale_f32_16x16x128_f8f6f4 v[42:45], v[18:25], v[216:223], v[42:45], v1, v1 op_sel_hi:[0,0,0]
	v_mfma_scale_f32_16x16x128_f8f6f4 v[58:61], v[18:25], v[208:215], v[58:61], v1, v1 op_sel_hi:[0,0,0]
	v_mfma_scale_f32_16x16x128_f8f6f4 v[74:77], v[18:25], v[200:207], v[74:77], v1, v1 op_sel_hi:[0,0,0]
	v_mfma_scale_f32_16x16x128_f8f6f4 v[90:93], v[18:25], v[192:199], v[90:93], v1, v1 op_sel_hi:[0,0,0]
	s_setprio 0
	s_setprio 1
	v_mfma_scale_f32_16x16x128_f8f6f4 v[86:89], v[10:17], v[192:199], v[86:89], v1, v1 op_sel_hi:[0,0,0]
	v_mfma_scale_f32_16x16x128_f8f6f4 v[70:73], v[10:17], v[200:207], v[70:73], v1, v1 op_sel_hi:[0,0,0]
	v_mfma_scale_f32_16x16x128_f8f6f4 v[54:57], v[10:17], v[208:215], v[54:57], v1, v1 op_sel_hi:[0,0,0]
	v_mfma_scale_f32_16x16x128_f8f6f4 v[38:41], v[10:17], v[216:223], v[38:41], v1, v1 op_sel_hi:[0,0,0]
	v_mfma_scale_f32_16x16x128_f8f6f4 v[34:37], v[2:9], v[216:223], v[34:37], v1, v1 op_sel_hi:[0,0,0]
	v_mfma_scale_f32_16x16x128_f8f6f4 v[46:49], v[2:9], v[208:215], v[46:49], v1, v1 op_sel_hi:[0,0,0]
	v_mfma_scale_f32_16x16x128_f8f6f4 v[62:65], v[2:9], v[200:207], v[62:65], v1, v1 op_sel_hi:[0,0,0]
	v_mfma_scale_f32_16x16x128_f8f6f4 v[78:81], v[2:9], v[192:199], v[78:81], v1, v1 op_sel_hi:[0,0,0]
	s_setprio 0
	s_barrier
	s_add_i32 s64, 0, 0x18000
	s_add_i32 s65, 0, 0x1c000
	v_add_u32_e32 v14, s64, v187
	v_add_u32_e32 v30, s65, v187
	ds_read_b128 v[2:5], v14
	ds_read_b128 v[6:9], v14 offset:1024
	ds_read_b128 v[10:13], v14 offset:2048
	ds_read_b128 v[14:17], v14 offset:3072
	ds_read_b128 v[18:21], v30
	ds_read_b128 v[22:25], v30 offset:1024
	ds_read_b128 v[26:29], v30 offset:2048
	ds_read_b128 v[30:33], v30 offset:3072
	s_add_u32 s42, s42, 0x80000
	s_addc_u32 s43, s43, 0
	s_mov_b32 m0, s45
	v_lshl_add_u64 v[224:225], s[42:43], 0, v[168:169]
	ds_read_b128 v[192:195], v191 offset:32768
	ds_read_b128 v[196:199], v191 offset:33792
	ds_read_b128 v[200:203], v191 offset:34816
	ds_read_b128 v[204:207], v191 offset:35840
	ds_read_b128 v[208:211], v191 offset:36864
	ds_read_b128 v[212:215], v191 offset:37888
	ds_read_b128 v[216:219], v191 offset:38912
	ds_read_b128 v[220:223], v191 offset:39936
	global_load_lds_dwordx4 v[224:225], off
	v_lshl_add_u64 v[224:225], s[42:43], 0, v[164:165]
	s_mov_b32 m0, s48
	s_nop 0
	global_load_lds_dwordx4 v[224:225], off
	s_waitcnt vmcnt(8)
	s_waitcnt lgkmcnt(0)
	s_barrier
	s_setprio 1
	s_waitcnt lgkmcnt(0)
	v_mfma_scale_f32_16x16x128_f8f6f4 v[158:161], v[2:9], v[192:199], v[158:161], v1, v1 op_sel_hi:[0,0,0]
	v_mfma_scale_f32_16x16x128_f8f6f4 v[146:149], v[2:9], v[200:207], v[146:149], v1, v1 op_sel_hi:[0,0,0]
	v_mfma_scale_f32_16x16x128_f8f6f4 v[130:133], v[2:9], v[208:215], v[130:133], v1, v1 op_sel_hi:[0,0,0]
	v_mfma_scale_f32_16x16x128_f8f6f4 v[114:117], v[2:9], v[216:223], v[114:117], v1, v1 op_sel_hi:[0,0,0]
	v_mfma_scale_f32_16x16x128_f8f6f4 v[106:109], v[10:17], v[216:223], v[106:109], v1, v1 op_sel_hi:[0,0,0]
	v_mfma_scale_f32_16x16x128_f8f6f4 v[122:125], v[10:17], v[208:215], v[122:125], v1, v1 op_sel_hi:[0,0,0]
	v_mfma_scale_f32_16x16x128_f8f6f4 v[138:141], v[10:17], v[200:207], v[138:141], v1, v1 op_sel_hi:[0,0,0]
	v_mfma_scale_f32_16x16x128_f8f6f4 v[154:157], v[10:17], v[192:199], v[154:157], v1, v1 op_sel_hi:[0,0,0]
	s_setprio 0
	s_setprio 1
	v_mfma_scale_f32_16x16x128_f8f6f4 v[150:153], v[18:25], v[192:199], v[150:153], v1, v1 op_sel_hi:[0,0,0]
	v_mfma_scale_f32_16x16x128_f8f6f4 v[134:137], v[18:25], v[200:207], v[134:137], v1, v1 op_sel_hi:[0,0,0]
	v_mfma_scale_f32_16x16x128_f8f6f4 v[118:121], v[18:25], v[208:215], v[118:121], v1, v1 op_sel_hi:[0,0,0]
	v_mfma_scale_f32_16x16x128_f8f6f4 v[102:105], v[18:25], v[216:223], v[102:105], v1, v1 op_sel_hi:[0,0,0]
	v_mfma_scale_f32_16x16x128_f8f6f4 v[98:101], v[26:33], v[216:223], v[98:101], v1, v1 op_sel_hi:[0,0,0]
	v_mfma_scale_f32_16x16x128_f8f6f4 v[110:113], v[26:33], v[208:215], v[110:113], v1, v1 op_sel_hi:[0,0,0]
	v_mfma_scale_f32_16x16x128_f8f6f4 v[126:129], v[26:33], v[200:207], v[126:129], v1, v1 op_sel_hi:[0,0,0]
	v_mfma_scale_f32_16x16x128_f8f6f4 v[142:145], v[26:33], v[192:199], v[142:145], v1, v1 op_sel_hi:[0,0,0]
	s_setprio 0
	s_barrier
	s_add_i32 s42, s64, s3
	v_lshl_add_u64 v[178:179], v[178:179], 0, s[12:13]
	s_mov_b32 m0, s42
	ds_read_b128 v[192:195], v191 offset:49152
	ds_read_b128 v[196:199], v191 offset:50176
	ds_read_b128 v[200:203], v191 offset:51200
	ds_read_b128 v[204:207], v191 offset:52224
	ds_read_b128 v[208:211], v191 offset:53248
	ds_read_b128 v[212:215], v191 offset:54272
	ds_read_b128 v[216:219], v191 offset:55296
	ds_read_b128 v[220:223], v191 offset:56320
	global_load_lds_dwordx4 v[178:179], off
	s_add_i32 m0, s42, 0x2000
	s_add_u32 s40, s40, 0x80080
	v_lshl_add_u64 v[178:179], v[180:181], 0, s[12:13]
	s_addc_u32 s41, s41, 0
	s_add_i32 s42, s65, s3
	global_load_lds_dwordx4 v[178:179], off
	v_lshl_add_u64 v[178:179], s[40:41], 0, v[166:167]
	s_mov_b32 m0, s42
	s_nop 0
	global_load_lds_dwordx4 v[178:179], off
	v_lshl_add_u64 v[178:179], s[40:41], 0, v[162:163]
	s_add_i32 m0, s42, 0x2000
	s_nop 0
	global_load_lds_dwordx4 v[178:179], off
	v_lshl_add_u64 v[178:179], v[182:183], 0, s[12:13]
	s_mov_b32 m0, s51
	s_nop 0
	global_load_lds_dwordx4 v[178:179], off
	v_lshl_add_u64 v[178:179], v[184:185], 0, s[12:13]
	s_mov_b32 m0, s58
	s_nop 0
	global_load_lds_dwordx4 v[178:179], off
	s_waitcnt vmcnt(8)
	s_waitcnt lgkmcnt(0)
	s_barrier
	s_setprio 1
	s_waitcnt lgkmcnt(0)
	v_mfma_scale_f32_16x16x128_f8f6f4 v[94:97], v[2:9], v[192:199], v[94:97], v1, v1 op_sel_hi:[0,0,0]
	v_mfma_scale_f32_16x16x128_f8f6f4 v[82:85], v[2:9], v[200:207], v[82:85], v1, v1 op_sel_hi:[0,0,0]
	v_mfma_scale_f32_16x16x128_f8f6f4 v[66:69], v[2:9], v[208:215], v[66:69], v1, v1 op_sel_hi:[0,0,0]
	v_mfma_scale_f32_16x16x128_f8f6f4 v[50:53], v[2:9], v[216:223], v[50:53], v1, v1 op_sel_hi:[0,0,0]
	v_mfma_scale_f32_16x16x128_f8f6f4 v[42:45], v[10:17], v[216:223], v[42:45], v1, v1 op_sel_hi:[0,0,0]
	v_mfma_scale_f32_16x16x128_f8f6f4 v[58:61], v[10:17], v[208:215], v[58:61], v1, v1 op_sel_hi:[0,0,0]
	v_mfma_scale_f32_16x16x128_f8f6f4 v[74:77], v[10:17], v[200:207], v[74:77], v1, v1 op_sel_hi:[0,0,0]
	v_mfma_scale_f32_16x16x128_f8f6f4 v[90:93], v[10:17], v[192:199], v[90:93], v1, v1 op_sel_hi:[0,0,0]
	s_setprio 0
	s_setprio 1
	v_mfma_scale_f32_16x16x128_f8f6f4 v[86:89], v[18:25], v[192:199], v[86:89], v1, v1 op_sel_hi:[0,0,0]
	v_mfma_scale_f32_16x16x128_f8f6f4 v[70:73], v[18:25], v[200:207], v[70:73], v1, v1 op_sel_hi:[0,0,0]
	v_mfma_scale_f32_16x16x128_f8f6f4 v[54:57], v[18:25], v[208:215], v[54:57], v1, v1 op_sel_hi:[0,0,0]
	v_mfma_scale_f32_16x16x128_f8f6f4 v[38:41], v[18:25], v[216:223], v[38:41], v1, v1 op_sel_hi:[0,0,0]
	v_mfma_scale_f32_16x16x128_f8f6f4 v[34:37], v[26:33], v[216:223], v[34:37], v1, v1 op_sel_hi:[0,0,0]
	v_mfma_scale_f32_16x16x128_f8f6f4 v[46:49], v[26:33], v[208:215], v[46:49], v1, v1 op_sel_hi:[0,0,0]
	v_mfma_scale_f32_16x16x128_f8f6f4 v[62:65], v[26:33], v[200:207], v[62:65], v1, v1 op_sel_hi:[0,0,0]
	v_mfma_scale_f32_16x16x128_f8f6f4 v[78:81], v[26:33], v[192:199], v[78:81], v1, v1 op_sel_hi:[0,0,0]
	s_setprio 0
	s_barrier
	s_add_i32 s72, s72, 2
	s_add_u32 s38, s38, 0x100
	s_addc_u32 s39, s39, 0
	s_add_u32 s70, s70, 0x100
	s_addc_u32 s71, s71, 0
	s_cmp_gt_u32 s72, 29
	s_cbranch_scc0 .LBB0_1309
	s_and_b64 vcc, exec, s[14:15]
	s_cbranch_vccz .LBB0_1312
	s_barrier

.LBB0_1437:
	v_and_b32_e32 v188, 15, v189
	v_and_b32_e32 v2, 48, v189
	v_lshlrev_b32_e32 v3, 2, v189
	s_and_b32 s8, s6, 3
	s_lshl_b32 s9, s7, 13
	v_lshl_or_b32 v2, v188, 6, v2
	v_and_b32_e32 v3, 32, v3
	v_bitop3_b32 v4, v2, s9, v3 bitop3:0xde
	s_lshl_b32 s9, s8, 12
	v_lshl_add_u64 v[180:181], s[20:21], 0, v[154:155]
	v_bitop3_b32 v2, v2, s9, v3 bitop3:0xde
	s_add_i32 s9, s60, s72
	v_lshl_add_u64 v[178:179], s[20:21], 0, v[182:183]
	v_lshl_add_u64 v[72:73], v[180:181], 0, s[36:37]
	s_mov_b32 m0, s9
	s_add_i32 s19, s9, 0x2000
	s_waitcnt vmcnt(2)
	s_barrier
	global_load_lds_dwordx4 v[72:73], off
	v_lshl_add_u64 v[158:159], v[178:179], 0, s[36:37]
	s_mov_b32 m0, s19
	s_add_i32 s18, s67, 0x8000
	global_load_lds_dwordx4 v[158:159], off
	v_lshl_add_u64 v[70:71], v[172:173], 0, s[36:37]
	s_mov_b32 m0, s18
	s_add_i32 s43, s67, 0xa000
	global_load_lds_dwordx4 v[70:71], off
	v_lshl_add_u64 v[160:161], v[170:171], 0, s[36:37]
	s_mov_b32 m0, s43
	s_add_i32 s44, s61, s72
	global_load_lds_dwordx4 v[160:161], off
	v_lshl_add_u64 v[162:163], s[24:25], 0, v[154:155]
	s_mov_b32 m0, s44
	s_add_i32 s45, s44, 0x2000
	global_load_lds_dwordx4 v[162:163], off
	v_lshl_add_u64 v[164:165], s[24:25], 0, v[182:183]
	s_mov_b32 m0, s45
	s_add_i32 s73, 0, 0x10000
	global_load_lds_dwordx4 v[164:165], off
	v_add_u32_e32 v195, s73, v2
	s_add_i32 s75, 0, 0x14000
	s_waitcnt vmcnt(6)
	s_barrier
	v_add_u32_e32 v194, s75, v2
	v_add_u32_e32 v191, 0, v4
	v_add_u32_e32 v193, s60, v2
	v_add_u32_e32 v192, s61, v2
	ds_read_b128 v[54:57], v195
	ds_read_b128 v[58:61], v195 offset:1024
	ds_read_b128 v[196:199], v195 offset:2048
	ds_read_b128 v[200:203], v195 offset:3072
	ds_read_b128 v[10:13], v194
	ds_read_b128 v[14:17], v194 offset:1024
	ds_read_b128 v[2:5], v194 offset:2048
	ds_read_b128 v[6:9], v194 offset:3072
	s_lshl_b32 s66, s7, 6
	v_lshl_add_u64 v[176:177], s[22:23], 0, v[154:155]
	v_lshl_add_u64 v[174:175], s[22:23], 0, v[182:183]
	s_add_u32 s70, s4, 0x10080
	s_addc_u32 s71, s5, 0
	s_add_i32 s74, s67, 0xc000
	v_lshl_add_u64 v[30:31], s[70:71], 0, v[154:155]
	s_mov_b32 m0, s74
	s_add_i32 s69, s67, 0xe000
	ds_read_b128 v[22:25], v191
	ds_read_b128 v[26:29], v191 offset:1024
	ds_read_b128 v[34:37], v191 offset:2048
	ds_read_b128 v[38:41], v191 offset:3072
	ds_read_b128 v[82:85], v191 offset:4096
	ds_read_b128 v[86:89], v191 offset:5120
	ds_read_b128 v[94:97], v191 offset:6144
	ds_read_b128 v[98:101], v191 offset:7168
	global_load_lds_dwordx4 v[30:31], off
	v_lshl_add_u64 v[30:31], s[70:71], 0, v[182:183]
	s_mov_b32 m0, s69
	s_nop 0
	global_load_lds_dwordx4 v[30:31], off
	s_waitcnt vmcnt(8)
	s_waitcnt lgkmcnt(0)
	s_barrier
	s_setprio 1
	v_mov_b64_e32 v[32:33], v[20:21]
	v_mov_b64_e32 v[152:153], v[20:21]
	v_mov_b64_e32 v[92:93], v[20:21]
	v_mov_b64_e32 v[44:45], v[20:21]
	v_mov_b64_e32 v[116:117], v[20:21]
	v_mov_b64_e32 v[64:65], v[20:21]
	v_mov_b64_e32 v[80:81], v[20:21]
	v_mov_b64_e32 v[52:53], v[20:21]
	v_mov_b64_e32 v[30:31], v[18:19]
	v_mov_b64_e32 v[150:151], v[18:19]
	v_mov_b64_e32 v[90:91], v[18:19]
	v_mov_b64_e32 v[42:43], v[18:19]
	v_mov_b64_e32 v[114:115], v[18:19]
	v_mov_b64_e32 v[62:63], v[18:19]
	v_mov_b64_e32 v[78:79], v[18:19]
	v_mov_b64_e32 v[50:51], v[18:19]
	s_waitcnt lgkmcnt(0)
	v_mfma_scale_f32_16x16x128_f8f6f4 v[30:33], v[54:61], v[22:29], v[30:33], v190, v190 op_sel_hi:[0,0,0]
	v_mfma_scale_f32_16x16x128_f8f6f4 v[90:93], v[54:61], v[34:41], v[90:93], v190, v190 op_sel_hi:[0,0,0]
	v_mfma_scale_f32_16x16x128_f8f6f4 v[114:117], v[54:61], v[82:89], v[114:117], v190, v190 op_sel_hi:[0,0,0]
	v_mfma_scale_f32_16x16x128_f8f6f4 v[78:81], v[54:61], v[94:101], v[78:81], v190, v190 op_sel_hi:[0,0,0]
	v_mfma_scale_f32_16x16x128_f8f6f4 v[50:53], v[196:203], v[94:101], v[50:53], v190, v190 op_sel_hi:[0,0,0]
	v_mfma_scale_f32_16x16x128_f8f6f4 v[62:65], v[196:203], v[82:89], v[62:65], v190, v190 op_sel_hi:[0,0,0]
	v_mfma_scale_f32_16x16x128_f8f6f4 v[42:45], v[196:203], v[34:41], v[42:45], v190, v190 op_sel_hi:[0,0,0]
	v_mfma_scale_f32_16x16x128_f8f6f4 v[150:153], v[196:203], v[22:29], v[150:153], v190, v190 op_sel_hi:[0,0,0]
	s_setprio 0
	s_setprio 1
	v_mov_b64_e32 v[144:145], v[20:21]
	v_mov_b64_e32 v[148:149], v[20:21]
	v_mov_b64_e32 v[142:143], v[18:19]
	v_mov_b64_e32 v[146:147], v[18:19]
	v_mfma_scale_f32_16x16x128_f8f6f4 v[142:145], v[10:17], v[22:29], v[142:145], v190, v190 op_sel_hi:[0,0,0]
	v_mfma_scale_f32_16x16x128_f8f6f4 v[146:149], v[2:9], v[22:29], v[146:149], v190, v190 op_sel_hi:[0,0,0]
	v_mov_b64_e32 v[28:29], v[20:21]
	v_mov_b64_e32 v[140:141], v[20:21]
	v_mov_b64_e32 v[26:27], v[18:19]
	v_mov_b64_e32 v[138:139], v[18:19]
	v_mfma_scale_f32_16x16x128_f8f6f4 v[26:29], v[10:17], v[34:41], v[26:29], v190, v190 op_sel_hi:[0,0,0]
	v_mfma_scale_f32_16x16x128_f8f6f4 v[138:141], v[2:9], v[34:41], v[138:141], v190, v190 op_sel_hi:[0,0,0]
	v_mov_b64_e32 v[40:41], v[20:21]
	v_mov_b64_e32 v[128:129], v[20:21]
	v_mov_b64_e32 v[24:25], v[20:21]
	v_mov_b64_e32 v[76:77], v[20:21]
	v_mov_b64_e32 v[38:39], v[18:19]
	v_mov_b64_e32 v[126:127], v[18:19]
	v_mov_b64_e32 v[22:23], v[18:19]
	v_mov_b64_e32 v[74:75], v[18:19]
	v_mfma_scale_f32_16x16x128_f8f6f4 v[38:41], v[10:17], v[82:89], v[38:41], v190, v190 op_sel_hi:[0,0,0]
	v_mfma_scale_f32_16x16x128_f8f6f4 v[126:129], v[2:9], v[82:89], v[126:129], v190, v190 op_sel_hi:[0,0,0]
	v_mfma_scale_f32_16x16x128_f8f6f4 v[22:25], v[10:17], v[94:101], v[22:25], v190, v190 op_sel_hi:[0,0,0]
	v_mfma_scale_f32_16x16x128_f8f6f4 v[74:77], v[2:9], v[94:101], v[74:77], v190, v190 op_sel_hi:[0,0,0]
	s_setprio 0
	s_barrier
	s_add_i32 s70, s73, s72
	v_lshl_add_u64 v[34:35], v[180:181], 0, s[14:15]
	s_mov_b32 m0, s70
	s_add_i32 s71, s70, 0x2000
	ds_read_b128 v[204:207], v191 offset:16384
	ds_read_b128 v[208:211], v191 offset:17408
	ds_read_b128 v[212:215], v191 offset:18432
	ds_read_b128 v[216:219], v191 offset:19456
	ds_read_b128 v[220:223], v191 offset:20480
	ds_read_b128 v[224:227], v191 offset:21504
	ds_read_b128 v[228:231], v191 offset:22528
	ds_read_b128 v[232:235], v191 offset:23552
	global_load_lds_dwordx4 v[34:35], off
	v_lshl_add_u64 v[34:35], v[178:179], 0, s[14:15]
	s_mov_b32 m0, s71
	s_add_i32 s72, s75, s72
	global_load_lds_dwordx4 v[34:35], off
	v_lshl_add_u64 v[34:35], s[26:27], 0, v[154:155]
	s_mov_b32 m0, s72
	s_add_i32 s73, s72, 0x2000
	global_load_lds_dwordx4 v[34:35], off
	v_lshl_add_u64 v[34:35], s[26:27], 0, v[182:183]
	s_mov_b32 m0, s73
	s_nop 0
	global_load_lds_dwordx4 v[34:35], off
	v_lshl_add_u64 v[34:35], v[172:173], 0, s[14:15]
	s_mov_b32 m0, s67
	s_nop 0
	global_load_lds_dwordx4 v[34:35], off
	v_lshl_add_u64 v[34:35], v[170:171], 0, s[14:15]
	s_mov_b32 m0, s68
	s_nop 0
	global_load_lds_dwordx4 v[34:35], off
	s_waitcnt vmcnt(8)
	s_waitcnt lgkmcnt(0)
	s_barrier
	s_setprio 1
	v_mov_b64_e32 v[136:137], v[20:21]
	v_mov_b64_e32 v[104:105], v[20:21]
	v_mov_b64_e32 v[124:125], v[20:21]
	v_mov_b64_e32 v[100:101], v[20:21]
	v_mov_b64_e32 v[112:113], v[20:21]
	v_mov_b64_e32 v[108:109], v[20:21]
	v_mov_b64_e32 v[88:89], v[20:21]
	v_mov_b64_e32 v[84:85], v[20:21]
	v_mov_b64_e32 v[134:135], v[18:19]
	v_mov_b64_e32 v[102:103], v[18:19]
	v_mov_b64_e32 v[122:123], v[18:19]
	v_mov_b64_e32 v[98:99], v[18:19]
	v_mov_b64_e32 v[110:111], v[18:19]
	v_mov_b64_e32 v[106:107], v[18:19]
	v_mov_b64_e32 v[86:87], v[18:19]
	v_mov_b64_e32 v[82:83], v[18:19]
	s_waitcnt lgkmcnt(0)
	v_mfma_scale_f32_16x16x128_f8f6f4 v[134:137], v[54:61], v[204:211], v[134:137], v190, v190 op_sel_hi:[0,0,0]
	v_mfma_scale_f32_16x16x128_f8f6f4 v[122:125], v[54:61], v[212:219], v[122:125], v190, v190 op_sel_hi:[0,0,0]
	v_mfma_scale_f32_16x16x128_f8f6f4 v[110:113], v[54:61], v[220:227], v[110:113], v190, v190 op_sel_hi:[0,0,0]
	v_mfma_scale_f32_16x16x128_f8f6f4 v[86:89], v[54:61], v[228:235], v[86:89], v190, v190 op_sel_hi:[0,0,0]
	v_mfma_scale_f32_16x16x128_f8f6f4 v[82:85], v[196:203], v[228:235], v[82:85], v190, v190 op_sel_hi:[0,0,0]
	v_mfma_scale_f32_16x16x128_f8f6f4 v[106:109], v[196:203], v[220:227], v[106:109], v190, v190 op_sel_hi:[0,0,0]
	v_mfma_scale_f32_16x16x128_f8f6f4 v[98:101], v[196:203], v[212:219], v[98:101], v190, v190 op_sel_hi:[0,0,0]
	v_mfma_scale_f32_16x16x128_f8f6f4 v[102:105], v[196:203], v[204:211], v[102:105], v190, v190 op_sel_hi:[0,0,0]
	s_setprio 0
	s_setprio 1
	v_mov_b64_e32 v[36:37], v[20:21]
	v_mov_b64_e32 v[132:133], v[20:21]
	v_mov_b64_e32 v[48:49], v[20:21]
	v_mov_b64_e32 v[120:121], v[20:21]
	v_mov_b64_e32 v[68:69], v[20:21]
	v_mov_b64_e32 v[96:97], v[20:21]
	v_mov_b64_e32 v[56:57], v[20:21]
	v_mov_b64_e32 v[60:61], v[20:21]
	v_mov_b64_e32 v[34:35], v[18:19]
	v_mov_b64_e32 v[130:131], v[18:19]
	v_mov_b64_e32 v[46:47], v[18:19]
	v_mov_b64_e32 v[118:119], v[18:19]
	v_mov_b64_e32 v[66:67], v[18:19]
	v_mov_b64_e32 v[94:95], v[18:19]
	v_mov_b64_e32 v[54:55], v[18:19]
	v_mov_b64_e32 v[58:59], v[18:19]
	v_mfma_scale_f32_16x16x128_f8f6f4 v[34:37], v[10:17], v[204:211], v[34:37], v190, v190 op_sel_hi:[0,0,0]
	v_mfma_scale_f32_16x16x128_f8f6f4 v[46:49], v[10:17], v[212:219], v[46:49], v190, v190 op_sel_hi:[0,0,0]
	v_mfma_scale_f32_16x16x128_f8f6f4 v[66:69], v[10:17], v[220:227], v[66:69], v190, v190 op_sel_hi:[0,0,0]
	v_mfma_scale_f32_16x16x128_f8f6f4 v[54:57], v[10:17], v[228:235], v[54:57], v190, v190 op_sel_hi:[0,0,0]
	v_mfma_scale_f32_16x16x128_f8f6f4 v[58:61], v[2:9], v[228:235], v[58:61], v190, v190 op_sel_hi:[0,0,0]
	v_mfma_scale_f32_16x16x128_f8f6f4 v[94:97], v[2:9], v[220:227], v[94:97], v190, v190 op_sel_hi:[0,0,0]
	v_mfma_scale_f32_16x16x128_f8f6f4 v[118:121], v[2:9], v[212:219], v[118:121], v190, v190 op_sel_hi:[0,0,0]
	v_mfma_scale_f32_16x16x128_f8f6f4 v[130:133], v[2:9], v[204:211], v[130:133], v190, v190 op_sel_hi:[0,0,0]
	s_setprio 0
	s_barrier
	ds_read_b128 v[2:5], v193
	ds_read_b128 v[6:9], v193 offset:1024
	ds_read_b128 v[10:13], v193 offset:2048
	ds_read_b128 v[14:17], v193 offset:3072
	ds_read_b128 v[196:199], v192
	ds_read_b128 v[200:203], v192 offset:1024
	ds_read_b128 v[204:207], v192 offset:2048
	ds_read_b128 v[208:211], v192 offset:3072
	s_add_u32 s76, s4, 0x10100
	s_addc_u32 s77, s5, 0
	s_mov_b32 m0, s48
	v_lshl_add_u64 v[244:245], s[76:77], 0, v[154:155]
	ds_read_b128 v[212:215], v191 offset:32768
	ds_read_b128 v[216:219], v191 offset:33792
	ds_read_b128 v[220:223], v191 offset:34816
	ds_read_b128 v[224:227], v191 offset:35840
	ds_read_b128 v[228:231], v191 offset:36864
	ds_read_b128 v[232:235], v191 offset:37888
	ds_read_b128 v[236:239], v191 offset:38912
	ds_read_b128 v[240:243], v191 offset:39936
	global_load_lds_dwordx4 v[244:245], off
	v_lshl_add_u64 v[244:245], s[76:77], 0, v[182:183]
	s_mov_b32 m0, s49
	s_nop 0
	global_load_lds_dwordx4 v[244:245], off
	s_waitcnt vmcnt(8)
	s_waitcnt lgkmcnt(0)
	s_barrier
	s_setprio 1
	s_waitcnt lgkmcnt(0)
	v_mfma_scale_f32_16x16x128_f8f6f4 v[30:33], v[2:9], v[212:219], v[30:33], v190, v190 op_sel_hi:[0,0,0]
	v_mfma_scale_f32_16x16x128_f8f6f4 v[90:93], v[2:9], v[220:227], v[90:93], v190, v190 op_sel_hi:[0,0,0]
	v_mfma_scale_f32_16x16x128_f8f6f4 v[114:117], v[2:9], v[228:235], v[114:117], v190, v190 op_sel_hi:[0,0,0]
	v_mfma_scale_f32_16x16x128_f8f6f4 v[78:81], v[2:9], v[236:243], v[78:81], v190, v190 op_sel_hi:[0,0,0]
	v_mfma_scale_f32_16x16x128_f8f6f4 v[50:53], v[10:17], v[236:243], v[50:53], v190, v190 op_sel_hi:[0,0,0]
	v_mfma_scale_f32_16x16x128_f8f6f4 v[62:65], v[10:17], v[228:235], v[62:65], v190, v190 op_sel_hi:[0,0,0]
	v_mfma_scale_f32_16x16x128_f8f6f4 v[42:45], v[10:17], v[220:227], v[42:45], v190, v190 op_sel_hi:[0,0,0]
	v_mfma_scale_f32_16x16x128_f8f6f4 v[150:153], v[10:17], v[212:219], v[150:153], v190, v190 op_sel_hi:[0,0,0]
	s_setprio 0
	s_setprio 1
	v_mfma_scale_f32_16x16x128_f8f6f4 v[142:145], v[196:203], v[212:219], v[142:145], v190, v190 op_sel_hi:[0,0,0]
	v_mfma_scale_f32_16x16x128_f8f6f4 v[26:29], v[196:203], v[220:227], v[26:29], v190, v190 op_sel_hi:[0,0,0]
	v_mfma_scale_f32_16x16x128_f8f6f4 v[38:41], v[196:203], v[228:235], v[38:41], v190, v190 op_sel_hi:[0,0,0]
	v_mfma_scale_f32_16x16x128_f8f6f4 v[22:25], v[196:203], v[236:243], v[22:25], v190, v190 op_sel_hi:[0,0,0]
	v_mfma_scale_f32_16x16x128_f8f6f4 v[74:77], v[204:211], v[236:243], v[74:77], v190, v190 op_sel_hi:[0,0,0]
	v_mfma_scale_f32_16x16x128_f8f6f4 v[126:129], v[204:211], v[228:235], v[126:129], v190, v190 op_sel_hi:[0,0,0]
	v_mfma_scale_f32_16x16x128_f8f6f4 v[138:141], v[204:211], v[220:227], v[138:141], v190, v190 op_sel_hi:[0,0,0]
	v_mfma_scale_f32_16x16x128_f8f6f4 v[146:149], v[204:211], v[212:219], v[146:149], v190, v190 op_sel_hi:[0,0,0]
	s_setprio 0
	s_barrier
	s_mov_b32 m0, s9
	v_lshl_add_u64 v[244:245], v[180:181], 0, s[38:39]
	ds_read_b128 v[212:215], v191 offset:49152
	ds_read_b128 v[216:219], v191 offset:50176
	ds_read_b128 v[220:223], v191 offset:51200
	ds_read_b128 v[224:227], v191 offset:52224
	ds_read_b128 v[228:231], v191 offset:53248
	ds_read_b128 v[232:235], v191 offset:54272
	ds_read_b128 v[236:239], v191 offset:55296
	ds_read_b128 v[240:243], v191 offset:56320
	global_load_lds_dwordx4 v[244:245], off
	v_lshl_add_u64 v[244:245], v[178:179], 0, s[38:39]
	s_mov_b32 m0, s19
	s_nop 0
	global_load_lds_dwordx4 v[244:245], off
	v_lshl_add_u64 v[244:245], s[28:29], 0, v[154:155]
	s_mov_b32 m0, s44
	s_nop 0
	global_load_lds_dwordx4 v[244:245], off
	v_lshl_add_u64 v[244:245], s[28:29], 0, v[182:183]
	s_mov_b32 m0, s45
	s_nop 0
	global_load_lds_dwordx4 v[244:245], off
	v_lshl_add_u64 v[244:245], v[172:173], 0, s[38:39]
	s_mov_b32 m0, s18
	s_nop 0
	global_load_lds_dwordx4 v[244:245], off
	v_lshl_add_u64 v[244:245], v[170:171], 0, s[38:39]
	s_mov_b32 m0, s43
	s_nop 0
	global_load_lds_dwordx4 v[244:245], off
	s_waitcnt vmcnt(8)
	s_waitcnt lgkmcnt(0)
	s_barrier
	s_setprio 1
	s_waitcnt lgkmcnt(0)
	v_mfma_scale_f32_16x16x128_f8f6f4 v[134:137], v[2:9], v[212:219], v[134:137], v190, v190 op_sel_hi:[0,0,0]
	v_mfma_scale_f32_16x16x128_f8f6f4 v[122:125], v[2:9], v[220:227], v[122:125], v190, v190 op_sel_hi:[0,0,0]
	v_mfma_scale_f32_16x16x128_f8f6f4 v[110:113], v[2:9], v[228:235], v[110:113], v190, v190 op_sel_hi:[0,0,0]
	v_mfma_scale_f32_16x16x128_f8f6f4 v[86:89], v[2:9], v[236:243], v[86:89], v190, v190 op_sel_hi:[0,0,0]
	v_mfma_scale_f32_16x16x128_f8f6f4 v[82:85], v[10:17], v[236:243], v[82:85], v190, v190 op_sel_hi:[0,0,0]
	v_mfma_scale_f32_16x16x128_f8f6f4 v[106:109], v[10:17], v[228:235], v[106:109], v190, v190 op_sel_hi:[0,0,0]
	v_mfma_scale_f32_16x16x128_f8f6f4 v[98:101], v[10:17], v[220:227], v[98:101], v190, v190 op_sel_hi:[0,0,0]
	v_mfma_scale_f32_16x16x128_f8f6f4 v[102:105], v[10:17], v[212:219], v[102:105], v190, v190 op_sel_hi:[0,0,0]
	s_setprio 0
	s_setprio 1
	v_mfma_scale_f32_16x16x128_f8f6f4 v[34:37], v[196:203], v[212:219], v[34:37], v190, v190 op_sel_hi:[0,0,0]
	v_mfma_scale_f32_16x16x128_f8f6f4 v[46:49], v[196:203], v[220:227], v[46:49], v190, v190 op_sel_hi:[0,0,0]
	v_mfma_scale_f32_16x16x128_f8f6f4 v[66:69], v[196:203], v[228:235], v[66:69], v190, v190 op_sel_hi:[0,0,0]
	v_mfma_scale_f32_16x16x128_f8f6f4 v[54:57], v[196:203], v[236:243], v[54:57], v190, v190 op_sel_hi:[0,0,0]
	v_mfma_scale_f32_16x16x128_f8f6f4 v[58:61], v[204:211], v[236:243], v[58:61], v190, v190 op_sel_hi:[0,0,0]
	v_mfma_scale_f32_16x16x128_f8f6f4 v[94:97], v[204:211], v[228:235], v[94:97], v190, v190 op_sel_hi:[0,0,0]
	v_mfma_scale_f32_16x16x128_f8f6f4 v[118:121], v[204:211], v[220:227], v[118:121], v190, v190 op_sel_hi:[0,0,0]
	v_mfma_scale_f32_16x16x128_f8f6f4 v[130:133], v[204:211], v[212:219], v[130:133], v190, v190 op_sel_hi:[0,0,0]
	s_setprio 0
	s_barrier
	ds_read_b128 v[2:5], v195
	ds_read_b128 v[6:9], v195 offset:1024
	ds_read_b128 v[10:13], v195 offset:2048
	ds_read_b128 v[14:17], v195 offset:3072
	ds_read_b128 v[196:199], v194
	ds_read_b128 v[200:203], v194 offset:1024
	ds_read_b128 v[204:207], v194 offset:2048
	ds_read_b128 v[208:211], v194 offset:3072
	s_add_u32 s4, s4, 0x10180
	s_addc_u32 s5, s5, 0
	s_mov_b32 m0, s74
	v_lshl_add_u64 v[194:195], s[4:5], 0, v[154:155]
	ds_read_b128 v[212:215], v191
	ds_read_b128 v[216:219], v191 offset:1024
	ds_read_b128 v[220:223], v191 offset:2048
	ds_read_b128 v[224:227], v191 offset:3072
	ds_read_b128 v[228:231], v191 offset:4096
	ds_read_b128 v[232:235], v191 offset:5120
	ds_read_b128 v[236:239], v191 offset:6144
	ds_read_b128 v[240:243], v191 offset:7168
	global_load_lds_dwordx4 v[194:195], off
	v_lshl_add_u64 v[182:183], s[4:5], 0, v[182:183]
	s_mov_b32 m0, s69
	s_nop 0
	global_load_lds_dwordx4 v[182:183], off
	s_waitcnt vmcnt(8)
	s_waitcnt lgkmcnt(0)
	s_barrier
	s_setprio 1
	s_waitcnt lgkmcnt(0)
	v_mfma_scale_f32_16x16x128_f8f6f4 v[30:33], v[2:9], v[212:219], v[30:33], v190, v190 op_sel_hi:[0,0,0]
	v_mfma_scale_f32_16x16x128_f8f6f4 v[90:93], v[2:9], v[220:227], v[90:93], v190, v190 op_sel_hi:[0,0,0]
	v_mfma_scale_f32_16x16x128_f8f6f4 v[114:117], v[2:9], v[228:235], v[114:117], v190, v190 op_sel_hi:[0,0,0]
	v_mfma_scale_f32_16x16x128_f8f6f4 v[78:81], v[2:9], v[236:243], v[78:81], v190, v190 op_sel_hi:[0,0,0]
	v_mfma_scale_f32_16x16x128_f8f6f4 v[50:53], v[10:17], v[236:243], v[50:53], v190, v190 op_sel_hi:[0,0,0]
	v_mfma_scale_f32_16x16x128_f8f6f4 v[62:65], v[10:17], v[228:235], v[62:65], v190, v190 op_sel_hi:[0,0,0]
	v_mfma_scale_f32_16x16x128_f8f6f4 v[42:45], v[10:17], v[220:227], v[42:45], v190, v190 op_sel_hi:[0,0,0]
	v_mfma_scale_f32_16x16x128_f8f6f4 v[150:153], v[10:17], v[212:219], v[150:153], v190, v190 op_sel_hi:[0,0,0]
	s_setprio 0
	s_setprio 1
	v_mfma_scale_f32_16x16x128_f8f6f4 v[142:145], v[196:203], v[212:219], v[142:145], v190, v190 op_sel_hi:[0,0,0]
	v_mfma_scale_f32_16x16x128_f8f6f4 v[26:29], v[196:203], v[220:227], v[26:29], v190, v190 op_sel_hi:[0,0,0]
	v_mfma_scale_f32_16x16x128_f8f6f4 v[38:41], v[196:203], v[228:235], v[38:41], v190, v190 op_sel_hi:[0,0,0]
	v_mfma_scale_f32_16x16x128_f8f6f4 v[22:25], v[196:203], v[236:243], v[22:25], v190, v190 op_sel_hi:[0,0,0]
	v_mfma_scale_f32_16x16x128_f8f6f4 v[74:77], v[204:211], v[236:243], v[74:77], v190, v190 op_sel_hi:[0,0,0]
	v_mfma_scale_f32_16x16x128_f8f6f4 v[126:129], v[204:211], v[228:235], v[126:129], v190, v190 op_sel_hi:[0,0,0]
	v_mfma_scale_f32_16x16x128_f8f6f4 v[138:141], v[204:211], v[220:227], v[138:141], v190, v190 op_sel_hi:[0,0,0]
	v_mfma_scale_f32_16x16x128_f8f6f4 v[146:149], v[204:211], v[212:219], v[146:149], v190, v190 op_sel_hi:[0,0,0]
	s_setprio 0
	s_barrier
	s_mov_b32 m0, s70
	ds_read_b128 v[212:215], v191 offset:16384
	ds_read_b128 v[216:219], v191 offset:17408
	ds_read_b128 v[220:223], v191 offset:18432
	ds_read_b128 v[224:227], v191 offset:19456
	ds_read_b128 v[228:231], v191 offset:20480
	ds_read_b128 v[232:235], v191 offset:21504
	ds_read_b128 v[236:239], v191 offset:22528
	ds_read_b128 v[240:243], v191 offset:23552
	global_load_lds_dwordx4 v[180:181], off
	s_mov_b32 m0, s71
	s_nop 0
	global_load_lds_dwordx4 v[178:179], off
	s_mov_b32 m0, s72
	s_nop 0
	global_load_lds_dwordx4 v[176:177], off
	s_mov_b32 m0, s73
	s_nop 0
	global_load_lds_dwordx4 v[174:175], off
	s_mov_b32 m0, s67
	s_nop 0
	global_load_lds_dwordx4 v[172:173], off
	s_mov_b32 m0, s68
	s_nop 0
	global_load_lds_dwordx4 v[170:171], off
	s_waitcnt vmcnt(8)
	s_waitcnt lgkmcnt(0)
	s_barrier
	s_setprio 1
	s_waitcnt lgkmcnt(0)
	v_mfma_scale_f32_16x16x128_f8f6f4 v[134:137], v[2:9], v[212:219], v[134:137], v190, v190 op_sel_hi:[0,0,0]
	v_mfma_scale_f32_16x16x128_f8f6f4 v[122:125], v[2:9], v[220:227], v[122:125], v190, v190 op_sel_hi:[0,0,0]
	v_mfma_scale_f32_16x16x128_f8f6f4 v[110:113], v[2:9], v[228:235], v[110:113], v190, v190 op_sel_hi:[0,0,0]
	v_mfma_scale_f32_16x16x128_f8f6f4 v[86:89], v[2:9], v[236:243], v[86:89], v190, v190 op_sel_hi:[0,0,0]
	v_mfma_scale_f32_16x16x128_f8f6f4 v[82:85], v[10:17], v[236:243], v[82:85], v190, v190 op_sel_hi:[0,0,0]
	v_mfma_scale_f32_16x16x128_f8f6f4 v[106:109], v[10:17], v[228:235], v[106:109], v190, v190 op_sel_hi:[0,0,0]
	v_mfma_scale_f32_16x16x128_f8f6f4 v[98:101], v[10:17], v[220:227], v[98:101], v190, v190 op_sel_hi:[0,0,0]
	v_mfma_scale_f32_16x16x128_f8f6f4 v[102:105], v[10:17], v[212:219], v[102:105], v190, v190 op_sel_hi:[0,0,0]
	s_setprio 0
	s_setprio 1
	v_mfma_scale_f32_16x16x128_f8f6f4 v[34:37], v[196:203], v[212:219], v[34:37], v190, v190 op_sel_hi:[0,0,0]
	v_mfma_scale_f32_16x16x128_f8f6f4 v[46:49], v[196:203], v[220:227], v[46:49], v190, v190 op_sel_hi:[0,0,0]
	v_mfma_scale_f32_16x16x128_f8f6f4 v[66:69], v[196:203], v[228:235], v[66:69], v190, v190 op_sel_hi:[0,0,0]
	v_mfma_scale_f32_16x16x128_f8f6f4 v[54:57], v[196:203], v[236:243], v[54:57], v190, v190 op_sel_hi:[0,0,0]
	v_mfma_scale_f32_16x16x128_f8f6f4 v[58:61], v[204:211], v[236:243], v[58:61], v190, v190 op_sel_hi:[0,0,0]
	v_mfma_scale_f32_16x16x128_f8f6f4 v[94:97], v[204:211], v[228:235], v[94:97], v190, v190 op_sel_hi:[0,0,0]
	v_mfma_scale_f32_16x16x128_f8f6f4 v[118:121], v[204:211], v[220:227], v[118:121], v190, v190 op_sel_hi:[0,0,0]
	v_mfma_scale_f32_16x16x128_f8f6f4 v[130:133], v[204:211], v[212:219], v[130:133], v190, v190 op_sel_hi:[0,0,0]
	s_setprio 0
	s_barrier
	ds_read_b128 v[2:5], v193
	ds_read_b128 v[6:9], v193 offset:1024
	ds_read_b128 v[10:13], v193 offset:2048
	ds_read_b128 v[14:17], v193 offset:3072
	ds_read_b128 v[170:173], v192
	ds_read_b128 v[174:177], v192 offset:1024
	ds_read_b128 v[194:197], v192 offset:2048
	ds_read_b128 v[198:201], v192 offset:3072
	s_mov_b32 m0, s48
	ds_read_b128 v[202:205], v191 offset:32768
	ds_read_b128 v[206:209], v191 offset:33792
	ds_read_b128 v[210:213], v191 offset:34816
	ds_read_b128 v[214:217], v191 offset:35840
	ds_read_b128 v[218:221], v191 offset:36864
	ds_read_b128 v[222:225], v191 offset:37888
	ds_read_b128 v[226:229], v191 offset:38912
	ds_read_b128 v[230:233], v191 offset:39936
	global_load_lds_dwordx4 v[166:167], off
	s_mov_b32 m0, s49
	s_nop 0
	global_load_lds_dwordx4 v[168:169], off
	s_waitcnt vmcnt(8)
	s_waitcnt lgkmcnt(0)
	s_barrier
	s_setprio 1
	s_waitcnt lgkmcnt(0)
	v_mfma_scale_f32_16x16x128_f8f6f4 v[30:33], v[2:9], v[202:209], v[30:33], v190, v190 op_sel_hi:[0,0,0]
	v_mfma_scale_f32_16x16x128_f8f6f4 v[90:93], v[2:9], v[210:217], v[90:93], v190, v190 op_sel_hi:[0,0,0]
	v_mfma_scale_f32_16x16x128_f8f6f4 v[114:117], v[2:9], v[218:225], v[114:117], v190, v190 op_sel_hi:[0,0,0]
	v_mfma_scale_f32_16x16x128_f8f6f4 v[78:81], v[2:9], v[226:233], v[78:81], v190, v190 op_sel_hi:[0,0,0]
	v_mfma_scale_f32_16x16x128_f8f6f4 v[50:53], v[10:17], v[226:233], v[50:53], v190, v190 op_sel_hi:[0,0,0]
	v_mfma_scale_f32_16x16x128_f8f6f4 v[62:65], v[10:17], v[218:225], v[62:65], v190, v190 op_sel_hi:[0,0,0]
	v_mfma_scale_f32_16x16x128_f8f6f4 v[42:45], v[10:17], v[210:217], v[42:45], v190, v190 op_sel_hi:[0,0,0]
	v_mfma_scale_f32_16x16x128_f8f6f4 v[150:153], v[10:17], v[202:209], v[150:153], v190, v190 op_sel_hi:[0,0,0]
	s_setprio 0
	s_setprio 1
	v_mfma_scale_f32_16x16x128_f8f6f4 v[142:145], v[170:177], v[202:209], v[142:145], v190, v190 op_sel_hi:[0,0,0]
	v_mfma_scale_f32_16x16x128_f8f6f4 v[26:29], v[170:177], v[210:217], v[26:29], v190, v190 op_sel_hi:[0,0,0]
	v_mfma_scale_f32_16x16x128_f8f6f4 v[38:41], v[170:177], v[218:225], v[38:41], v190, v190 op_sel_hi:[0,0,0]
	v_mfma_scale_f32_16x16x128_f8f6f4 v[22:25], v[170:177], v[226:233], v[22:25], v190, v190 op_sel_hi:[0,0,0]
	v_mfma_scale_f32_16x16x128_f8f6f4 v[74:77], v[194:201], v[226:233], v[74:77], v190, v190 op_sel_hi:[0,0,0]
	v_mfma_scale_f32_16x16x128_f8f6f4 v[126:129], v[194:201], v[218:225], v[126:129], v190, v190 op_sel_hi:[0,0,0]
	v_mfma_scale_f32_16x16x128_f8f6f4 v[138:141], v[194:201], v[210:217], v[138:141], v190, v190 op_sel_hi:[0,0,0]
	v_mfma_scale_f32_16x16x128_f8f6f4 v[146:149], v[194:201], v[202:209], v[146:149], v190, v190 op_sel_hi:[0,0,0]
	s_setprio 0
	s_barrier
	s_mov_b32 m0, s9
	ds_read_b128 v[202:205], v191 offset:49152
	ds_read_b128 v[206:209], v191 offset:50176
	ds_read_b128 v[210:213], v191 offset:51200
	ds_read_b128 v[214:217], v191 offset:52224
	ds_read_b128 v[218:221], v191 offset:53248
	ds_read_b128 v[222:225], v191 offset:54272
	ds_read_b128 v[226:229], v191 offset:55296
	ds_read_b128 v[230:233], v191 offset:56320
	global_load_lds_dwordx4 v[72:73], off
	s_mov_b32 m0, s19
	s_nop 0
	global_load_lds_dwordx4 v[158:159], off
	s_mov_b32 m0, s44
	s_nop 0
	global_load_lds_dwordx4 v[162:163], off
	s_mov_b32 m0, s45
	s_nop 0
	global_load_lds_dwordx4 v[164:165], off
	s_mov_b32 m0, s18
	s_nop 0
	global_load_lds_dwordx4 v[70:71], off
	s_mov_b32 m0, s43
	s_nop 0
	global_load_lds_dwordx4 v[160:161], off
	s_waitcnt vmcnt(8)
	s_waitcnt lgkmcnt(0)
	s_barrier
	s_setprio 1
	s_waitcnt lgkmcnt(0)
	v_mfma_scale_f32_16x16x128_f8f6f4 v[134:137], v[2:9], v[202:209], v[134:137], v190, v190 op_sel_hi:[0,0,0]
	v_mfma_scale_f32_16x16x128_f8f6f4 v[122:125], v[2:9], v[210:217], v[122:125], v190, v190 op_sel_hi:[0,0,0]
	v_mfma_scale_f32_16x16x128_f8f6f4 v[110:113], v[2:9], v[218:225], v[110:113], v190, v190 op_sel_hi:[0,0,0]
	v_mfma_scale_f32_16x16x128_f8f6f4 v[86:89], v[2:9], v[226:233], v[86:89], v190, v190 op_sel_hi:[0,0,0]
	v_mfma_scale_f32_16x16x128_f8f6f4 v[82:85], v[10:17], v[226:233], v[82:85], v190, v190 op_sel_hi:[0,0,0]
	v_mfma_scale_f32_16x16x128_f8f6f4 v[106:109], v[10:17], v[218:225], v[106:109], v190, v190 op_sel_hi:[0,0,0]
	v_mfma_scale_f32_16x16x128_f8f6f4 v[98:101], v[10:17], v[210:217], v[98:101], v190, v190 op_sel_hi:[0,0,0]
	v_mfma_scale_f32_16x16x128_f8f6f4 v[102:105], v[10:17], v[202:209], v[102:105], v190, v190 op_sel_hi:[0,0,0]
	s_setprio 0
	s_setprio 1
	v_mfma_scale_f32_16x16x128_f8f6f4 v[34:37], v[170:177], v[202:209], v[34:37], v190, v190 op_sel_hi:[0,0,0]
	v_mfma_scale_f32_16x16x128_f8f6f4 v[46:49], v[170:177], v[210:217], v[46:49], v190, v190 op_sel_hi:[0,0,0]
	v_mfma_scale_f32_16x16x128_f8f6f4 v[66:69], v[170:177], v[218:225], v[66:69], v190, v190 op_sel_hi:[0,0,0]
	v_mfma_scale_f32_16x16x128_f8f6f4 v[54:57], v[170:177], v[226:233], v[54:57], v190, v190 op_sel_hi:[0,0,0]
	v_mfma_scale_f32_16x16x128_f8f6f4 v[58:61], v[194:201], v[226:233], v[58:61], v190, v190 op_sel_hi:[0,0,0]
	v_mfma_scale_f32_16x16x128_f8f6f4 v[94:97], v[194:201], v[218:225], v[94:97], v190, v190 op_sel_hi:[0,0,0]
	v_mfma_scale_f32_16x16x128_f8f6f4 v[118:121], v[194:201], v[210:217], v[118:121], v190, v190 op_sel_hi:[0,0,0]
	v_mfma_scale_f32_16x16x128_f8f6f4 v[130:133], v[194:201], v[202:209], v[130:133], v190, v190 op_sel_hi:[0,0,0]
	s_setprio 0
	s_barrier
	s_waitcnt vmcnt(0)
	s_cmpk_gt_u32 s65, 0xff
	s_cbranch_scc1 .LBB0_1439
	s_barrier

.LBB0_1558:
	s_add_u32 s39, s30, s38
	s_addc_u32 s44, s31, 0
	s_add_u32 s42, s39, 0x100
	s_addc_u32 s43, s44, 0
	s_and_b64 s[40:41], s[36:37], exec
	s_cselect_b32 s41, s18, s43
	s_cselect_b32 s40, s19, s42
	s_add_u32 s38, s28, s38
	s_addc_u32 s42, s29, 0
	s_add_u32 s38, s38, 0x100
	s_addc_u32 s42, s42, 0
	s_and_b64 s[36:37], s[36:37], exec
	s_cselect_b32 s43, s17, s42
	s_cselect_b32 s42, s21, s38
	s_add_u32 s76, s39, 0x10080
	ds_read_b128 v[26:29], v181
	ds_read_b128 v[30:33], v181 offset:1024
	ds_read_b128 v[18:21], v181 offset:2048
	ds_read_b128 v[22:25], v181 offset:3072
	ds_read_b128 v[10:13], v182
	ds_read_b128 v[14:17], v182 offset:1024
	ds_read_b128 v[2:5], v182 offset:2048
	ds_read_b128 v[6:9], v182 offset:3072
	s_addc_u32 s77, s44, 0
	s_add_i32 s75, s63, s15
	s_add_i32 m0, s27, 0xc000
	s_add_i32 s78, s27, 0xe000
	s_add_i32 s72, s75, 0x2000
	s_add_u32 s44, s42, 0x10000
	s_addc_u32 s45, s43, 0
	s_add_i32 s74, s64, s15
	s_add_i32 s73, s74, 0x2000
	s_add_i32 s71, 0, 0x18000
	s_add_i32 s70, 0, 0x1c000
	s_add_u32 s38, s40, 0x10000
	s_addc_u32 s39, s41, 0
	s_add_i32 s69, s71, s15
	s_add_i32 s67, s69, 0x2000
	s_add_u32 s36, s42, 0x10080
	s_addc_u32 s37, s43, 0
	s_add_i32 s68, s70, s15
	s_add_i32 s66, s68, 0x2000
	v_lshl_add_u64 v[208:209], s[76:77], 0, v[164:165]
	ds_read_b128 v[170:173], v183
	ds_read_b128 v[174:177], v183 offset:1024
	ds_read_b128 v[184:187], v183 offset:2048
	ds_read_b128 v[188:191], v183 offset:3072
	ds_read_b128 v[192:195], v183 offset:4096
	ds_read_b128 v[196:199], v183 offset:5120
	ds_read_b128 v[200:203], v183 offset:6144
	ds_read_b128 v[204:207], v183 offset:7168
	global_load_lds_dwordx4 v[208:209], off
	v_lshl_add_u64 v[208:209], s[76:77], 0, v[162:163]
	s_mov_b32 m0, s78
	s_nop 0
	global_load_lds_dwordx4 v[208:209], off
	s_waitcnt vmcnt(8)
	s_waitcnt lgkmcnt(0)
	s_barrier
	s_setprio 1
	s_waitcnt lgkmcnt(0)
	v_mfma_scale_f32_16x16x128_f8f6f4 v[158:161], v[26:33], v[170:177], v[158:161], v1, v1 op_sel_hi:[0,0,0]
	v_mfma_scale_f32_16x16x128_f8f6f4 v[142:145], v[26:33], v[184:191], v[142:145], v1, v1 op_sel_hi:[0,0,0]
	v_mfma_scale_f32_16x16x128_f8f6f4 v[126:129], v[26:33], v[192:199], v[126:129], v1, v1 op_sel_hi:[0,0,0]
	v_mfma_scale_f32_16x16x128_f8f6f4 v[110:113], v[26:33], v[200:207], v[110:113], v1, v1 op_sel_hi:[0,0,0]
	v_mfma_scale_f32_16x16x128_f8f6f4 v[106:109], v[18:25], v[200:207], v[106:109], v1, v1 op_sel_hi:[0,0,0]
	v_mfma_scale_f32_16x16x128_f8f6f4 v[122:125], v[18:25], v[192:199], v[122:125], v1, v1 op_sel_hi:[0,0,0]
	v_mfma_scale_f32_16x16x128_f8f6f4 v[138:141], v[18:25], v[184:191], v[138:141], v1, v1 op_sel_hi:[0,0,0]
	v_mfma_scale_f32_16x16x128_f8f6f4 v[154:157], v[18:25], v[170:177], v[154:157], v1, v1 op_sel_hi:[0,0,0]
	s_setprio 0
	s_setprio 1
	v_mfma_scale_f32_16x16x128_f8f6f4 v[150:153], v[10:17], v[170:177], v[150:153], v1, v1 op_sel_hi:[0,0,0]
	v_mfma_scale_f32_16x16x128_f8f6f4 v[134:137], v[10:17], v[184:191], v[134:137], v1, v1 op_sel_hi:[0,0,0]
	v_mfma_scale_f32_16x16x128_f8f6f4 v[118:121], v[10:17], v[192:199], v[118:121], v1, v1 op_sel_hi:[0,0,0]
	v_mfma_scale_f32_16x16x128_f8f6f4 v[102:105], v[10:17], v[200:207], v[102:105], v1, v1 op_sel_hi:[0,0,0]
	v_mfma_scale_f32_16x16x128_f8f6f4 v[98:101], v[2:9], v[200:207], v[98:101], v1, v1 op_sel_hi:[0,0,0]
	v_mfma_scale_f32_16x16x128_f8f6f4 v[114:117], v[2:9], v[192:199], v[114:117], v1, v1 op_sel_hi:[0,0,0]
	v_mfma_scale_f32_16x16x128_f8f6f4 v[130:133], v[2:9], v[184:191], v[130:133], v1, v1 op_sel_hi:[0,0,0]
	v_mfma_scale_f32_16x16x128_f8f6f4 v[146:149], v[2:9], v[170:177], v[146:149], v1, v1 op_sel_hi:[0,0,0]
	s_setprio 0
	s_barrier
	s_mov_b32 m0, s75
	v_lshl_add_u64 v[170:171], s[42:43], 0, v[164:165]
	ds_read_b128 v[184:187], v183 offset:16384
	ds_read_b128 v[188:191], v183 offset:17408
	ds_read_b128 v[192:195], v183 offset:18432
	ds_read_b128 v[196:199], v183 offset:19456
	ds_read_b128 v[200:203], v183 offset:20480
	ds_read_b128 v[204:207], v183 offset:21504
	ds_read_b128 v[208:211], v183 offset:22528
	ds_read_b128 v[212:215], v183 offset:23552
	global_load_lds_dwordx4 v[170:171], off
	v_lshl_add_u64 v[172:173], s[42:43], 0, v[162:163]
	s_mov_b32 m0, s72
	v_lshl_add_u64 v[174:175], s[44:45], 0, v[164:165]
	global_load_lds_dwordx4 v[172:173], off
	s_mov_b32 m0, s74
	v_lshl_add_u64 v[176:177], s[40:41], 0, v[162:163]
	global_load_lds_dwordx4 v[174:175], off
	v_lshl_add_u64 v[174:175], s[44:45], 0, v[162:163]
	s_mov_b32 m0, s73
	s_nop 0
	global_load_lds_dwordx4 v[174:175], off
	v_lshl_add_u64 v[174:175], s[40:41], 0, v[164:165]
	s_mov_b32 m0, s27
	s_nop 0
	global_load_lds_dwordx4 v[174:175], off
	s_mov_b32 m0, s49
	s_nop 0
	global_load_lds_dwordx4 v[176:177], off
	s_waitcnt vmcnt(8)
	s_waitcnt lgkmcnt(0)
	s_barrier
	s_setprio 1
	s_waitcnt lgkmcnt(0)
	v_mfma_scale_f32_16x16x128_f8f6f4 v[94:97], v[26:33], v[184:191], v[94:97], v1, v1 op_sel_hi:[0,0,0]
	v_mfma_scale_f32_16x16x128_f8f6f4 v[78:81], v[26:33], v[192:199], v[78:81], v1, v1 op_sel_hi:[0,0,0]
	v_mfma_scale_f32_16x16x128_f8f6f4 v[62:65], v[26:33], v[200:207], v[62:65], v1, v1 op_sel_hi:[0,0,0]
	v_mfma_scale_f32_16x16x128_f8f6f4 v[54:57], v[26:33], v[208:215], v[54:57], v1, v1 op_sel_hi:[0,0,0]
	v_mfma_scale_f32_16x16x128_f8f6f4 v[42:45], v[18:25], v[208:215], v[42:45], v1, v1 op_sel_hi:[0,0,0]
	v_mfma_scale_f32_16x16x128_f8f6f4 v[58:61], v[18:25], v[200:207], v[58:61], v1, v1 op_sel_hi:[0,0,0]
	v_mfma_scale_f32_16x16x128_f8f6f4 v[74:77], v[18:25], v[192:199], v[74:77], v1, v1 op_sel_hi:[0,0,0]
	v_mfma_scale_f32_16x16x128_f8f6f4 v[90:93], v[18:25], v[184:191], v[90:93], v1, v1 op_sel_hi:[0,0,0]
	s_setprio 0
	s_setprio 1
	v_mfma_scale_f32_16x16x128_f8f6f4 v[86:89], v[10:17], v[184:191], v[86:89], v1, v1 op_sel_hi:[0,0,0]
	v_mfma_scale_f32_16x16x128_f8f6f4 v[70:73], v[10:17], v[192:199], v[70:73], v1, v1 op_sel_hi:[0,0,0]
	v_mfma_scale_f32_16x16x128_f8f6f4 v[50:53], v[10:17], v[200:207], v[50:53], v1, v1 op_sel_hi:[0,0,0]
	v_mfma_scale_f32_16x16x128_f8f6f4 v[38:41], v[10:17], v[208:215], v[38:41], v1, v1 op_sel_hi:[0,0,0]
	v_mfma_scale_f32_16x16x128_f8f6f4 v[34:37], v[2:9], v[208:215], v[34:37], v1, v1 op_sel_hi:[0,0,0]
	v_mfma_scale_f32_16x16x128_f8f6f4 v[46:49], v[2:9], v[200:207], v[46:49], v1, v1 op_sel_hi:[0,0,0]
	v_mfma_scale_f32_16x16x128_f8f6f4 v[66:69], v[2:9], v[192:199], v[66:69], v1, v1 op_sel_hi:[0,0,0]
	v_mfma_scale_f32_16x16x128_f8f6f4 v[82:85], v[2:9], v[184:191], v[82:85], v1, v1 op_sel_hi:[0,0,0]
	s_setprio 0
	s_barrier
	v_add_u32_e32 v14, s71, v179
	v_add_u32_e32 v30, s70, v179
	ds_read_b128 v[2:5], v14
	ds_read_b128 v[6:9], v14 offset:1024
	ds_read_b128 v[10:13], v14 offset:2048
	ds_read_b128 v[14:17], v14 offset:3072
	ds_read_b128 v[18:21], v30
	ds_read_b128 v[22:25], v30 offset:1024
	ds_read_b128 v[26:29], v30 offset:2048
	ds_read_b128 v[30:33], v30 offset:3072
	s_mov_b32 m0, s50
	v_lshl_add_u64 v[216:217], s[38:39], 0, v[164:165]
	ds_read_b128 v[184:187], v183 offset:32768
	ds_read_b128 v[188:191], v183 offset:33792
	ds_read_b128 v[192:195], v183 offset:34816
	ds_read_b128 v[196:199], v183 offset:35840
	ds_read_b128 v[200:203], v183 offset:36864
	ds_read_b128 v[204:207], v183 offset:37888
	ds_read_b128 v[208:211], v183 offset:38912
	ds_read_b128 v[212:215], v183 offset:39936
	global_load_lds_dwordx4 v[216:217], off
	v_lshl_add_u64 v[216:217], s[38:39], 0, v[162:163]
	s_mov_b32 m0, s51
	s_nop 0
	global_load_lds_dwordx4 v[216:217], off
	s_waitcnt vmcnt(8)
	s_waitcnt lgkmcnt(0)
	s_barrier
	s_setprio 1
	s_waitcnt lgkmcnt(0)
	v_mfma_scale_f32_16x16x128_f8f6f4 v[158:161], v[2:9], v[184:191], v[158:161], v1, v1 op_sel_hi:[0,0,0]
	v_mfma_scale_f32_16x16x128_f8f6f4 v[142:145], v[2:9], v[192:199], v[142:145], v1, v1 op_sel_hi:[0,0,0]
	v_mfma_scale_f32_16x16x128_f8f6f4 v[126:129], v[2:9], v[200:207], v[126:129], v1, v1 op_sel_hi:[0,0,0]
	v_mfma_scale_f32_16x16x128_f8f6f4 v[110:113], v[2:9], v[208:215], v[110:113], v1, v1 op_sel_hi:[0,0,0]
	v_mfma_scale_f32_16x16x128_f8f6f4 v[106:109], v[10:17], v[208:215], v[106:109], v1, v1 op_sel_hi:[0,0,0]
	v_mfma_scale_f32_16x16x128_f8f6f4 v[122:125], v[10:17], v[200:207], v[122:125], v1, v1 op_sel_hi:[0,0,0]
	v_mfma_scale_f32_16x16x128_f8f6f4 v[138:141], v[10:17], v[192:199], v[138:141], v1, v1 op_sel_hi:[0,0,0]
	v_mfma_scale_f32_16x16x128_f8f6f4 v[154:157], v[10:17], v[184:191], v[154:157], v1, v1 op_sel_hi:[0,0,0]
	s_setprio 0
	s_setprio 1
	v_mfma_scale_f32_16x16x128_f8f6f4 v[150:153], v[18:25], v[184:191], v[150:153], v1, v1 op_sel_hi:[0,0,0]
	v_mfma_scale_f32_16x16x128_f8f6f4 v[134:137], v[18:25], v[192:199], v[134:137], v1, v1 op_sel_hi:[0,0,0]
	v_mfma_scale_f32_16x16x128_f8f6f4 v[118:121], v[18:25], v[200:207], v[118:121], v1, v1 op_sel_hi:[0,0,0]
	v_mfma_scale_f32_16x16x128_f8f6f4 v[102:105], v[18:25], v[208:215], v[102:105], v1, v1 op_sel_hi:[0,0,0]
	v_mfma_scale_f32_16x16x128_f8f6f4 v[98:101], v[26:33], v[208:215], v[98:101], v1, v1 op_sel_hi:[0,0,0]
	v_mfma_scale_f32_16x16x128_f8f6f4 v[114:117], v[26:33], v[200:207], v[114:117], v1, v1 op_sel_hi:[0,0,0]
	v_mfma_scale_f32_16x16x128_f8f6f4 v[130:133], v[26:33], v[192:199], v[130:133], v1, v1 op_sel_hi:[0,0,0]
	v_mfma_scale_f32_16x16x128_f8f6f4 v[146:149], v[26:33], v[184:191], v[146:149], v1, v1 op_sel_hi:[0,0,0]
	s_setprio 0
	s_barrier
	s_mov_b32 m0, s69
	v_lshl_add_u64 v[170:171], v[170:171], 0, s[8:9]
	ds_read_b128 v[184:187], v183 offset:49152
	ds_read_b128 v[188:191], v183 offset:50176
	ds_read_b128 v[192:195], v183 offset:51200
	ds_read_b128 v[196:199], v183 offset:52224
	ds_read_b128 v[200:203], v183 offset:53248
	ds_read_b128 v[204:207], v183 offset:54272
	ds_read_b128 v[208:211], v183 offset:55296
	ds_read_b128 v[212:215], v183 offset:56320
	global_load_lds_dwordx4 v[170:171], off
	v_lshl_add_u64 v[170:171], v[172:173], 0, s[8:9]
	s_mov_b32 m0, s67
	s_nop 0
	global_load_lds_dwordx4 v[170:171], off
	v_lshl_add_u64 v[170:171], s[36:37], 0, v[164:165]
	s_mov_b32 m0, s68
	s_nop 0
	global_load_lds_dwordx4 v[170:171], off
	v_lshl_add_u64 v[170:171], s[36:37], 0, v[162:163]
	s_mov_b32 m0, s66
	s_nop 0
	global_load_lds_dwordx4 v[170:171], off
	v_lshl_add_u64 v[170:171], v[174:175], 0, s[8:9]
	s_mov_b32 m0, s61
	s_nop 0
	global_load_lds_dwordx4 v[170:171], off
	v_lshl_add_u64 v[170:171], v[176:177], 0, s[8:9]
	s_mov_b32 m0, s62
	s_nop 0
	global_load_lds_dwordx4 v[170:171], off
	s_waitcnt vmcnt(8)
	s_waitcnt lgkmcnt(0)
	s_barrier
	s_setprio 1
	s_waitcnt lgkmcnt(0)
	v_mfma_scale_f32_16x16x128_f8f6f4 v[94:97], v[2:9], v[184:191], v[94:97], v1, v1 op_sel_hi:[0,0,0]
	v_mfma_scale_f32_16x16x128_f8f6f4 v[78:81], v[2:9], v[192:199], v[78:81], v1, v1 op_sel_hi:[0,0,0]
	v_mfma_scale_f32_16x16x128_f8f6f4 v[62:65], v[2:9], v[200:207], v[62:65], v1, v1 op_sel_hi:[0,0,0]
	v_mfma_scale_f32_16x16x128_f8f6f4 v[54:57], v[2:9], v[208:215], v[54:57], v1, v1 op_sel_hi:[0,0,0]
	v_mfma_scale_f32_16x16x128_f8f6f4 v[42:45], v[10:17], v[208:215], v[42:45], v1, v1 op_sel_hi:[0,0,0]
	v_mfma_scale_f32_16x16x128_f8f6f4 v[58:61], v[10:17], v[200:207], v[58:61], v1, v1 op_sel_hi:[0,0,0]
	v_mfma_scale_f32_16x16x128_f8f6f4 v[74:77], v[10:17], v[192:199], v[74:77], v1, v1 op_sel_hi:[0,0,0]
	v_mfma_scale_f32_16x16x128_f8f6f4 v[90:93], v[10:17], v[184:191], v[90:93], v1, v1 op_sel_hi:[0,0,0]
	s_setprio 0
	s_setprio 1
	v_mfma_scale_f32_16x16x128_f8f6f4 v[86:89], v[18:25], v[184:191], v[86:89], v1, v1 op_sel_hi:[0,0,0]
	v_mfma_scale_f32_16x16x128_f8f6f4 v[70:73], v[18:25], v[192:199], v[70:73], v1, v1 op_sel_hi:[0,0,0]
	v_mfma_scale_f32_16x16x128_f8f6f4 v[50:53], v[18:25], v[200:207], v[50:53], v1, v1 op_sel_hi:[0,0,0]
	v_mfma_scale_f32_16x16x128_f8f6f4 v[38:41], v[18:25], v[208:215], v[38:41], v1, v1 op_sel_hi:[0,0,0]
	v_mfma_scale_f32_16x16x128_f8f6f4 v[34:37], v[26:33], v[208:215], v[34:37], v1, v1 op_sel_hi:[0,0,0]
	v_mfma_scale_f32_16x16x128_f8f6f4 v[46:49], v[26:33], v[200:207], v[46:49], v1, v1 op_sel_hi:[0,0,0]
	v_mfma_scale_f32_16x16x128_f8f6f4 v[66:69], v[26:33], v[192:199], v[66:69], v1, v1 op_sel_hi:[0,0,0]
	v_mfma_scale_f32_16x16x128_f8f6f4 v[82:85], v[26:33], v[184:191], v[82:85], v1, v1 op_sel_hi:[0,0,0]
	s_setprio 0
	s_barrier
	s_movk_i32 s38, 0x100
	s_andn2_b64 vcc, exec, s[34:35]
	s_mov_b64 s[36:37], -1
	s_mov_b64 s[34:35], 0
	s_cbranch_vccz .LBB0_1558
	s_and_b64 vcc, exec, s[12:13]
	s_cbranch_vccz .LBB0_1561
	s_barrier

.LBB0_1681:
	ds_read_b128 v[26:29], v189
	ds_read_b128 v[30:33], v189 offset:1024
	ds_read_b128 v[18:21], v189 offset:2048
	ds_read_b128 v[22:25], v189 offset:3072
	ds_read_b128 v[10:13], v190
	ds_read_b128 v[14:17], v190 offset:1024
	ds_read_b128 v[2:5], v190 offset:2048
	ds_read_b128 v[6:9], v190 offset:3072
	s_add_u32 s34, s30, 0xfff80080
	s_addc_u32 s35, s31, -1
	s_cmp_eq_u32 s60, 28
	s_cselect_b32 s37, s18, s35
	s_cselect_b32 s36, s19, s34
	s_cselect_b32 s35, s21, s59
	s_cselect_b32 s34, s23, s58
	s_mov_b32 m0, s43
	s_nop 0
	global_load_lds_dwordx4 v168, s[100:101]
	s_mov_b32 m0, s44
	s_nop 0
	global_load_lds_dwordx4 v164, s[100:101]
	s_add_i32 m0, s29, 0xc000
	ds_read_b128 v[178:181], v191
	ds_read_b128 v[182:185], v191 offset:1024
	ds_read_b128 v[194:197], v191 offset:2048
	ds_read_b128 v[198:201], v191 offset:3072
	ds_read_b128 v[202:205], v191 offset:4096
	ds_read_b128 v[206:209], v191 offset:5120
	ds_read_b128 v[210:213], v191 offset:6144
	ds_read_b128 v[214:217], v191 offset:7168
	global_load_lds_dwordx4 v170, s[30:31]
	s_add_i32 m0, s29, 0xe000
	s_nop 0
	global_load_lds_dwordx4 v172, s[30:31]
	s_waitcnt vmcnt(8)
	s_waitcnt lgkmcnt(0)
	s_barrier
	s_setprio 1
	s_waitcnt lgkmcnt(0)
	v_mfma_scale_f32_16x16x128_f8f6f4 v[158:161], v[26:33], v[178:185], v[158:161], v1, v1 op_sel_hi:[0,0,0]
	v_mfma_scale_f32_16x16x128_f8f6f4 v[142:145], v[26:33], v[194:201], v[142:145], v1, v1 op_sel_hi:[0,0,0]
	v_mfma_scale_f32_16x16x128_f8f6f4 v[126:129], v[26:33], v[202:209], v[126:129], v1, v1 op_sel_hi:[0,0,0]
	v_mfma_scale_f32_16x16x128_f8f6f4 v[110:113], v[26:33], v[210:217], v[110:113], v1, v1 op_sel_hi:[0,0,0]
	v_mfma_scale_f32_16x16x128_f8f6f4 v[106:109], v[18:25], v[210:217], v[106:109], v1, v1 op_sel_hi:[0,0,0]
	v_mfma_scale_f32_16x16x128_f8f6f4 v[122:125], v[18:25], v[202:209], v[122:125], v1, v1 op_sel_hi:[0,0,0]
	v_mfma_scale_f32_16x16x128_f8f6f4 v[138:141], v[18:25], v[194:201], v[138:141], v1, v1 op_sel_hi:[0,0,0]
	v_mfma_scale_f32_16x16x128_f8f6f4 v[154:157], v[18:25], v[178:185], v[154:157], v1, v1 op_sel_hi:[0,0,0]
	s_setprio 0
	s_setprio 1
	v_mfma_scale_f32_16x16x128_f8f6f4 v[150:153], v[10:17], v[178:185], v[150:153], v1, v1 op_sel_hi:[0,0,0]
	v_mfma_scale_f32_16x16x128_f8f6f4 v[134:137], v[10:17], v[194:201], v[134:137], v1, v1 op_sel_hi:[0,0,0]
	v_mfma_scale_f32_16x16x128_f8f6f4 v[118:121], v[10:17], v[202:209], v[118:121], v1, v1 op_sel_hi:[0,0,0]
	v_mfma_scale_f32_16x16x128_f8f6f4 v[102:105], v[10:17], v[210:217], v[102:105], v1, v1 op_sel_hi:[0,0,0]
	v_mfma_scale_f32_16x16x128_f8f6f4 v[98:101], v[2:9], v[210:217], v[98:101], v1, v1 op_sel_hi:[0,0,0]
	v_mfma_scale_f32_16x16x128_f8f6f4 v[114:117], v[2:9], v[202:209], v[114:117], v1, v1 op_sel_hi:[0,0,0]
	v_mfma_scale_f32_16x16x128_f8f6f4 v[130:133], v[2:9], v[194:201], v[130:133], v1, v1 op_sel_hi:[0,0,0]
	v_mfma_scale_f32_16x16x128_f8f6f4 v[146:149], v[2:9], v[178:185], v[146:149], v1, v1 op_sel_hi:[0,0,0]
	s_setprio 0
	s_barrier
	s_add_i32 s61, s45, s3
	s_mov_b32 m0, s61
	ds_read_b128 v[194:197], v191 offset:16384
	ds_read_b128 v[198:201], v191 offset:17408
	ds_read_b128 v[202:205], v191 offset:18432
	ds_read_b128 v[206:209], v191 offset:19456
	ds_read_b128 v[210:213], v191 offset:20480
	ds_read_b128 v[214:217], v191 offset:21504
	ds_read_b128 v[218:221], v191 offset:22528
	ds_read_b128 v[222:225], v191 offset:23552
	global_load_lds_dwordx4 v166, s[34:35]
	s_add_i32 m0, s61, 0x2000
	s_add_u32 s62, s34, 0x80000
	s_addc_u32 s63, s35, 0
	s_add_i32 s61, s48, s3
	global_load_lds_dwordx4 v162, s[34:35]
	s_mov_b32 m0, s61
	s_nop 0
	global_load_lds_dwordx4 v166, s[62:63]
	s_add_i32 m0, s61, 0x2000
	s_nop 0
	global_load_lds_dwordx4 v162, s[62:63]
	s_waitcnt vmcnt(6)
	s_waitcnt lgkmcnt(0)
	s_barrier
	s_setprio 1
	s_waitcnt lgkmcnt(0)
	v_mfma_scale_f32_16x16x128_f8f6f4 v[94:97], v[26:33], v[194:201], v[94:97], v1, v1 op_sel_hi:[0,0,0]
	v_mfma_scale_f32_16x16x128_f8f6f4 v[78:81], v[26:33], v[202:209], v[78:81], v1, v1 op_sel_hi:[0,0,0]
	v_mfma_scale_f32_16x16x128_f8f6f4 v[62:65], v[26:33], v[210:217], v[62:65], v1, v1 op_sel_hi:[0,0,0]
	v_mfma_scale_f32_16x16x128_f8f6f4 v[46:49], v[26:33], v[218:225], v[46:49], v1, v1 op_sel_hi:[0,0,0]
	v_mfma_scale_f32_16x16x128_f8f6f4 v[42:45], v[18:25], v[218:225], v[42:45], v1, v1 op_sel_hi:[0,0,0]
	v_mfma_scale_f32_16x16x128_f8f6f4 v[58:61], v[18:25], v[210:217], v[58:61], v1, v1 op_sel_hi:[0,0,0]
	v_mfma_scale_f32_16x16x128_f8f6f4 v[74:77], v[18:25], v[202:209], v[74:77], v1, v1 op_sel_hi:[0,0,0]
	v_mfma_scale_f32_16x16x128_f8f6f4 v[90:93], v[18:25], v[194:201], v[90:93], v1, v1 op_sel_hi:[0,0,0]
	s_setprio 0
	s_setprio 1
	v_mfma_scale_f32_16x16x128_f8f6f4 v[86:89], v[10:17], v[194:201], v[86:89], v1, v1 op_sel_hi:[0,0,0]
	v_mfma_scale_f32_16x16x128_f8f6f4 v[70:73], v[10:17], v[202:209], v[70:73], v1, v1 op_sel_hi:[0,0,0]
	v_mfma_scale_f32_16x16x128_f8f6f4 v[54:57], v[10:17], v[210:217], v[54:57], v1, v1 op_sel_hi:[0,0,0]
	v_mfma_scale_f32_16x16x128_f8f6f4 v[38:41], v[10:17], v[218:225], v[38:41], v1, v1 op_sel_hi:[0,0,0]
	v_mfma_scale_f32_16x16x128_f8f6f4 v[34:37], v[2:9], v[218:225], v[34:37], v1, v1 op_sel_hi:[0,0,0]
	v_mfma_scale_f32_16x16x128_f8f6f4 v[50:53], v[2:9], v[210:217], v[50:53], v1, v1 op_sel_hi:[0,0,0]
	v_mfma_scale_f32_16x16x128_f8f6f4 v[66:69], v[2:9], v[202:209], v[66:69], v1, v1 op_sel_hi:[0,0,0]
	v_mfma_scale_f32_16x16x128_f8f6f4 v[82:85], v[2:9], v[194:201], v[82:85], v1, v1 op_sel_hi:[0,0,0]
	s_setprio 0
	s_barrier
	s_add_i32 s61, 0, 0x18000
	s_add_i32 s62, 0, 0x1c000
	v_add_u32_e32 v14, s61, v187
	v_add_u32_e32 v30, s62, v187
	ds_read_b128 v[2:5], v14
	ds_read_b128 v[6:9], v14 offset:1024
	ds_read_b128 v[10:13], v14 offset:2048
	ds_read_b128 v[14:17], v14 offset:3072
	ds_read_b128 v[18:21], v30
	ds_read_b128 v[22:25], v30 offset:1024
	ds_read_b128 v[26:29], v30 offset:2048
	ds_read_b128 v[30:33], v30 offset:3072
	s_mov_b32 m0, s29
	s_nop 0
	global_load_lds_dwordx4 v168, s[36:37]
	s_mov_b32 m0, s38
	s_nop 0
	global_load_lds_dwordx4 v164, s[36:37]
	s_add_u32 s36, s36, 0x80000
	s_addc_u32 s37, s37, 0
	s_add_u32 s100, s36, 0xfff80080
	s_addc_u32 s101, s37, -1
	s_mov_b32 m0, s39
	ds_read_b128 v[194:197], v191 offset:32768
	ds_read_b128 v[198:201], v191 offset:33792
	ds_read_b128 v[202:205], v191 offset:34816
	ds_read_b128 v[206:209], v191 offset:35840
	ds_read_b128 v[210:213], v191 offset:36864
	ds_read_b128 v[214:217], v191 offset:37888
	ds_read_b128 v[218:221], v191 offset:38912
	ds_read_b128 v[222:225], v191 offset:39936
	global_load_lds_dwordx4 v168, s[36:37]
	s_mov_b32 m0, s40
	s_nop 0
	global_load_lds_dwordx4 v164, s[36:37]
	s_waitcnt vmcnt(8)
	s_waitcnt lgkmcnt(0)
	s_barrier
	s_setprio 1
	s_waitcnt lgkmcnt(0)
	v_mfma_scale_f32_16x16x128_f8f6f4 v[158:161], v[2:9], v[194:201], v[158:161], v1, v1 op_sel_hi:[0,0,0]
	v_mfma_scale_f32_16x16x128_f8f6f4 v[142:145], v[2:9], v[202:209], v[142:145], v1, v1 op_sel_hi:[0,0,0]
	v_mfma_scale_f32_16x16x128_f8f6f4 v[126:129], v[2:9], v[210:217], v[126:129], v1, v1 op_sel_hi:[0,0,0]
	v_mfma_scale_f32_16x16x128_f8f6f4 v[110:113], v[2:9], v[218:225], v[110:113], v1, v1 op_sel_hi:[0,0,0]
	v_mfma_scale_f32_16x16x128_f8f6f4 v[106:109], v[10:17], v[218:225], v[106:109], v1, v1 op_sel_hi:[0,0,0]
	v_mfma_scale_f32_16x16x128_f8f6f4 v[122:125], v[10:17], v[210:217], v[122:125], v1, v1 op_sel_hi:[0,0,0]
	v_mfma_scale_f32_16x16x128_f8f6f4 v[138:141], v[10:17], v[202:209], v[138:141], v1, v1 op_sel_hi:[0,0,0]
	v_mfma_scale_f32_16x16x128_f8f6f4 v[154:157], v[10:17], v[194:201], v[154:157], v1, v1 op_sel_hi:[0,0,0]
	s_setprio 0
	s_setprio 1
	v_mfma_scale_f32_16x16x128_f8f6f4 v[150:153], v[18:25], v[194:201], v[150:153], v1, v1 op_sel_hi:[0,0,0]
	v_mfma_scale_f32_16x16x128_f8f6f4 v[134:137], v[18:25], v[202:209], v[134:137], v1, v1 op_sel_hi:[0,0,0]
	v_mfma_scale_f32_16x16x128_f8f6f4 v[118:121], v[18:25], v[210:217], v[118:121], v1, v1 op_sel_hi:[0,0,0]
	v_mfma_scale_f32_16x16x128_f8f6f4 v[102:105], v[18:25], v[218:225], v[102:105], v1, v1 op_sel_hi:[0,0,0]
	v_mfma_scale_f32_16x16x128_f8f6f4 v[98:101], v[26:33], v[218:225], v[98:101], v1, v1 op_sel_hi:[0,0,0]
	v_mfma_scale_f32_16x16x128_f8f6f4 v[114:117], v[26:33], v[210:217], v[114:117], v1, v1 op_sel_hi:[0,0,0]
	v_mfma_scale_f32_16x16x128_f8f6f4 v[130:133], v[26:33], v[202:209], v[130:133], v1, v1 op_sel_hi:[0,0,0]
	v_mfma_scale_f32_16x16x128_f8f6f4 v[146:149], v[26:33], v[194:201], v[146:149], v1, v1 op_sel_hi:[0,0,0]
	s_setprio 0
	s_barrier
	s_add_i32 s36, s61, s3
	s_mov_b32 m0, s36
	s_add_u32 s98, s34, 0x80
	s_addc_u32 s99, s35, 0
	ds_read_b128 v[194:197], v191 offset:49152
	ds_read_b128 v[198:201], v191 offset:50176
	ds_read_b128 v[202:205], v191 offset:51200
	ds_read_b128 v[206:209], v191 offset:52224
	ds_read_b128 v[210:213], v191 offset:53248
	ds_read_b128 v[214:217], v191 offset:54272
	ds_read_b128 v[218:221], v191 offset:55296
	ds_read_b128 v[222:225], v191 offset:56320
	global_load_lds_dwordx4 v166, s[98:99]
	s_add_i32 m0, s36, 0x2000
	s_add_u32 s34, s34, 0x80080
	s_addc_u32 s35, s35, 0
	s_add_i32 s36, s62, s3
	global_load_lds_dwordx4 v162, s[98:99]
	s_mov_b32 m0, s36
	s_nop 0
	global_load_lds_dwordx4 v166, s[34:35]
	s_add_i32 m0, s36, 0x2000
	s_nop 0
	global_load_lds_dwordx4 v162, s[34:35]
	s_waitcnt vmcnt(6)
	s_waitcnt lgkmcnt(0)
	s_barrier
	s_setprio 1
	s_waitcnt lgkmcnt(0)
	v_mfma_scale_f32_16x16x128_f8f6f4 v[94:97], v[2:9], v[194:201], v[94:97], v1, v1 op_sel_hi:[0,0,0]
	v_mfma_scale_f32_16x16x128_f8f6f4 v[78:81], v[2:9], v[202:209], v[78:81], v1, v1 op_sel_hi:[0,0,0]
	v_mfma_scale_f32_16x16x128_f8f6f4 v[62:65], v[2:9], v[210:217], v[62:65], v1, v1 op_sel_hi:[0,0,0]
	v_mfma_scale_f32_16x16x128_f8f6f4 v[46:49], v[2:9], v[218:225], v[46:49], v1, v1 op_sel_hi:[0,0,0]
	v_mfma_scale_f32_16x16x128_f8f6f4 v[42:45], v[10:17], v[218:225], v[42:45], v1, v1 op_sel_hi:[0,0,0]
	v_mfma_scale_f32_16x16x128_f8f6f4 v[58:61], v[10:17], v[210:217], v[58:61], v1, v1 op_sel_hi:[0,0,0]
	v_mfma_scale_f32_16x16x128_f8f6f4 v[74:77], v[10:17], v[202:209], v[74:77], v1, v1 op_sel_hi:[0,0,0]
	v_mfma_scale_f32_16x16x128_f8f6f4 v[90:93], v[10:17], v[194:201], v[90:93], v1, v1 op_sel_hi:[0,0,0]
	s_setprio 0
	s_setprio 1
	v_mfma_scale_f32_16x16x128_f8f6f4 v[86:89], v[18:25], v[194:201], v[86:89], v1, v1 op_sel_hi:[0,0,0]
	v_mfma_scale_f32_16x16x128_f8f6f4 v[70:73], v[18:25], v[202:209], v[70:73], v1, v1 op_sel_hi:[0,0,0]
	v_mfma_scale_f32_16x16x128_f8f6f4 v[54:57], v[18:25], v[210:217], v[54:57], v1, v1 op_sel_hi:[0,0,0]
	v_mfma_scale_f32_16x16x128_f8f6f4 v[38:41], v[18:25], v[218:225], v[38:41], v1, v1 op_sel_hi:[0,0,0]
	v_mfma_scale_f32_16x16x128_f8f6f4 v[34:37], v[26:33], v[218:225], v[34:37], v1, v1 op_sel_hi:[0,0,0]
	v_mfma_scale_f32_16x16x128_f8f6f4 v[50:53], v[26:33], v[210:217], v[50:53], v1, v1 op_sel_hi:[0,0,0]
	v_mfma_scale_f32_16x16x128_f8f6f4 v[66:69], v[26:33], v[202:209], v[66:69], v1, v1 op_sel_hi:[0,0,0]
	v_mfma_scale_f32_16x16x128_f8f6f4 v[82:85], v[26:33], v[194:201], v[82:85], v1, v1 op_sel_hi:[0,0,0]
	s_setprio 0
	s_barrier
	s_add_i32 s60, s60, 2
	s_add_u32 s30, s30, 0x100
	s_addc_u32 s31, s31, 0
	s_add_u32 s58, s58, 0x100
	s_addc_u32 s59, s59, 0
	s_cmp_gt_u32 s60, 29
	s_cbranch_scc0 .LBB0_1681
	s_and_b64 vcc, exec, s[12:13]
	s_cbranch_vccz .LBB0_1684
	s_barrier

.LBB0_1745:
	s_add_u32 s8, s49, s6
	s_addc_u32 s9, s50, s7
	s_add_u32 s8, s8, 0x32800100
	s_addc_u32 s9, s9, 0
	s_add_u32 s73, s51, s6
	s_addc_u32 s74, s54, s7
	s_add_i32 s72, 0, 0x10000
	s_cmpk_eq_i32 s6, 0x2a00
	s_cselect_b32 s37, s5, s9
	s_cselect_b32 s36, s4, s8
	s_cselect_b32 s9, s13, s74
	s_cselect_b32 s8, s12, s73
	s_add_i32 s73, 0, 0x14000
	v_add_u32_e32 v2, s72, v188
	v_add_u32_e32 v6, s73, v188
	ds_read_b128 v[26:29], v2
	ds_read_b128 v[30:33], v2 offset:1024
	ds_read_b128 v[18:21], v2 offset:2048
	ds_read_b128 v[22:25], v2 offset:3072
	ds_read_b128 v[10:13], v6
	ds_read_b128 v[14:17], v6 offset:1024
	ds_read_b128 v[2:5], v6 offset:2048
	ds_read_b128 v[6:9], v6 offset:3072
	v_lshl_add_u64 v[214:215], v[168:169], 0, s[6:7]
	s_add_i32 m0, s64, 0xc000
	ds_read_b128 v[172:175], v189
	ds_read_b128 v[176:179], v189 offset:1024
	ds_read_b128 v[190:193], v189 offset:2048
	ds_read_b128 v[194:197], v189 offset:3072
	ds_read_b128 v[198:201], v189 offset:4096
	ds_read_b128 v[202:205], v189 offset:5120
	ds_read_b128 v[206:209], v189 offset:6144
	ds_read_b128 v[210:213], v189 offset:7168
	global_load_lds_dwordx4 v[214:215], off
	v_lshl_add_u64 v[214:215], v[170:171], 0, s[6:7]
	s_add_i32 m0, s64, 0xe000
	s_nop 0
	global_load_lds_dwordx4 v[214:215], off
	s_waitcnt vmcnt(8)
	s_waitcnt lgkmcnt(0)
	s_barrier
	s_setprio 1
	s_waitcnt lgkmcnt(0)
	v_mfma_scale_f32_16x16x128_f8f6f4 v[158:161], v[26:33], v[172:179], v[158:161], v187, v187 op_sel_hi:[0,0,0]
	v_mfma_scale_f32_16x16x128_f8f6f4 v[122:125], v[26:33], v[190:197], v[122:125], v187, v187 op_sel_hi:[0,0,0]
	v_mfma_scale_f32_16x16x128_f8f6f4 v[126:129], v[26:33], v[198:205], v[126:129], v187, v187 op_sel_hi:[0,0,0]
	v_mfma_scale_f32_16x16x128_f8f6f4 v[110:113], v[26:33], v[206:213], v[110:113], v187, v187 op_sel_hi:[0,0,0]
	v_mfma_scale_f32_16x16x128_f8f6f4 v[106:109], v[18:25], v[206:213], v[106:109], v187, v187 op_sel_hi:[0,0,0]
	v_mfma_scale_f32_16x16x128_f8f6f4 v[114:117], v[18:25], v[198:205], v[114:117], v187, v187 op_sel_hi:[0,0,0]
	v_mfma_scale_f32_16x16x128_f8f6f4 v[118:121], v[18:25], v[190:197], v[118:121], v187, v187 op_sel_hi:[0,0,0]
	v_mfma_scale_f32_16x16x128_f8f6f4 v[154:157], v[18:25], v[172:179], v[154:157], v187, v187 op_sel_hi:[0,0,0]
	s_setprio 0
	s_setprio 1
	v_mfma_scale_f32_16x16x128_f8f6f4 v[150:153], v[10:17], v[172:179], v[150:153], v187, v187 op_sel_hi:[0,0,0]
	v_mfma_scale_f32_16x16x128_f8f6f4 v[142:145], v[10:17], v[190:197], v[142:145], v187, v187 op_sel_hi:[0,0,0]
	v_mfma_scale_f32_16x16x128_f8f6f4 v[134:137], v[10:17], v[198:205], v[134:137], v187, v187 op_sel_hi:[0,0,0]
	v_mfma_scale_f32_16x16x128_f8f6f4 v[102:105], v[10:17], v[206:213], v[102:105], v187, v187 op_sel_hi:[0,0,0]
	v_mfma_scale_f32_16x16x128_f8f6f4 v[98:101], v[2:9], v[206:213], v[98:101], v187, v187 op_sel_hi:[0,0,0]
	v_mfma_scale_f32_16x16x128_f8f6f4 v[130:133], v[2:9], v[198:205], v[130:133], v187, v187 op_sel_hi:[0,0,0]
	v_mfma_scale_f32_16x16x128_f8f6f4 v[138:141], v[2:9], v[190:197], v[138:141], v187, v187 op_sel_hi:[0,0,0]
	v_mfma_scale_f32_16x16x128_f8f6f4 v[146:149], v[2:9], v[172:179], v[146:149], v187, v187 op_sel_hi:[0,0,0]
	s_setprio 0
	s_barrier
	s_add_i32 s72, s72, s43
	v_lshl_add_u64 v[172:173], s[8:9], 0, v[162:163]
	s_mov_b32 m0, s72
	ds_read_b128 v[190:193], v189 offset:16384
	ds_read_b128 v[194:197], v189 offset:17408
	ds_read_b128 v[198:201], v189 offset:18432
	ds_read_b128 v[202:205], v189 offset:19456
	ds_read_b128 v[206:209], v189 offset:20480
	ds_read_b128 v[210:213], v189 offset:21504
	ds_read_b128 v[214:217], v189 offset:22528
	ds_read_b128 v[218:221], v189 offset:23552
	global_load_lds_dwordx4 v[172:173], off
	s_add_i32 m0, s72, 0x2000
	s_add_u32 s74, s8, 0x158000
	v_lshl_add_u64 v[174:175], s[8:9], 0, v[166:167]
	s_addc_u32 s75, s9, 0
	s_add_i32 s72, s73, s43
	global_load_lds_dwordx4 v[174:175], off
	v_lshl_add_u64 v[176:177], s[74:75], 0, v[162:163]
	s_mov_b32 m0, s72
	v_lshl_add_u64 v[178:179], s[36:37], 0, v[166:167]
	global_load_lds_dwordx4 v[176:177], off
	v_lshl_add_u64 v[176:177], s[74:75], 0, v[166:167]
	s_add_i32 m0, s72, 0x2000
	s_nop 0
	global_load_lds_dwordx4 v[176:177], off
	v_lshl_add_u64 v[176:177], s[36:37], 0, v[162:163]
	s_mov_b32 m0, s64
	s_nop 0
	global_load_lds_dwordx4 v[176:177], off
	s_mov_b32 m0, s65
	s_nop 0
	global_load_lds_dwordx4 v[178:179], off
	s_waitcnt vmcnt(8)
	s_waitcnt lgkmcnt(0)
	s_barrier
	s_setprio 1
	s_waitcnt lgkmcnt(0)
	v_mfma_scale_f32_16x16x128_f8f6f4 v[94:97], v[26:33], v[190:197], v[94:97], v187, v187 op_sel_hi:[0,0,0]
	v_mfma_scale_f32_16x16x128_f8f6f4 v[78:81], v[26:33], v[198:205], v[78:81], v187, v187 op_sel_hi:[0,0,0]
	v_mfma_scale_f32_16x16x128_f8f6f4 v[62:65], v[26:33], v[206:213], v[62:65], v187, v187 op_sel_hi:[0,0,0]
	v_mfma_scale_f32_16x16x128_f8f6f4 v[46:49], v[26:33], v[214:221], v[46:49], v187, v187 op_sel_hi:[0,0,0]
	v_mfma_scale_f32_16x16x128_f8f6f4 v[42:45], v[18:25], v[214:221], v[42:45], v187, v187 op_sel_hi:[0,0,0]
	v_mfma_scale_f32_16x16x128_f8f6f4 v[58:61], v[18:25], v[206:213], v[58:61], v187, v187 op_sel_hi:[0,0,0]
	v_mfma_scale_f32_16x16x128_f8f6f4 v[74:77], v[18:25], v[198:205], v[74:77], v187, v187 op_sel_hi:[0,0,0]
	v_mfma_scale_f32_16x16x128_f8f6f4 v[90:93], v[18:25], v[190:197], v[90:93], v187, v187 op_sel_hi:[0,0,0]
	s_setprio 0
	s_setprio 1
	v_mfma_scale_f32_16x16x128_f8f6f4 v[86:89], v[10:17], v[190:197], v[86:89], v187, v187 op_sel_hi:[0,0,0]
	v_mfma_scale_f32_16x16x128_f8f6f4 v[70:73], v[10:17], v[198:205], v[70:73], v187, v187 op_sel_hi:[0,0,0]
	v_mfma_scale_f32_16x16x128_f8f6f4 v[54:57], v[10:17], v[206:213], v[54:57], v187, v187 op_sel_hi:[0,0,0]
	v_mfma_scale_f32_16x16x128_f8f6f4 v[38:41], v[10:17], v[214:221], v[38:41], v187, v187 op_sel_hi:[0,0,0]
	v_mfma_scale_f32_16x16x128_f8f6f4 v[34:37], v[2:9], v[214:221], v[34:37], v187, v187 op_sel_hi:[0,0,0]
	v_mfma_scale_f32_16x16x128_f8f6f4 v[50:53], v[2:9], v[206:213], v[50:53], v187, v187 op_sel_hi:[0,0,0]
	v_mfma_scale_f32_16x16x128_f8f6f4 v[66:69], v[2:9], v[198:205], v[66:69], v187, v187 op_sel_hi:[0,0,0]
	v_mfma_scale_f32_16x16x128_f8f6f4 v[82:85], v[2:9], v[190:197], v[82:85], v187, v187 op_sel_hi:[0,0,0]
	s_setprio 0
	s_barrier
	s_add_i32 s72, 0, 0x18000
	s_add_i32 s73, 0, 0x1c000
	v_add_u32_e32 v14, s72, v188
	v_add_u32_e32 v30, s73, v188
	ds_read_b128 v[2:5], v14
	ds_read_b128 v[6:9], v14 offset:1024
	ds_read_b128 v[10:13], v14 offset:2048
	ds_read_b128 v[14:17], v14 offset:3072
	ds_read_b128 v[18:21], v30
	ds_read_b128 v[22:25], v30 offset:1024
	ds_read_b128 v[26:29], v30 offset:2048
	ds_read_b128 v[30:33], v30 offset:3072
	s_add_u32 s36, s36, 0x158000
	s_addc_u32 s37, s37, 0
	s_mov_b32 m0, s66
	v_lshl_add_u64 v[222:223], s[36:37], 0, v[162:163]
	ds_read_b128 v[190:193], v189 offset:32768
	ds_read_b128 v[194:197], v189 offset:33792
	ds_read_b128 v[198:201], v189 offset:34816
	ds_read_b128 v[202:205], v189 offset:35840
	ds_read_b128 v[206:209], v189 offset:36864
	ds_read_b128 v[210:213], v189 offset:37888
	ds_read_b128 v[214:217], v189 offset:38912
	ds_read_b128 v[218:221], v189 offset:39936
	global_load_lds_dwordx4 v[222:223], off
	v_lshl_add_u64 v[222:223], s[36:37], 0, v[166:167]
	s_mov_b32 m0, s67
	s_nop 0
	global_load_lds_dwordx4 v[222:223], off
	s_waitcnt vmcnt(8)
	s_waitcnt lgkmcnt(0)
	s_barrier
	s_setprio 1
	s_waitcnt lgkmcnt(0)
	v_mfma_scale_f32_16x16x128_f8f6f4 v[158:161], v[2:9], v[190:197], v[158:161], v187, v187 op_sel_hi:[0,0,0]
	v_mfma_scale_f32_16x16x128_f8f6f4 v[122:125], v[2:9], v[198:205], v[122:125], v187, v187 op_sel_hi:[0,0,0]
	v_mfma_scale_f32_16x16x128_f8f6f4 v[126:129], v[2:9], v[206:213], v[126:129], v187, v187 op_sel_hi:[0,0,0]
	v_mfma_scale_f32_16x16x128_f8f6f4 v[110:113], v[2:9], v[214:221], v[110:113], v187, v187 op_sel_hi:[0,0,0]
	v_mfma_scale_f32_16x16x128_f8f6f4 v[106:109], v[10:17], v[214:221], v[106:109], v187, v187 op_sel_hi:[0,0,0]
	v_mfma_scale_f32_16x16x128_f8f6f4 v[114:117], v[10:17], v[206:213], v[114:117], v187, v187 op_sel_hi:[0,0,0]
	v_mfma_scale_f32_16x16x128_f8f6f4 v[118:121], v[10:17], v[198:205], v[118:121], v187, v187 op_sel_hi:[0,0,0]
	v_mfma_scale_f32_16x16x128_f8f6f4 v[154:157], v[10:17], v[190:197], v[154:157], v187, v187 op_sel_hi:[0,0,0]
	s_setprio 0
	s_setprio 1
	v_mfma_scale_f32_16x16x128_f8f6f4 v[150:153], v[18:25], v[190:197], v[150:153], v187, v187 op_sel_hi:[0,0,0]
	v_mfma_scale_f32_16x16x128_f8f6f4 v[142:145], v[18:25], v[198:205], v[142:145], v187, v187 op_sel_hi:[0,0,0]
	v_mfma_scale_f32_16x16x128_f8f6f4 v[134:137], v[18:25], v[206:213], v[134:137], v187, v187 op_sel_hi:[0,0,0]
	v_mfma_scale_f32_16x16x128_f8f6f4 v[102:105], v[18:25], v[214:221], v[102:105], v187, v187 op_sel_hi:[0,0,0]
	v_mfma_scale_f32_16x16x128_f8f6f4 v[98:101], v[26:33], v[214:221], v[98:101], v187, v187 op_sel_hi:[0,0,0]
	v_mfma_scale_f32_16x16x128_f8f6f4 v[130:133], v[26:33], v[206:213], v[130:133], v187, v187 op_sel_hi:[0,0,0]
	v_mfma_scale_f32_16x16x128_f8f6f4 v[138:141], v[26:33], v[198:205], v[138:141], v187, v187 op_sel_hi:[0,0,0]
	v_mfma_scale_f32_16x16x128_f8f6f4 v[146:149], v[26:33], v[190:197], v[146:149], v187, v187 op_sel_hi:[0,0,0]
	s_setprio 0
	s_barrier
	s_add_i32 s36, s72, s43
	v_lshl_add_u64 v[172:173], v[172:173], 0, s[22:23]
	s_mov_b32 m0, s36
	ds_read_b128 v[190:193], v189 offset:49152
	ds_read_b128 v[194:197], v189 offset:50176
	ds_read_b128 v[198:201], v189 offset:51200
	ds_read_b128 v[202:205], v189 offset:52224
	ds_read_b128 v[206:209], v189 offset:53248
	ds_read_b128 v[210:213], v189 offset:54272
	ds_read_b128 v[214:217], v189 offset:55296
	ds_read_b128 v[218:221], v189 offset:56320
	global_load_lds_dwordx4 v[172:173], off
	s_add_i32 m0, s36, 0x2000
	s_add_u32 s8, s8, 0x158080
	v_lshl_add_u64 v[172:173], v[174:175], 0, s[22:23]
	s_addc_u32 s9, s9, 0
	s_add_i32 s36, s73, s43
	global_load_lds_dwordx4 v[172:173], off
	v_lshl_add_u64 v[172:173], s[8:9], 0, v[162:163]
	s_mov_b32 m0, s36
	s_nop 0
	global_load_lds_dwordx4 v[172:173], off
	v_lshl_add_u64 v[172:173], s[8:9], 0, v[166:167]
	s_add_i32 m0, s36, 0x2000
	s_nop 0
	global_load_lds_dwordx4 v[172:173], off
	v_lshl_add_u64 v[172:173], v[176:177], 0, s[22:23]
	s_mov_b32 m0, s69
	s_nop 0
	global_load_lds_dwordx4 v[172:173], off
	v_lshl_add_u64 v[172:173], v[178:179], 0, s[22:23]
	s_mov_b32 m0, s70
	s_nop 0
	global_load_lds_dwordx4 v[172:173], off
	s_waitcnt vmcnt(8)
	s_waitcnt lgkmcnt(0)
	s_barrier
	s_setprio 1
	s_waitcnt lgkmcnt(0)
	v_mfma_scale_f32_16x16x128_f8f6f4 v[94:97], v[2:9], v[190:197], v[94:97], v187, v187 op_sel_hi:[0,0,0]
	v_mfma_scale_f32_16x16x128_f8f6f4 v[78:81], v[2:9], v[198:205], v[78:81], v187, v187 op_sel_hi:[0,0,0]
	v_mfma_scale_f32_16x16x128_f8f6f4 v[62:65], v[2:9], v[206:213], v[62:65], v187, v187 op_sel_hi:[0,0,0]
	v_mfma_scale_f32_16x16x128_f8f6f4 v[46:49], v[2:9], v[214:221], v[46:49], v187, v187 op_sel_hi:[0,0,0]
	v_mfma_scale_f32_16x16x128_f8f6f4 v[42:45], v[10:17], v[214:221], v[42:45], v187, v187 op_sel_hi:[0,0,0]
	v_mfma_scale_f32_16x16x128_f8f6f4 v[58:61], v[10:17], v[206:213], v[58:61], v187, v187 op_sel_hi:[0,0,0]
	v_mfma_scale_f32_16x16x128_f8f6f4 v[74:77], v[10:17], v[198:205], v[74:77], v187, v187 op_sel_hi:[0,0,0]
	v_mfma_scale_f32_16x16x128_f8f6f4 v[90:93], v[10:17], v[190:197], v[90:93], v187, v187 op_sel_hi:[0,0,0]
	s_setprio 0
	s_setprio 1
	v_mfma_scale_f32_16x16x128_f8f6f4 v[86:89], v[18:25], v[190:197], v[86:89], v187, v187 op_sel_hi:[0,0,0]
	v_mfma_scale_f32_16x16x128_f8f6f4 v[70:73], v[18:25], v[198:205], v[70:73], v187, v187 op_sel_hi:[0,0,0]
	v_mfma_scale_f32_16x16x128_f8f6f4 v[54:57], v[18:25], v[206:213], v[54:57], v187, v187 op_sel_hi:[0,0,0]
	v_mfma_scale_f32_16x16x128_f8f6f4 v[38:41], v[18:25], v[214:221], v[38:41], v187, v187 op_sel_hi:[0,0,0]
	v_mfma_scale_f32_16x16x128_f8f6f4 v[34:37], v[26:33], v[214:221], v[34:37], v187, v187 op_sel_hi:[0,0,0]
	v_mfma_scale_f32_16x16x128_f8f6f4 v[50:53], v[26:33], v[206:213], v[50:53], v187, v187 op_sel_hi:[0,0,0]
	v_mfma_scale_f32_16x16x128_f8f6f4 v[66:69], v[26:33], v[198:205], v[66:69], v187, v187 op_sel_hi:[0,0,0]
	v_mfma_scale_f32_16x16x128_f8f6f4 v[82:85], v[26:33], v[190:197], v[82:85], v187, v187 op_sel_hi:[0,0,0]
	s_setprio 0
	s_barrier
	s_add_i32 s71, s71, 2
	s_add_u32 s6, s6, 0x100
	s_addc_u32 s7, s7, 0
	s_cmpk_lt_u32 s71, 0x54
	s_cbranch_scc1 .LBB0_1745
	s_waitcnt vmcnt(0)
	s_cmpk_gt_u32 s40, 0xff
	s_cbranch_scc1 .LBB0_1748
	s_barrier

.LBB0_1807:
	ds_read_b128 v[26:29], v185
	ds_read_b128 v[30:33], v185 offset:1024
	ds_read_b128 v[18:21], v185 offset:2048
	ds_read_b128 v[22:25], v185 offset:3072
	ds_read_b128 v[10:13], v186
	ds_read_b128 v[14:17], v186 offset:1024
	ds_read_b128 v[2:5], v186 offset:2048
	ds_read_b128 v[6:9], v186 offset:3072
	s_add_u32 s28, s26, 0xffea8080
	s_addc_u32 s29, s27, -1
	s_cmpk_eq_i32 s58, 0x52
	s_cselect_b32 s31, s5, s29
	s_cselect_b32 s30, s4, s28
	s_cselect_b32 s29, s25, s57
	s_cselect_b32 s28, s24, s56
	v_lshl_add_u64 v[212:213], s[26:27], 0, v[166:167]
	s_add_i32 m0, s34, 0xc000
	ds_read_b128 v[174:177], v187
	ds_read_b128 v[178:181], v187 offset:1024
	ds_read_b128 v[188:191], v187 offset:2048
	ds_read_b128 v[192:195], v187 offset:3072
	ds_read_b128 v[196:199], v187 offset:4096
	ds_read_b128 v[200:203], v187 offset:5120
	ds_read_b128 v[204:207], v187 offset:6144
	ds_read_b128 v[208:211], v187 offset:7168
	global_load_lds_dwordx4 v[212:213], off
	v_lshl_add_u64 v[212:213], s[26:27], 0, v[168:169]
	s_add_i32 m0, s34, 0xe000
	s_nop 0
	global_load_lds_dwordx4 v[212:213], off
	s_waitcnt vmcnt(8)
	s_waitcnt lgkmcnt(0)
	s_barrier
	s_setprio 1
	s_waitcnt lgkmcnt(0)
	v_mfma_scale_f32_16x16x128_f8f6f4 v[158:161], v[26:33], v[174:181], v[158:161], v1, v1 op_sel_hi:[0,0,0]
	v_mfma_scale_f32_16x16x128_f8f6f4 v[142:145], v[26:33], v[188:195], v[142:145], v1, v1 op_sel_hi:[0,0,0]
	v_mfma_scale_f32_16x16x128_f8f6f4 v[126:129], v[26:33], v[196:203], v[126:129], v1, v1 op_sel_hi:[0,0,0]
	v_mfma_scale_f32_16x16x128_f8f6f4 v[110:113], v[26:33], v[204:211], v[110:113], v1, v1 op_sel_hi:[0,0,0]
	v_mfma_scale_f32_16x16x128_f8f6f4 v[106:109], v[18:25], v[204:211], v[106:109], v1, v1 op_sel_hi:[0,0,0]
	v_mfma_scale_f32_16x16x128_f8f6f4 v[122:125], v[18:25], v[196:203], v[122:125], v1, v1 op_sel_hi:[0,0,0]
	v_mfma_scale_f32_16x16x128_f8f6f4 v[138:141], v[18:25], v[188:195], v[138:141], v1, v1 op_sel_hi:[0,0,0]
	v_mfma_scale_f32_16x16x128_f8f6f4 v[154:157], v[18:25], v[174:181], v[154:157], v1, v1 op_sel_hi:[0,0,0]
	s_setprio 0
	s_setprio 1
	v_mfma_scale_f32_16x16x128_f8f6f4 v[150:153], v[10:17], v[174:181], v[150:153], v1, v1 op_sel_hi:[0,0,0]
	v_mfma_scale_f32_16x16x128_f8f6f4 v[134:137], v[10:17], v[188:195], v[134:137], v1, v1 op_sel_hi:[0,0,0]
	v_mfma_scale_f32_16x16x128_f8f6f4 v[118:121], v[10:17], v[196:203], v[118:121], v1, v1 op_sel_hi:[0,0,0]
	v_mfma_scale_f32_16x16x128_f8f6f4 v[102:105], v[10:17], v[204:211], v[102:105], v1, v1 op_sel_hi:[0,0,0]
	v_mfma_scale_f32_16x16x128_f8f6f4 v[98:101], v[2:9], v[204:211], v[98:101], v1, v1 op_sel_hi:[0,0,0]
	v_mfma_scale_f32_16x16x128_f8f6f4 v[114:117], v[2:9], v[196:203], v[114:117], v1, v1 op_sel_hi:[0,0,0]
	v_mfma_scale_f32_16x16x128_f8f6f4 v[130:133], v[2:9], v[188:195], v[130:133], v1, v1 op_sel_hi:[0,0,0]
	v_mfma_scale_f32_16x16x128_f8f6f4 v[146:149], v[2:9], v[174:181], v[146:149], v1, v1 op_sel_hi:[0,0,0]
	s_setprio 0
	s_barrier
	s_add_i32 s59, s42, s3
	v_lshl_add_u64 v[174:175], s[28:29], 0, v[164:165]
	s_mov_b32 m0, s59
	ds_read_b128 v[188:191], v187 offset:16384
	ds_read_b128 v[192:195], v187 offset:17408
	ds_read_b128 v[196:199], v187 offset:18432
	ds_read_b128 v[200:203], v187 offset:19456
	ds_read_b128 v[204:207], v187 offset:20480
	ds_read_b128 v[208:211], v187 offset:21504
	ds_read_b128 v[212:215], v187 offset:22528
	ds_read_b128 v[216:219], v187 offset:23552
	global_load_lds_dwordx4 v[174:175], off
	s_add_i32 m0, s59, 0x2000
	s_add_u32 s60, s28, 0x158000
	v_lshl_add_u64 v[176:177], s[28:29], 0, v[162:163]
	s_addc_u32 s61, s29, 0
	s_add_i32 s59, s43, s3
	global_load_lds_dwordx4 v[176:177], off
	v_lshl_add_u64 v[178:179], s[60:61], 0, v[164:165]
	s_mov_b32 m0, s59
	v_lshl_add_u64 v[180:181], s[30:31], 0, v[162:163]
	global_load_lds_dwordx4 v[178:179], off
	v_lshl_add_u64 v[178:179], s[60:61], 0, v[162:163]
	s_add_i32 m0, s59, 0x2000
	s_nop 0
	global_load_lds_dwordx4 v[178:179], off
	v_lshl_add_u64 v[178:179], s[30:31], 0, v[164:165]
	s_mov_b32 m0, s34
	s_nop 0
	global_load_lds_dwordx4 v[178:179], off
	s_mov_b32 m0, s35
	s_nop 0
	global_load_lds_dwordx4 v[180:181], off
	s_waitcnt vmcnt(8)
	s_waitcnt lgkmcnt(0)
	s_barrier
	s_setprio 1
	s_waitcnt lgkmcnt(0)
	v_mfma_scale_f32_16x16x128_f8f6f4 v[94:97], v[26:33], v[188:195], v[94:97], v1, v1 op_sel_hi:[0,0,0]
	v_mfma_scale_f32_16x16x128_f8f6f4 v[78:81], v[26:33], v[196:203], v[78:81], v1, v1 op_sel_hi:[0,0,0]
	v_mfma_scale_f32_16x16x128_f8f6f4 v[62:65], v[26:33], v[204:211], v[62:65], v1, v1 op_sel_hi:[0,0,0]
	v_mfma_scale_f32_16x16x128_f8f6f4 v[54:57], v[26:33], v[212:219], v[54:57], v1, v1 op_sel_hi:[0,0,0]
	v_mfma_scale_f32_16x16x128_f8f6f4 v[42:45], v[18:25], v[212:219], v[42:45], v1, v1 op_sel_hi:[0,0,0]
	v_mfma_scale_f32_16x16x128_f8f6f4 v[58:61], v[18:25], v[204:211], v[58:61], v1, v1 op_sel_hi:[0,0,0]
	v_mfma_scale_f32_16x16x128_f8f6f4 v[74:77], v[18:25], v[196:203], v[74:77], v1, v1 op_sel_hi:[0,0,0]
	v_mfma_scale_f32_16x16x128_f8f6f4 v[90:93], v[18:25], v[188:195], v[90:93], v1, v1 op_sel_hi:[0,0,0]
	s_setprio 0
	s_setprio 1
	v_mfma_scale_f32_16x16x128_f8f6f4 v[86:89], v[10:17], v[188:195], v[86:89], v1, v1 op_sel_hi:[0,0,0]
	v_mfma_scale_f32_16x16x128_f8f6f4 v[70:73], v[10:17], v[196:203], v[70:73], v1, v1 op_sel_hi:[0,0,0]
	v_mfma_scale_f32_16x16x128_f8f6f4 v[50:53], v[10:17], v[204:211], v[50:53], v1, v1 op_sel_hi:[0,0,0]
	v_mfma_scale_f32_16x16x128_f8f6f4 v[38:41], v[10:17], v[212:219], v[38:41], v1, v1 op_sel_hi:[0,0,0]
	v_mfma_scale_f32_16x16x128_f8f6f4 v[34:37], v[2:9], v[212:219], v[34:37], v1, v1 op_sel_hi:[0,0,0]
	v_mfma_scale_f32_16x16x128_f8f6f4 v[46:49], v[2:9], v[204:211], v[46:49], v1, v1 op_sel_hi:[0,0,0]
	v_mfma_scale_f32_16x16x128_f8f6f4 v[66:69], v[2:9], v[196:203], v[66:69], v1, v1 op_sel_hi:[0,0,0]
	v_mfma_scale_f32_16x16x128_f8f6f4 v[82:85], v[2:9], v[188:195], v[82:85], v1, v1 op_sel_hi:[0,0,0]
	s_setprio 0
	s_barrier
	s_add_i32 s59, 0, 0x18000
	s_add_i32 s60, 0, 0x1c000
	v_add_u32_e32 v14, s59, v183
	v_add_u32_e32 v30, s60, v183
	ds_read_b128 v[2:5], v14
	ds_read_b128 v[6:9], v14 offset:1024
	ds_read_b128 v[10:13], v14 offset:2048
	ds_read_b128 v[14:17], v14 offset:3072
	ds_read_b128 v[18:21], v30
	ds_read_b128 v[22:25], v30 offset:1024
	ds_read_b128 v[26:29], v30 offset:2048
	ds_read_b128 v[30:33], v30 offset:3072
	s_add_u32 s30, s30, 0x158000
	s_addc_u32 s31, s31, 0
	s_mov_b32 m0, s36
	v_lshl_add_u64 v[220:221], s[30:31], 0, v[164:165]
	ds_read_b128 v[188:191], v187 offset:32768
	ds_read_b128 v[192:195], v187 offset:33792
	ds_read_b128 v[196:199], v187 offset:34816
	ds_read_b128 v[200:203], v187 offset:35840
	ds_read_b128 v[204:207], v187 offset:36864
	ds_read_b128 v[208:211], v187 offset:37888
	ds_read_b128 v[212:215], v187 offset:38912
	ds_read_b128 v[216:219], v187 offset:39936
	global_load_lds_dwordx4 v[220:221], off
	v_lshl_add_u64 v[220:221], s[30:31], 0, v[162:163]
	s_mov_b32 m0, s37
	s_nop 0
	global_load_lds_dwordx4 v[220:221], off
	s_waitcnt vmcnt(8)
	s_waitcnt lgkmcnt(0)
	s_barrier
	s_setprio 1
	s_waitcnt lgkmcnt(0)
	v_mfma_scale_f32_16x16x128_f8f6f4 v[158:161], v[2:9], v[188:195], v[158:161], v1, v1 op_sel_hi:[0,0,0]
	v_mfma_scale_f32_16x16x128_f8f6f4 v[142:145], v[2:9], v[196:203], v[142:145], v1, v1 op_sel_hi:[0,0,0]
	v_mfma_scale_f32_16x16x128_f8f6f4 v[126:129], v[2:9], v[204:211], v[126:129], v1, v1 op_sel_hi:[0,0,0]
	v_mfma_scale_f32_16x16x128_f8f6f4 v[110:113], v[2:9], v[212:219], v[110:113], v1, v1 op_sel_hi:[0,0,0]
	v_mfma_scale_f32_16x16x128_f8f6f4 v[106:109], v[10:17], v[212:219], v[106:109], v1, v1 op_sel_hi:[0,0,0]
	v_mfma_scale_f32_16x16x128_f8f6f4 v[122:125], v[10:17], v[204:211], v[122:125], v1, v1 op_sel_hi:[0,0,0]
	v_mfma_scale_f32_16x16x128_f8f6f4 v[138:141], v[10:17], v[196:203], v[138:141], v1, v1 op_sel_hi:[0,0,0]
	v_mfma_scale_f32_16x16x128_f8f6f4 v[154:157], v[10:17], v[188:195], v[154:157], v1, v1 op_sel_hi:[0,0,0]
	s_setprio 0
	s_setprio 1
	v_mfma_scale_f32_16x16x128_f8f6f4 v[150:153], v[18:25], v[188:195], v[150:153], v1, v1 op_sel_hi:[0,0,0]
	v_mfma_scale_f32_16x16x128_f8f6f4 v[134:137], v[18:25], v[196:203], v[134:137], v1, v1 op_sel_hi:[0,0,0]
	v_mfma_scale_f32_16x16x128_f8f6f4 v[118:121], v[18:25], v[204:211], v[118:121], v1, v1 op_sel_hi:[0,0,0]
	v_mfma_scale_f32_16x16x128_f8f6f4 v[102:105], v[18:25], v[212:219], v[102:105], v1, v1 op_sel_hi:[0,0,0]
	v_mfma_scale_f32_16x16x128_f8f6f4 v[98:101], v[26:33], v[212:219], v[98:101], v1, v1 op_sel_hi:[0,0,0]
	v_mfma_scale_f32_16x16x128_f8f6f4 v[114:117], v[26:33], v[204:211], v[114:117], v1, v1 op_sel_hi:[0,0,0]
	v_mfma_scale_f32_16x16x128_f8f6f4 v[130:133], v[26:33], v[196:203], v[130:133], v1, v1 op_sel_hi:[0,0,0]
	v_mfma_scale_f32_16x16x128_f8f6f4 v[146:149], v[26:33], v[188:195], v[146:149], v1, v1 op_sel_hi:[0,0,0]
	s_setprio 0
	s_barrier
	s_add_i32 s30, s59, s3
	v_lshl_add_u64 v[174:175], v[174:175], 0, s[10:11]
	s_mov_b32 m0, s30
	ds_read_b128 v[188:191], v187 offset:49152
	ds_read_b128 v[192:195], v187 offset:50176
	ds_read_b128 v[196:199], v187 offset:51200
	ds_read_b128 v[200:203], v187 offset:52224
	ds_read_b128 v[204:207], v187 offset:53248
	ds_read_b128 v[208:211], v187 offset:54272
	ds_read_b128 v[212:215], v187 offset:55296
	ds_read_b128 v[216:219], v187 offset:56320
	global_load_lds_dwordx4 v[174:175], off
	s_add_i32 m0, s30, 0x2000
	s_add_u32 s28, s28, 0x158080
	v_lshl_add_u64 v[174:175], v[176:177], 0, s[10:11]
	s_addc_u32 s29, s29, 0
	s_add_i32 s30, s60, s3
	global_load_lds_dwordx4 v[174:175], off
	v_lshl_add_u64 v[174:175], s[28:29], 0, v[164:165]
	s_mov_b32 m0, s30
	s_nop 0
	global_load_lds_dwordx4 v[174:175], off
	v_lshl_add_u64 v[174:175], s[28:29], 0, v[162:163]
	s_add_i32 m0, s30, 0x2000
	s_nop 0
	global_load_lds_dwordx4 v[174:175], off
	v_lshl_add_u64 v[174:175], v[178:179], 0, s[10:11]
	s_mov_b32 m0, s40
	s_nop 0
	global_load_lds_dwordx4 v[174:175], off
	v_lshl_add_u64 v[174:175], v[180:181], 0, s[10:11]
	s_mov_b32 m0, s41
	s_nop 0
	global_load_lds_dwordx4 v[174:175], off
	s_waitcnt vmcnt(8)
	s_waitcnt lgkmcnt(0)
	s_barrier
	s_setprio 1
	s_waitcnt lgkmcnt(0)
	v_mfma_scale_f32_16x16x128_f8f6f4 v[94:97], v[2:9], v[188:195], v[94:97], v1, v1 op_sel_hi:[0,0,0]
	v_mfma_scale_f32_16x16x128_f8f6f4 v[78:81], v[2:9], v[196:203], v[78:81], v1, v1 op_sel_hi:[0,0,0]
	v_mfma_scale_f32_16x16x128_f8f6f4 v[62:65], v[2:9], v[204:211], v[62:65], v1, v1 op_sel_hi:[0,0,0]
	v_mfma_scale_f32_16x16x128_f8f6f4 v[54:57], v[2:9], v[212:219], v[54:57], v1, v1 op_sel_hi:[0,0,0]
	v_mfma_scale_f32_16x16x128_f8f6f4 v[42:45], v[10:17], v[212:219], v[42:45], v1, v1 op_sel_hi:[0,0,0]
	v_mfma_scale_f32_16x16x128_f8f6f4 v[58:61], v[10:17], v[204:211], v[58:61], v1, v1 op_sel_hi:[0,0,0]
	v_mfma_scale_f32_16x16x128_f8f6f4 v[74:77], v[10:17], v[196:203], v[74:77], v1, v1 op_sel_hi:[0,0,0]
	v_mfma_scale_f32_16x16x128_f8f6f4 v[90:93], v[10:17], v[188:195], v[90:93], v1, v1 op_sel_hi:[0,0,0]
	s_setprio 0
	s_setprio 1
	v_mfma_scale_f32_16x16x128_f8f6f4 v[86:89], v[18:25], v[188:195], v[86:89], v1, v1 op_sel_hi:[0,0,0]
	v_mfma_scale_f32_16x16x128_f8f6f4 v[70:73], v[18:25], v[196:203], v[70:73], v1, v1 op_sel_hi:[0,0,0]
	v_mfma_scale_f32_16x16x128_f8f6f4 v[50:53], v[18:25], v[204:211], v[50:53], v1, v1 op_sel_hi:[0,0,0]
	v_mfma_scale_f32_16x16x128_f8f6f4 v[38:41], v[18:25], v[212:219], v[38:41], v1, v1 op_sel_hi:[0,0,0]
	v_mfma_scale_f32_16x16x128_f8f6f4 v[34:37], v[26:33], v[212:219], v[34:37], v1, v1 op_sel_hi:[0,0,0]
	v_mfma_scale_f32_16x16x128_f8f6f4 v[46:49], v[26:33], v[204:211], v[46:49], v1, v1 op_sel_hi:[0,0,0]
	v_mfma_scale_f32_16x16x128_f8f6f4 v[66:69], v[26:33], v[196:203], v[66:69], v1, v1 op_sel_hi:[0,0,0]
	v_mfma_scale_f32_16x16x128_f8f6f4 v[82:85], v[26:33], v[188:195], v[82:85], v1, v1 op_sel_hi:[0,0,0]
	s_setprio 0
	s_barrier
	s_add_i32 s58, s58, 2
	s_add_u32 s26, s26, 0x100
	s_addc_u32 s27, s27, 0
	s_add_u32 s56, s56, 0x100
	s_addc_u32 s57, s57, 0
	s_cmpk_gt_u32 s58, 0x53
	s_cbranch_scc0 .LBB0_1807
	s_and_b64 vcc, exec, s[12:13]
	s_cbranch_vccz .LBB0_1810
	s_barrier
